# speedup vs baseline: 1.0010x; 1.0010x over previous
.LBB0_2:
	s_or_b64 exec, exec, s[80:81]
	v_lshl_add_u32 v1, v206, 2, s22
	s_add_i32 s19, s19, 0x22200
	ds_write_b32 v1, v72
	v_lshl_or_b32 v1, v124, 3, s19
	v_lshl_add_u32 v187, v67, 2, s22
	s_movk_i32 s22, 0x110
	v_mad_u32_u24 v186, v67, s22, v1
	s_add_i32 s22, s7, 0x180
	v_and_b32_e32 v102, 15, v0
	s_lshl_b32 s27, s34, 8
	s_and_b32 s25, s22, 0x380
	s_add_i32 s22, s7, 0x280
	v_lshlrev_b32_e32 v66, 2, v124
	v_mul_u32_u24_e32 v1, 0x110, v102
	v_and_b32_e32 v209, 48, v0
	s_and_b32 s23, s22, 0x380
	s_add_i32 s22, s7, 0x300
	v_mov_b32_e32 v67, 0x200
	s_addk_i32 s27, 0x380
	v_or_b32_e32 v133, s7, v66
	v_add3_u32 v1, s19, v1, v209
	s_lshl_b32 s19, s35, 15
	v_lshlrev_b32_e32 v210, 4, v206
	v_or_b32_e32 v189, s24, v66
	s_xor_b32 s24, s7, 0x200
	s_and_b32 s22, s22, 0x300
	v_bitop3_b32 v197, s7, v66, v67 bitop3:0xde
	s_and_b32 s7, s27, 0x380
	v_lshrrev_b32_e32 v185, 4, v206
	s_ashr_i32 s11, s10, 31
	v_or_b32_e32 v184, s19, v210
	v_or_b32_e32 v188, s26, v66
	v_or_b32_e32 v198, s25, v66
	v_or_b32_e32 v196, s23, v66
	v_or_b32_e32 v195, s22, v66
	v_or_b32_e32 v194, s7, v66
	v_mov_b32_e32 v102, v133
	v_and_b32_e32 v248, 2, v206
	v_cmp_ne_u32_e32 vcc, 0, v248
	v_mov_b32_e32 v249, 0x44444444
	v_mov_b32_e32 v250, 0xeeeeeeee
	s_nop 1
	v_cndmask_b32_e32 v223, v249, v250, vcc
	v_lshrrev_b32_e32 v248, 4, v206
	v_lshl_add_u32 v248, v248, 4, 1
	v_add_u32_e32 v249, 0, v248
	v_cvt_f32_u32_e32 v249, v249
	v_add_u32_e32 v250, 1, v248
	v_cvt_f32_u32_e32 v250, v250
	v_cvt_pk_bf16_f32 v232, v249, v250
	v_add_u32_e32 v249, 2, v248
	v_cvt_f32_u32_e32 v249, v249
	v_add_u32_e32 v250, 3, v248
	v_cvt_f32_u32_e32 v250, v250
	v_cvt_pk_bf16_f32 v233, v249, v250
	v_add_u32_e32 v249, 4, v248
	v_cvt_f32_u32_e32 v249, v249
	v_add_u32_e32 v250, 5, v248
	v_cvt_f32_u32_e32 v250, v250
	v_cvt_pk_bf16_f32 v234, v249, v250
	v_add_u32_e32 v249, 6, v248
	v_cvt_f32_u32_e32 v249, v249
	v_add_u32_e32 v250, 7, v248
	v_cvt_f32_u32_e32 v250, v250
	v_cvt_pk_bf16_f32 v235, v249, v250
	v_add_u32_e32 v249, 8, v248
	v_cvt_f32_u32_e32 v249, v249
	v_add_u32_e32 v250, 9, v248
	v_cvt_f32_u32_e32 v250, v250
	v_cvt_pk_bf16_f32 v236, v249, v250
	v_add_u32_e32 v249, 10, v248
	v_cvt_f32_u32_e32 v249, v249
	v_add_u32_e32 v250, 11, v248
	v_cvt_f32_u32_e32 v250, v250
	v_cvt_pk_bf16_f32 v237, v249, v250
	v_add_u32_e32 v249, 12, v248
	v_cvt_f32_u32_e32 v249, v249
	v_add_u32_e32 v250, 13, v248
	v_cvt_f32_u32_e32 v250, v250
	v_cvt_pk_bf16_f32 v238, v249, v250
	v_add_u32_e32 v249, 14, v248
	v_cvt_f32_u32_e32 v249, v249
	v_add_u32_e32 v250, 15, v248
	v_cvt_f32_u32_e32 v250, v250
	v_cvt_pk_bf16_f32 v239, v249, v250
	v_and_b32_e32 v248, 15, v206
	v_lshrrev_b32_e32 v249, 2, v248
	v_and_b32_e32 v250, 1, v248
	v_lshl_add_u32 v249, v249, 1, v250
	v_and_b32_e32 v250, 3, v249
	v_lshrrev_b32_e32 v251, 4, v206
	v_cmp_eq_u32_e32 vcc, v250, v251
	v_lshrrev_b32_e32 v249, 2, v249
	v_cmp_ne_u32_e64 s[78:79], 0, v249
	v_mov_b32_e32 v250, 0x3f80
	v_mov_b32_e32 v251, 0x3f800000
	s_nop 1
	v_cndmask_b32_e64 v250, v250, v251, s[78:79]
	v_cndmask_b32_e32 v252, 0, v250, vcc
	s_lshr_b32 s77, s19, 15
	s_mulk_i32 s77, 0x1100
	s_add_i32 s77, s77, 0x22200
	v_lshrrev_b32_e32 v248, 4, v206
	v_and_b32_e32 v249, 1, v248
	v_lshrrev_b32_e32 v250, 1, v248
	v_lshlrev_b32_e32 v249, 6, v249
	v_lshl_add_u32 v253, v250, 1, v249
	v_and_b32_e32 v248, 15, v206
	v_cmp_eq_u32_e64 s[78:79], 0, v248
	v_mov_b32_e32 v244, v252
	v_mov_b32_e32 v245, 0
	v_mov_b32_e32 v246, 0
	v_mov_b32_e32 v247, 0
	v_mov_b64_e32 v[240:241], 0
	v_mov_b64_e32 v[242:243], 0
	s_nop 1
	v_smfmac_f32_16x16x64_bf16 v[240:243], v[244:247], v[232:239], v223
	s_nop 15
	s_nop 3
	s_and_saveexec_b64 s[80:81], s[78:79]
	v_cvt_u32_f32_e32 v248, v240
	v_add_u32_e32 v248, -1, v248
	v_lshl_add_u32 v248, v248, 2, s77
	v_add_u32_e32 v249, 0, v253
	ds_write_b32 v248, v249
	v_cvt_u32_f32_e32 v248, v241
	v_add_u32_e32 v248, -1, v248
	v_lshl_add_u32 v248, v248, 2, s77
	v_add_u32_e32 v249, 32, v253
	ds_write_b32 v248, v249
	v_cvt_u32_f32_e32 v248, v242
	v_add_u32_e32 v248, -1, v248
	v_lshl_add_u32 v248, v248, 2, s77
	v_add_u32_e32 v249, 16, v253
	ds_write_b32 v248, v249
	v_cvt_u32_f32_e32 v248, v243
	v_add_u32_e32 v248, -1, v248
	v_lshl_add_u32 v248, v248, 2, s77
	v_add_u32_e32 v249, 48, v253
	ds_write_b32 v248, v249
	s_or_b64 exec, exec, s[80:81]
	v_mov_b32_e32 v244, 0
	v_mov_b32_e32 v245, v252
	v_mov_b32_e32 v246, 0
	v_mov_b32_e32 v247, 0
	v_mov_b64_e32 v[240:241], 0
	v_mov_b64_e32 v[242:243], 0
	s_nop 1
	v_smfmac_f32_16x16x64_bf16 v[240:243], v[244:247], v[232:239], v223
	s_nop 15
	s_nop 3
	s_and_saveexec_b64 s[80:81], s[78:79]
	v_cvt_u32_f32_e32 v248, v240
	v_add_u32_e32 v248, -1, v248
	v_lshl_add_u32 v248, v248, 2, s77
	v_add_u32_e32 v249, 4, v253
	ds_write_b32 v248, v249
	v_cvt_u32_f32_e32 v248, v241
	v_add_u32_e32 v248, -1, v248
	v_lshl_add_u32 v248, v248, 2, s77
	v_add_u32_e32 v249, 36, v253
	ds_write_b32 v248, v249
	v_cvt_u32_f32_e32 v248, v242
	v_add_u32_e32 v248, -1, v248
	v_lshl_add_u32 v248, v248, 2, s77
	v_add_u32_e32 v249, 20, v253
	ds_write_b32 v248, v249
	v_cvt_u32_f32_e32 v248, v243
	v_add_u32_e32 v248, -1, v248
	v_lshl_add_u32 v248, v248, 2, s77
	v_add_u32_e32 v249, 52, v253
	ds_write_b32 v248, v249
	s_or_b64 exec, exec, s[80:81]
	v_mov_b32_e32 v244, 0
	v_mov_b32_e32 v245, 0
	v_mov_b32_e32 v246, v252
	v_mov_b32_e32 v247, 0
	v_mov_b64_e32 v[240:241], 0
	v_mov_b64_e32 v[242:243], 0
	s_nop 1
	v_smfmac_f32_16x16x64_bf16 v[240:243], v[244:247], v[232:239], v223
	s_nop 15
	s_nop 3
	s_and_saveexec_b64 s[80:81], s[78:79]
	v_cvt_u32_f32_e32 v248, v240
	v_add_u32_e32 v248, -1, v248
	v_lshl_add_u32 v248, v248, 2, s77
	v_add_u32_e32 v249, 8, v253
	ds_write_b32 v248, v249
	v_cvt_u32_f32_e32 v248, v241
	v_add_u32_e32 v248, -1, v248
	v_lshl_add_u32 v248, v248, 2, s77
	v_add_u32_e32 v249, 40, v253
	ds_write_b32 v248, v249
	v_cvt_u32_f32_e32 v248, v242
	v_add_u32_e32 v248, -1, v248
	v_lshl_add_u32 v248, v248, 2, s77
	v_add_u32_e32 v249, 24, v253
	ds_write_b32 v248, v249
	v_cvt_u32_f32_e32 v248, v243
	v_add_u32_e32 v248, -1, v248
	v_lshl_add_u32 v248, v248, 2, s77
	v_add_u32_e32 v249, 56, v253
	ds_write_b32 v248, v249
	s_or_b64 exec, exec, s[80:81]
	v_mov_b32_e32 v244, 0
	v_mov_b32_e32 v245, 0
	v_mov_b32_e32 v246, 0
	v_mov_b32_e32 v247, v252
	v_mov_b64_e32 v[240:241], 0
	v_mov_b64_e32 v[242:243], 0
	s_nop 1
	v_smfmac_f32_16x16x64_bf16 v[240:243], v[244:247], v[232:239], v223
	s_nop 15
	s_nop 3
	s_and_saveexec_b64 s[80:81], s[78:79]
	v_cvt_u32_f32_e32 v248, v240
	v_add_u32_e32 v248, -1, v248
	v_lshl_add_u32 v248, v248, 2, s77
	v_add_u32_e32 v249, 12, v253
	ds_write_b32 v248, v249
	v_cvt_u32_f32_e32 v248, v241
	v_add_u32_e32 v248, -1, v248
	v_lshl_add_u32 v248, v248, 2, s77
	v_add_u32_e32 v249, 44, v253
	ds_write_b32 v248, v249
	v_cvt_u32_f32_e32 v248, v242
	v_add_u32_e32 v248, -1, v248
	v_lshl_add_u32 v248, v248, 2, s77
	v_add_u32_e32 v249, 28, v253
	ds_write_b32 v248, v249
	v_cvt_u32_f32_e32 v248, v243
	v_add_u32_e32 v248, -1, v248
	v_lshl_add_u32 v248, v248, 2, s77
	v_add_u32_e32 v249, 60, v253
	ds_write_b32 v248, v249
	s_or_b64 exec, exec, s[80:81]
	v_bfe_u32 v248, v206, 3, 2
	v_lshrrev_b32_e32 v249, 5, v206
	v_lshlrev_b32_e32 v248, 4, v248
	v_lshl_or_b32 v248, v249, 3, v248
	v_and_b32_e32 v249, 7, v206
	v_or_b32_e32 v248, v248, v249
	v_lshl_add_u32 v248, v248, 2, s77
	s_waitcnt lgkmcnt(0)
	ds_read_b32 v254, v248
	v_and_b32_e32 v248, 15, v206
	v_bfe_u32 v249, v248, 1, 2
	v_lshrrev_b32_e32 v250, 3, v248
	v_lshlrev_b32_e32 v249, 4, v249
	v_lshl_or_b32 v249, v250, 3, v249
	v_and_b32_e32 v250, 1, v248
	v_lshl_or_b32 v249, v250, 2, v249
	v_lshl_add_u32 v249, v249, 2, s77
	ds_read_b128 v[248:251], v249
	s_lshr_b32 s76, s19, 6
	s_add_i32 s76, s76, 0x20000
	v_lshrrev_b32_e32 v252, 4, v206
	v_lshl_add_u32 v252, v252, 7, s76
	s_waitcnt lgkmcnt(0)
	v_add_u32_e32 v248, v252, v248
	v_add_u32_e32 v249, v252, v249
	v_add_u32_e32 v250, v252, v250
	v_add_u32_e32 v251, v252, v251
	v_cvt_pk_bf16_f32 v236, v224, v225
	v_cvt_pk_bf16_f32 v237, v226, v227
	v_lshlrev_b32_e32 v238, 16, v236
	v_and_b32_e32 v239, 0xffff0000, v236
	v_lshlrev_b32_e32 v240, 16, v237
	v_and_b32_e32 v241, 0xffff0000, v237
	v_sub_f32_e32 v238, v224, v238
	v_sub_f32_e32 v239, v225, v239
	v_sub_f32_e32 v240, v226, v240
	v_sub_f32_e32 v241, v227, v241
	v_cvt_pk_bf16_f32 v238, v238, v239
	v_cvt_pk_bf16_f32 v239, v240, v241
	ds_write_b16 v248, v236
	ds_write_b16_d16_hi v249, v236
	ds_write_b16 v250, v237
	ds_write_b16_d16_hi v251, v237
	ds_write_b16 v248, v238 offset:2176
	ds_write_b16_d16_hi v249, v238 offset:2176
	ds_write_b16 v250, v239 offset:2176
	ds_write_b16_d16_hi v251, v239 offset:2176
	ds_read_b32 v232, v187 offset:192
	ds_read_b32 v234, v187 offset:200
	ds_read_b32 v236, v187 offset:208
	ds_read_b32 v238, v187 offset:216
	ds_read_b32 v240, v187 offset:224
	ds_read_b32 v242, v187 offset:232
	ds_read_b32 v244, v187 offset:240
	ds_read_b32 v246, v187 offset:248
	v_or_b32_e32 v103, 48, v132
	v_add_u32_e32 v104, 1, v102
	v_cmp_eq_u32_e32 vcc, v102, v103
	v_add_u32_e32 v105, 3, v102
	v_add_u32_e32 v106, 2, v102
	v_cndmask_b32_e64 v72, 0, 1.0, vcc
	v_cmp_eq_u32_e32 vcc, v104, v103
	v_or_b32_e32 v107, 50, v132
	v_or_b32_e32 v108, 52, v132
	v_cndmask_b32_e64 v73, 0, 1.0, vcc
	v_cmp_eq_u32_e32 vcc, v105, v103
	s_waitcnt lgkmcnt(0)
	s_waitcnt vmcnt(23)
	v_pk_fma_f32 v[68:69], v[232:233], v[68:69], v[72:73] op_sel_hi:[0,1,1] neg_lo:[1,0,0] neg_hi:[1,0,0]
	v_cvt_pk_bf16_f32 v68, v68, v69
	v_cndmask_b32_e64 v73, 0, 1.0, vcc
	v_cmp_eq_u32_e32 vcc, v106, v103
	v_or_b32_e32 v109, 54, v132
	v_or_b32_e32 v110, 56, v132
	v_cndmask_b32_e64 v72, 0, 1.0, vcc
	v_pk_fma_f32 v[66:67], v[232:233], v[70:71], v[72:73] op_sel_hi:[0,1,1] neg_lo:[1,0,0] neg_hi:[1,0,0]
	v_cvt_pk_bf16_f32 v69, v66, v67
	ds_write_b64 v186, v[68:69]
	v_cmp_eq_u32_e32 vcc, v102, v107
	v_or_b32_e32 v111, 58, v132
	v_or_b32_e32 v112, 60, v132
	v_cndmask_b32_e64 v68, 0, 1.0, vcc
	v_cmp_eq_u32_e32 vcc, v104, v107
	v_or_b32_e32 v113, 62, v132
	v_or_b32_e32 v193, 2, v132
	v_cndmask_b32_e64 v69, 0, 1.0, vcc
	v_cmp_eq_u32_e32 vcc, v105, v107
	s_waitcnt vmcnt(22)
	v_pk_fma_f32 v[68:69], v[234:235], v[78:79], v[68:69] op_sel_hi:[0,1,1] neg_lo:[1,0,0] neg_hi:[1,0,0]
	v_cvt_pk_bf16_f32 v68, v68, v69
	v_cndmask_b32_e64 v71, 0, 1.0, vcc
	v_cmp_eq_u32_e32 vcc, v106, v107
	v_or_b32_e32 v192, 4, v132
	v_or_b32_e32 v190, 6, v132
	v_cndmask_b32_e64 v70, 0, 1.0, vcc
	v_pk_fma_f32 v[66:67], v[234:235], v[80:81], v[70:71] op_sel_hi:[0,1,1] neg_lo:[1,0,0] neg_hi:[1,0,0]
	v_cvt_pk_bf16_f32 v69, v66, v67
	ds_write_b64 v186, v[68:69] offset:544
	v_cmp_eq_u32_e32 vcc, v102, v108
	v_or_b32_e32 v149, 8, v132
	v_or_b32_e32 v148, 10, v132
	v_cndmask_b32_e64 v68, 0, 1.0, vcc
	v_cmp_eq_u32_e32 vcc, v104, v108
	v_or_b32_e32 v147, 12, v132
	v_or_b32_e32 v146, 14, v132
	v_cndmask_b32_e64 v69, 0, 1.0, vcc
	v_cmp_eq_u32_e32 vcc, v105, v108
	s_waitcnt vmcnt(21)
	v_pk_fma_f32 v[68:69], v[236:237], v[82:83], v[68:69] op_sel_hi:[0,1,1] neg_lo:[1,0,0] neg_hi:[1,0,0]
	v_cvt_pk_bf16_f32 v68, v68, v69
	v_cndmask_b32_e64 v71, 0, 1.0, vcc
	v_cmp_eq_u32_e32 vcc, v106, v108
	s_nop 1
	v_cndmask_b32_e64 v70, 0, 1.0, vcc
	v_pk_fma_f32 v[66:67], v[236:237], v[84:85], v[70:71] op_sel_hi:[0,1,1] neg_lo:[1,0,0] neg_hi:[1,0,0]
	v_cvt_pk_bf16_f32 v69, v66, v67
	ds_write_b64 v186, v[68:69] offset:1088
	v_cmp_eq_u32_e32 vcc, v102, v109
	s_nop 1
	v_cndmask_b32_e64 v68, 0, 1.0, vcc
	v_cmp_eq_u32_e32 vcc, v104, v109
	s_nop 1
	v_cndmask_b32_e64 v69, 0, 1.0, vcc
	v_cmp_eq_u32_e32 vcc, v105, v109
	s_waitcnt vmcnt(20)
	v_pk_fma_f32 v[68:69], v[238:239], v[90:91], v[68:69] op_sel_hi:[0,1,1] neg_lo:[1,0,0] neg_hi:[1,0,0]
	v_cvt_pk_bf16_f32 v68, v68, v69
	v_cndmask_b32_e64 v71, 0, 1.0, vcc
	v_cmp_eq_u32_e32 vcc, v106, v109
	s_nop 1
	v_cndmask_b32_e64 v70, 0, 1.0, vcc
	v_pk_fma_f32 v[66:67], v[238:239], v[92:93], v[70:71] op_sel_hi:[0,1,1] neg_lo:[1,0,0] neg_hi:[1,0,0]
	v_cvt_pk_bf16_f32 v69, v66, v67
	ds_write_b64 v186, v[68:69] offset:1632
	v_cmp_eq_u32_e32 vcc, v102, v110
	s_nop 1
	v_cndmask_b32_e64 v68, 0, 1.0, vcc
	v_cmp_eq_u32_e32 vcc, v104, v110
	s_nop 1
	v_cndmask_b32_e64 v69, 0, 1.0, vcc
	v_cmp_eq_u32_e32 vcc, v105, v110
	s_waitcnt vmcnt(19)
	v_pk_fma_f32 v[68:69], v[240:241], v[98:99], v[68:69] op_sel_hi:[0,1,1] neg_lo:[1,0,0] neg_hi:[1,0,0]
	v_cvt_pk_bf16_f32 v68, v68, v69
	v_cndmask_b32_e64 v71, 0, 1.0, vcc
	v_cmp_eq_u32_e32 vcc, v106, v110
	s_nop 1
	v_cndmask_b32_e64 v70, 0, 1.0, vcc
	v_pk_fma_f32 v[66:67], v[240:241], v[100:101], v[70:71] op_sel_hi:[0,1,1] neg_lo:[1,0,0] neg_hi:[1,0,0]
	v_cvt_pk_bf16_f32 v69, v66, v67
	ds_write_b64 v186, v[68:69] offset:2176
	v_cmp_eq_u32_e32 vcc, v102, v111
	s_nop 1
	v_cndmask_b32_e64 v68, 0, 1.0, vcc
	v_cmp_eq_u32_e32 vcc, v104, v111
	s_nop 1
	v_cndmask_b32_e64 v69, 0, 1.0, vcc
	v_cmp_eq_u32_e32 vcc, v105, v111
	s_waitcnt vmcnt(18)
	v_pk_fma_f32 v[62:63], v[242:243], v[62:63], v[68:69] op_sel_hi:[0,1,1] neg_lo:[1,0,0] neg_hi:[1,0,0]
	v_cvt_pk_bf16_f32 v62, v62, v63
	v_cndmask_b32_e64 v69, 0, 1.0, vcc
	v_cmp_eq_u32_e32 vcc, v106, v111
	s_nop 1
	v_cndmask_b32_e64 v68, 0, 1.0, vcc
	v_pk_fma_f32 v[64:65], v[242:243], v[64:65], v[68:69] op_sel_hi:[0,1,1] neg_lo:[1,0,0] neg_hi:[1,0,0]
	v_cvt_pk_bf16_f32 v63, v64, v65
	ds_write_b64 v186, v[62:63] offset:2720
	v_cmp_eq_u32_e32 vcc, v102, v112
	s_nop 1
	v_cndmask_b32_e64 v64, 0, 1.0, vcc
	v_cmp_eq_u32_e32 vcc, v104, v112
	s_nop 1
	v_cndmask_b32_e64 v65, 0, 1.0, vcc
	v_cmp_eq_u32_e32 vcc, v105, v112
	s_waitcnt vmcnt(17)
	v_pk_fma_f32 v[54:55], v[244:245], v[54:55], v[64:65] op_sel_hi:[0,1,1] neg_lo:[1,0,0] neg_hi:[1,0,0]
	v_cvt_pk_bf16_f32 v54, v54, v55
	v_cndmask_b32_e64 v65, 0, 1.0, vcc
	v_cmp_eq_u32_e32 vcc, v106, v112
	s_nop 1
	v_cndmask_b32_e64 v64, 0, 1.0, vcc
	v_pk_fma_f32 v[56:57], v[244:245], v[56:57], v[64:65] op_sel_hi:[0,1,1] neg_lo:[1,0,0] neg_hi:[1,0,0]
	v_cvt_pk_bf16_f32 v55, v56, v57
	ds_write_b64 v186, v[54:55] offset:3264
	v_cmp_eq_u32_e32 vcc, v102, v113
	s_nop 1
	v_cndmask_b32_e64 v56, 0, 1.0, vcc
	v_cmp_eq_u32_e32 vcc, v104, v113
	s_nop 1
	v_cndmask_b32_e64 v57, 0, 1.0, vcc
	v_cmp_eq_u32_e32 vcc, v105, v113
	s_waitcnt vmcnt(16)
	v_pk_fma_f32 v[46:47], v[246:247], v[46:47], v[56:57] op_sel_hi:[0,1,1] neg_lo:[1,0,0] neg_hi:[1,0,0]
	v_cvt_pk_bf16_f32 v46, v46, v47
	v_cndmask_b32_e64 v57, 0, 1.0, vcc
	v_cmp_eq_u32_e32 vcc, v106, v113
	s_nop 1
	v_cndmask_b32_e64 v56, 0, 1.0, vcc
	v_pk_fma_f32 v[48:49], v[246:247], v[48:49], v[56:57] op_sel_hi:[0,1,1] neg_lo:[1,0,0] neg_hi:[1,0,0]
	v_cvt_pk_bf16_f32 v47, v48, v49
	ds_write_b64 v186, v[46:47] offset:3808
	ds_read_b128 v[232:235], v1
	ds_read_b128 v[236:239], v1 offset:64
	ds_read_b128 v[240:243], v1 offset:128
	ds_read_b128 v[244:247], v1 offset:192
	s_waitcnt lgkmcnt(0)
	ds_write_b128 v184, v[232:235]
	ds_write_b128 v184, v[236:239] offset:1024
	ds_write_b128 v184, v[240:243] offset:2048
	ds_write_b128 v184, v[244:247] offset:3072
	ds_read_b32 v232, v187 offset:192
	ds_read_b32 v234, v187 offset:200
	ds_read_b32 v236, v187 offset:208
	ds_read_b32 v238, v187 offset:216
	ds_read_b32 v240, v187 offset:224
	ds_read_b32 v242, v187 offset:232
	ds_read_b32 v244, v187 offset:240
	ds_read_b32 v246, v187 offset:248
	s_lshl_b32 s30, s25, 2
	s_mov_b32 s31, s21
	v_lshl_add_u64 v[46:47], v[126:127], 0, s[30:31]
	v_lshl_add_u64 v[48:49], v[128:129], 0, s[30:31]
	v_lshl_add_u64 v[54:55], v[134:135], 0, s[30:31]
	v_lshl_add_u64 v[56:57], v[136:137], 0, s[30:31]
	v_lshl_add_u64 v[62:63], v[138:139], 0, s[30:31]
	v_lshl_add_u64 v[64:65], v[140:141], 0, s[30:31]
	v_lshl_add_u64 v[98:99], v[142:143], 0, s[30:31]
	v_lshl_add_u64 v[100:101], v[144:145], 0, s[30:31]
	global_load_dwordx4 v[90:93], v[46:47], off nt
	global_load_dwordx4 v[82:85], v[48:49], off nt
	global_load_dwordx4 v[78:81], v[54:55], off nt
	global_load_dwordx4 v[70:73], v[56:57], off nt
	global_load_dwordx4 v[66:69], v[62:63], off nt
	s_nop 0
	global_load_dwordx4 v[62:65], v[64:65], off nt
	s_nop 0
	global_load_dwordx4 v[54:57], v[98:99], off nt
	global_load_dwordx4 v[46:49], v[100:101], off nt
	v_mov_b32_e32 v99, v189
	v_add_u32_e32 v102, 1, v99
	v_cmp_eq_u32_e32 vcc, v99, v103
	v_add_u32_e32 v104, 3, v99
	v_add_u32_e32 v105, 2, v99
	v_cndmask_b32_e64 v100, 0, 1.0, vcc
	v_cmp_eq_u32_e32 vcc, v102, v103
	s_nop 1
	v_cndmask_b32_e64 v101, 0, 1.0, vcc
	v_cmp_eq_u32_e32 vcc, v104, v103
	s_waitcnt lgkmcnt(0)
	s_waitcnt vmcnt(23)
	v_pk_fma_f32 v[94:95], v[232:233], v[94:95], v[100:101] op_sel_hi:[0,1,1] neg_lo:[1,0,0] neg_hi:[1,0,0]
	v_cvt_pk_bf16_f32 v94, v94, v95
	v_cndmask_b32_e64 v101, 0, 1.0, vcc
	v_cmp_eq_u32_e32 vcc, v105, v103
	s_nop 1
	v_cndmask_b32_e64 v100, 0, 1.0, vcc
	v_pk_fma_f32 v[96:97], v[232:233], v[96:97], v[100:101] op_sel_hi:[0,1,1] neg_lo:[1,0,0] neg_hi:[1,0,0]
	v_cvt_pk_bf16_f32 v95, v96, v97
	ds_write_b64 v186, v[94:95]
	v_cmp_eq_u32_e32 vcc, v99, v107
	s_nop 1
	v_cndmask_b32_e64 v96, 0, 1.0, vcc
	v_cmp_eq_u32_e32 vcc, v102, v107
	s_nop 1
	v_cndmask_b32_e64 v97, 0, 1.0, vcc
	v_cmp_eq_u32_e32 vcc, v104, v107
	s_waitcnt vmcnt(22)
	v_pk_fma_f32 v[86:87], v[234:235], v[86:87], v[96:97] op_sel_hi:[0,1,1] neg_lo:[1,0,0] neg_hi:[1,0,0]
	v_cvt_pk_bf16_f32 v86, v86, v87
	v_cndmask_b32_e64 v97, 0, 1.0, vcc
	v_cmp_eq_u32_e32 vcc, v105, v107
	s_nop 1
	v_cndmask_b32_e64 v96, 0, 1.0, vcc
	v_pk_fma_f32 v[88:89], v[234:235], v[88:89], v[96:97] op_sel_hi:[0,1,1] neg_lo:[1,0,0] neg_hi:[1,0,0]
	v_cvt_pk_bf16_f32 v87, v88, v89
	ds_write_b64 v186, v[86:87] offset:544
	v_cmp_eq_u32_e32 vcc, v99, v108
	s_nop 1
	v_cndmask_b32_e64 v88, 0, 1.0, vcc
	v_cmp_eq_u32_e32 vcc, v102, v108
	s_nop 1
	v_cndmask_b32_e64 v89, 0, 1.0, vcc
	v_cmp_eq_u32_e32 vcc, v104, v108
	s_waitcnt vmcnt(21)
	v_pk_fma_f32 v[74:75], v[236:237], v[74:75], v[88:89] op_sel_hi:[0,1,1] neg_lo:[1,0,0] neg_hi:[1,0,0]
	v_cvt_pk_bf16_f32 v74, v74, v75
	v_cndmask_b32_e64 v89, 0, 1.0, vcc
	v_cmp_eq_u32_e32 vcc, v105, v108
	s_nop 1
	v_cndmask_b32_e64 v88, 0, 1.0, vcc
	v_pk_fma_f32 v[76:77], v[236:237], v[76:77], v[88:89] op_sel_hi:[0,1,1] neg_lo:[1,0,0] neg_hi:[1,0,0]
	v_cvt_pk_bf16_f32 v75, v76, v77
	ds_write_b64 v186, v[74:75] offset:1088
	v_cmp_eq_u32_e32 vcc, v99, v109
	s_nop 1
	v_cndmask_b32_e64 v76, 0, 1.0, vcc
	v_cmp_eq_u32_e32 vcc, v102, v109
	s_nop 1
	v_cndmask_b32_e64 v77, 0, 1.0, vcc
	v_cmp_eq_u32_e32 vcc, v104, v109
	s_waitcnt vmcnt(20)
	v_pk_fma_f32 v[58:59], v[238:239], v[58:59], v[76:77] op_sel_hi:[0,1,1] neg_lo:[1,0,0] neg_hi:[1,0,0]
	v_cvt_pk_bf16_f32 v58, v58, v59
	v_cndmask_b32_e64 v77, 0, 1.0, vcc
	v_cmp_eq_u32_e32 vcc, v105, v109
	s_nop 1
	v_cndmask_b32_e64 v76, 0, 1.0, vcc
	v_pk_fma_f32 v[60:61], v[238:239], v[60:61], v[76:77] op_sel_hi:[0,1,1] neg_lo:[1,0,0] neg_hi:[1,0,0]
	v_cvt_pk_bf16_f32 v59, v60, v61
	ds_write_b64 v186, v[58:59] offset:1632
	v_cmp_eq_u32_e32 vcc, v99, v110
	s_nop 1
	v_cndmask_b32_e64 v60, 0, 1.0, vcc
	v_cmp_eq_u32_e32 vcc, v102, v110
	s_nop 1
	v_cndmask_b32_e64 v61, 0, 1.0, vcc
	v_cmp_eq_u32_e32 vcc, v104, v110
	s_waitcnt vmcnt(19)
	v_pk_fma_f32 v[50:51], v[240:241], v[50:51], v[60:61] op_sel_hi:[0,1,1] neg_lo:[1,0,0] neg_hi:[1,0,0]
	v_cvt_pk_bf16_f32 v50, v50, v51
	v_cndmask_b32_e64 v61, 0, 1.0, vcc
	v_cmp_eq_u32_e32 vcc, v105, v110
	s_nop 1
	v_cndmask_b32_e64 v60, 0, 1.0, vcc
	v_pk_fma_f32 v[52:53], v[240:241], v[52:53], v[60:61] op_sel_hi:[0,1,1] neg_lo:[1,0,0] neg_hi:[1,0,0]
	v_cvt_pk_bf16_f32 v51, v52, v53
	ds_write_b64 v186, v[50:51] offset:2176
	v_cmp_eq_u32_e32 vcc, v99, v111
	s_nop 1
	v_cndmask_b32_e64 v52, 0, 1.0, vcc
	v_cmp_eq_u32_e32 vcc, v102, v111
	s_nop 1
	v_cndmask_b32_e64 v53, 0, 1.0, vcc
	v_cmp_eq_u32_e32 vcc, v104, v111
	s_waitcnt vmcnt(18)
	v_pk_fma_f32 v[42:43], v[242:243], v[42:43], v[52:53] op_sel_hi:[0,1,1] neg_lo:[1,0,0] neg_hi:[1,0,0]
	v_cvt_pk_bf16_f32 v42, v42, v43
	v_cndmask_b32_e64 v53, 0, 1.0, vcc
	v_cmp_eq_u32_e32 vcc, v105, v111
	s_nop 1
	v_cndmask_b32_e64 v52, 0, 1.0, vcc
	v_pk_fma_f32 v[44:45], v[242:243], v[44:45], v[52:53] op_sel_hi:[0,1,1] neg_lo:[1,0,0] neg_hi:[1,0,0]
	v_cvt_pk_bf16_f32 v43, v44, v45
	ds_write_b64 v186, v[42:43] offset:2720
	v_cmp_eq_u32_e32 vcc, v99, v112
	s_nop 1
	v_cndmask_b32_e64 v44, 0, 1.0, vcc
	v_cmp_eq_u32_e32 vcc, v102, v112
	s_nop 1
	v_cndmask_b32_e64 v45, 0, 1.0, vcc
	v_cmp_eq_u32_e32 vcc, v104, v112
	s_waitcnt vmcnt(17)
	v_pk_fma_f32 v[38:39], v[244:245], v[38:39], v[44:45] op_sel_hi:[0,1,1] neg_lo:[1,0,0] neg_hi:[1,0,0]
	v_cvt_pk_bf16_f32 v38, v38, v39
	v_cndmask_b32_e64 v45, 0, 1.0, vcc
	v_cmp_eq_u32_e32 vcc, v105, v112
	s_nop 1
	v_cndmask_b32_e64 v44, 0, 1.0, vcc
	v_pk_fma_f32 v[40:41], v[244:245], v[40:41], v[44:45] op_sel_hi:[0,1,1] neg_lo:[1,0,0] neg_hi:[1,0,0]
	v_cvt_pk_bf16_f32 v39, v40, v41
	ds_write_b64 v186, v[38:39] offset:3264
	v_cmp_eq_u32_e32 vcc, v99, v113
	s_nop 1
	v_cndmask_b32_e64 v40, 0, 1.0, vcc
	v_cmp_eq_u32_e32 vcc, v102, v113
	s_nop 1
	v_cndmask_b32_e64 v41, 0, 1.0, vcc
	v_cmp_eq_u32_e32 vcc, v104, v113
	s_waitcnt vmcnt(16)
	v_pk_fma_f32 v[34:35], v[246:247], v[34:35], v[40:41] op_sel_hi:[0,1,1] neg_lo:[1,0,0] neg_hi:[1,0,0]
	v_cvt_pk_bf16_f32 v34, v34, v35
	v_cndmask_b32_e64 v41, 0, 1.0, vcc
	v_cmp_eq_u32_e32 vcc, v105, v113
	s_nop 1
	v_cndmask_b32_e64 v40, 0, 1.0, vcc
	v_pk_fma_f32 v[36:37], v[246:247], v[36:37], v[40:41] op_sel_hi:[0,1,1] neg_lo:[1,0,0] neg_hi:[1,0,0]
	v_cvt_pk_bf16_f32 v35, v36, v37
	ds_write_b64 v186, v[34:35] offset:3808
	ds_read_b128 v[232:235], v1
	ds_read_b128 v[236:239], v1 offset:64
	ds_read_b128 v[240:243], v1 offset:128
	ds_read_b128 v[244:247], v1 offset:192
	s_waitcnt lgkmcnt(0)
	ds_write_b128 v184, v[232:235] offset:4096
	ds_write_b128 v184, v[236:239] offset:5120
	ds_write_b128 v184, v[240:243] offset:6144
	ds_write_b128 v184, v[244:247] offset:7168
	ds_read_b32 v232, v187 offset:192
	ds_read_b32 v234, v187 offset:200
	ds_read_b32 v236, v187 offset:208
	ds_read_b32 v238, v187 offset:216
	ds_read_b32 v240, v187 offset:224
	ds_read_b32 v242, v187 offset:232
	ds_read_b32 v244, v187 offset:240
	ds_read_b32 v246, v187 offset:248
	s_lshl_b32 s28, s24, 2
	s_mov_b32 s29, s21
	v_lshl_add_u64 v[34:35], v[126:127], 0, s[28:29]
	v_lshl_add_u64 v[36:37], v[128:129], 0, s[28:29]
	v_lshl_add_u64 v[38:39], v[134:135], 0, s[28:29]
	v_lshl_add_u64 v[40:41], v[136:137], 0, s[28:29]
	v_lshl_add_u64 v[42:43], v[138:139], 0, s[28:29]
	v_lshl_add_u64 v[44:45], v[140:141], 0, s[28:29]
	v_lshl_add_u64 v[50:51], v[142:143], 0, s[28:29]
	v_lshl_add_u64 v[52:53], v[144:145], 0, s[28:29]
	global_load_dwordx4 v[122:125], v[34:35], off nt
	global_load_dwordx4 v[114:117], v[36:37], off nt
	global_load_dwordx4 v[106:109], v[38:39], off nt
	global_load_dwordx4 v[86:89], v[40:41], off nt
	global_load_dwordx4 v[74:77], v[42:43], off nt
	s_nop 0
	global_load_dwordx4 v[42:45], v[44:45], off nt
	s_nop 0
	global_load_dwordx4 v[38:41], v[50:51], off nt
	global_load_dwordx4 v[34:37], v[52:53], off nt
	v_mov_b32_e32 v50, v188
	s_waitcnt lgkmcnt(0)
	s_waitcnt vmcnt(23)
	v_pk_fma_f32 v[30:31], v[232:233], v[30:31], 0 op_sel_hi:[0,1,0] neg_lo:[1,0,0] neg_hi:[1,0,0]
	v_pk_fma_f32 v[32:33], v[232:233], v[32:33], 0 op_sel_hi:[0,1,0] neg_lo:[1,0,0] neg_hi:[1,0,0]
	v_cvt_pk_bf16_f32 v30, v30, v31
	v_cvt_pk_bf16_f32 v31, v32, v33
	ds_write_b64 v186, v[30:31]
	s_waitcnt vmcnt(22)
	v_pk_fma_f32 v[26:27], v[234:235], v[26:27], 0 op_sel_hi:[0,1,0] neg_lo:[1,0,0] neg_hi:[1,0,0]
	v_pk_fma_f32 v[28:29], v[234:235], v[28:29], 0 op_sel_hi:[0,1,0] neg_lo:[1,0,0] neg_hi:[1,0,0]
	v_cvt_pk_bf16_f32 v26, v26, v27
	v_cvt_pk_bf16_f32 v27, v28, v29
	ds_write_b64 v186, v[26:27] offset:544
	s_waitcnt vmcnt(21)
	v_pk_fma_f32 v[22:23], v[236:237], v[22:23], 0 op_sel_hi:[0,1,0] neg_lo:[1,0,0] neg_hi:[1,0,0]
	v_pk_fma_f32 v[24:25], v[236:237], v[24:25], 0 op_sel_hi:[0,1,0] neg_lo:[1,0,0] neg_hi:[1,0,0]
	v_cvt_pk_bf16_f32 v22, v22, v23
	v_cvt_pk_bf16_f32 v23, v24, v25
	ds_write_b64 v186, v[22:23] offset:1088
	s_waitcnt vmcnt(20)
	v_pk_fma_f32 v[18:19], v[238:239], v[18:19], 0 op_sel_hi:[0,1,0] neg_lo:[1,0,0] neg_hi:[1,0,0]
	v_pk_fma_f32 v[20:21], v[238:239], v[20:21], 0 op_sel_hi:[0,1,0] neg_lo:[1,0,0] neg_hi:[1,0,0]
	v_cvt_pk_bf16_f32 v18, v18, v19
	v_cvt_pk_bf16_f32 v19, v20, v21
	ds_write_b64 v186, v[18:19] offset:1632
	s_waitcnt vmcnt(19)
	v_pk_fma_f32 v[14:15], v[240:241], v[14:15], 0 op_sel_hi:[0,1,0] neg_lo:[1,0,0] neg_hi:[1,0,0]
	v_pk_fma_f32 v[16:17], v[240:241], v[16:17], 0 op_sel_hi:[0,1,0] neg_lo:[1,0,0] neg_hi:[1,0,0]
	v_cvt_pk_bf16_f32 v14, v14, v15
	v_cvt_pk_bf16_f32 v15, v16, v17
	ds_write_b64 v186, v[14:15] offset:2176
	s_waitcnt vmcnt(18)
	v_pk_fma_f32 v[10:11], v[242:243], v[10:11], 0 op_sel_hi:[0,1,0] neg_lo:[1,0,0] neg_hi:[1,0,0]
	v_pk_fma_f32 v[12:13], v[242:243], v[12:13], 0 op_sel_hi:[0,1,0] neg_lo:[1,0,0] neg_hi:[1,0,0]
	v_cvt_pk_bf16_f32 v10, v10, v11
	v_cvt_pk_bf16_f32 v11, v12, v13
	ds_write_b64 v186, v[10:11] offset:2720
	s_waitcnt vmcnt(17)
	v_pk_fma_f32 v[6:7], v[244:245], v[6:7], 0 op_sel_hi:[0,1,0] neg_lo:[1,0,0] neg_hi:[1,0,0]
	v_pk_fma_f32 v[8:9], v[244:245], v[8:9], 0 op_sel_hi:[0,1,0] neg_lo:[1,0,0] neg_hi:[1,0,0]
	v_cvt_pk_bf16_f32 v6, v6, v7
	v_cvt_pk_bf16_f32 v7, v8, v9
	ds_write_b64 v186, v[6:7] offset:3264
	s_waitcnt vmcnt(16)
	v_pk_fma_f32 v[2:3], v[246:247], v[2:3], 0 op_sel_hi:[0,1,0] neg_lo:[1,0,0] neg_hi:[1,0,0]
	v_pk_fma_f32 v[4:5], v[246:247], v[4:5], 0 op_sel_hi:[0,1,0] neg_lo:[1,0,0] neg_hi:[1,0,0]
	v_cvt_pk_bf16_f32 v2, v2, v3
	v_cvt_pk_bf16_f32 v3, v4, v5
	ds_write_b64 v186, v[2:3] offset:3808
	ds_read_b128 v[232:235], v1
	ds_read_b128 v[236:239], v1 offset:64
	ds_read_b128 v[240:243], v1 offset:128
	ds_read_b128 v[244:247], v1 offset:192
	s_waitcnt lgkmcnt(0)
	ds_write_b128 v184, v[232:235] offset:8192
	ds_write_b128 v184, v[236:239] offset:9216
	ds_write_b128 v184, v[240:243] offset:10240
	ds_write_b128 v184, v[244:247] offset:11264
	ds_read_b32 v232, v187 offset:192
	ds_read_b32 v234, v187 offset:200
	ds_read_b32 v236, v187 offset:208
	ds_read_b32 v238, v187 offset:216
	ds_read_b32 v240, v187 offset:224
	ds_read_b32 v242, v187 offset:232
	ds_read_b32 v244, v187 offset:240
	ds_read_b32 v246, v187 offset:248
	s_lshl_b32 s26, s23, 2
	s_mov_b32 s27, s21
	v_lshl_add_u64 v[2:3], v[126:127], 0, s[26:27]
	v_lshl_add_u64 v[4:5], v[128:129], 0, s[26:27]
	v_lshl_add_u64 v[6:7], v[134:135], 0, s[26:27]
	v_lshl_add_u64 v[8:9], v[136:137], 0, s[26:27]
	v_lshl_add_u64 v[10:11], v[138:139], 0, s[26:27]
	v_lshl_add_u64 v[12:13], v[140:141], 0, s[26:27]
	v_lshl_add_u64 v[14:15], v[142:143], 0, s[26:27]
	v_lshl_add_u64 v[16:17], v[144:145], 0, s[26:27]
	global_load_dwordx4 v[118:121], v[2:3], off nt
	global_load_dwordx4 v[110:113], v[4:5], off nt
	global_load_dwordx4 v[102:105], v[6:7], off nt
	global_load_dwordx4 v[98:101], v[8:9], off nt
	global_load_dwordx4 v[58:61], v[10:11], off nt
	global_load_dwordx4 v[50:53], v[12:13], off nt
	global_load_dwordx4 v[30:33], v[14:15], off nt
	global_load_dwordx4 v[22:25], v[16:17], off nt
	v_mov_b32_e32 v2, v198
	s_waitcnt lgkmcnt(0)
	s_waitcnt vmcnt(23)
	v_pk_fma_f32 v[4:5], v[232:233], v[90:91], 0 op_sel_hi:[0,1,0] neg_lo:[1,0,0] neg_hi:[1,0,0]
	v_pk_fma_f32 v[2:3], v[232:233], v[92:93], 0 op_sel_hi:[0,1,0] neg_lo:[1,0,0] neg_hi:[1,0,0]
	v_cvt_pk_bf16_f32 v4, v4, v5
	v_cvt_pk_bf16_f32 v5, v2, v3
	ds_write_b64 v186, v[4:5]
	s_waitcnt vmcnt(22)
	v_pk_fma_f32 v[4:5], v[234:235], v[82:83], 0 op_sel_hi:[0,1,0] neg_lo:[1,0,0] neg_hi:[1,0,0]
	v_pk_fma_f32 v[2:3], v[234:235], v[84:85], 0 op_sel_hi:[0,1,0] neg_lo:[1,0,0] neg_hi:[1,0,0]
	v_cvt_pk_bf16_f32 v4, v4, v5
	v_cvt_pk_bf16_f32 v5, v2, v3
	ds_write_b64 v186, v[4:5] offset:544
	s_waitcnt vmcnt(21)
	v_pk_fma_f32 v[4:5], v[236:237], v[78:79], 0 op_sel_hi:[0,1,0] neg_lo:[1,0,0] neg_hi:[1,0,0]
	v_pk_fma_f32 v[2:3], v[236:237], v[80:81], 0 op_sel_hi:[0,1,0] neg_lo:[1,0,0] neg_hi:[1,0,0]
	v_cvt_pk_bf16_f32 v4, v4, v5
	v_cvt_pk_bf16_f32 v5, v2, v3
	ds_write_b64 v186, v[4:5] offset:1088
	s_waitcnt vmcnt(20)
	v_pk_fma_f32 v[4:5], v[238:239], v[70:71], 0 op_sel_hi:[0,1,0] neg_lo:[1,0,0] neg_hi:[1,0,0]
	v_pk_fma_f32 v[2:3], v[238:239], v[72:73], 0 op_sel_hi:[0,1,0] neg_lo:[1,0,0] neg_hi:[1,0,0]
	v_cvt_pk_bf16_f32 v4, v4, v5
	v_cvt_pk_bf16_f32 v5, v2, v3
	ds_write_b64 v186, v[4:5] offset:1632
	s_waitcnt vmcnt(19)
	v_pk_fma_f32 v[4:5], v[240:241], v[66:67], 0 op_sel_hi:[0,1,0] neg_lo:[1,0,0] neg_hi:[1,0,0]
	v_pk_fma_f32 v[2:3], v[240:241], v[68:69], 0 op_sel_hi:[0,1,0] neg_lo:[1,0,0] neg_hi:[1,0,0]
	v_cvt_pk_bf16_f32 v4, v4, v5
	v_cvt_pk_bf16_f32 v5, v2, v3
	ds_write_b64 v186, v[4:5] offset:2176
	s_waitcnt vmcnt(18)
	v_pk_fma_f32 v[4:5], v[242:243], v[62:63], 0 op_sel_hi:[0,1,0] neg_lo:[1,0,0] neg_hi:[1,0,0]
	v_pk_fma_f32 v[2:3], v[242:243], v[64:65], 0 op_sel_hi:[0,1,0] neg_lo:[1,0,0] neg_hi:[1,0,0]
	v_cvt_pk_bf16_f32 v4, v4, v5
	v_cvt_pk_bf16_f32 v5, v2, v3
	ds_write_b64 v186, v[4:5] offset:2720
	s_waitcnt vmcnt(17)
	v_pk_fma_f32 v[4:5], v[244:245], v[54:55], 0 op_sel_hi:[0,1,0] neg_lo:[1,0,0] neg_hi:[1,0,0]
	v_pk_fma_f32 v[2:3], v[244:245], v[56:57], 0 op_sel_hi:[0,1,0] neg_lo:[1,0,0] neg_hi:[1,0,0]
	v_cvt_pk_bf16_f32 v4, v4, v5
	v_cvt_pk_bf16_f32 v5, v2, v3
	ds_write_b64 v186, v[4:5] offset:3264
	s_waitcnt vmcnt(16)
	v_pk_fma_f32 v[4:5], v[246:247], v[46:47], 0 op_sel_hi:[0,1,0] neg_lo:[1,0,0] neg_hi:[1,0,0]
	v_pk_fma_f32 v[2:3], v[246:247], v[48:49], 0 op_sel_hi:[0,1,0] neg_lo:[1,0,0] neg_hi:[1,0,0]
	v_cvt_pk_bf16_f32 v4, v4, v5
	v_cvt_pk_bf16_f32 v5, v2, v3
	ds_write_b64 v186, v[4:5] offset:3808
	ds_read_b128 v[232:235], v1
	ds_read_b128 v[236:239], v1 offset:64
	ds_read_b128 v[240:243], v1 offset:128
	ds_read_b128 v[244:247], v1 offset:192
	s_waitcnt lgkmcnt(0)
	ds_write_b128 v184, v[232:235] offset:12288
	ds_write_b128 v184, v[236:239] offset:13312
	ds_write_b128 v184, v[240:243] offset:14336
	ds_write_b128 v184, v[244:247] offset:15360
	ds_read_b32 v232, v187 offset:192
	ds_read_b32 v234, v187 offset:200
	ds_read_b32 v236, v187 offset:208
	ds_read_b32 v238, v187 offset:216
	ds_read_b32 v240, v187 offset:224
	ds_read_b32 v242, v187 offset:232
	ds_read_b32 v244, v187 offset:240
	ds_read_b32 v246, v187 offset:248
	s_lshl_b32 s24, s22, 2
	s_mov_b32 s25, s21
	v_lshl_add_u64 v[2:3], v[126:127], 0, s[24:25]
	v_lshl_add_u64 v[6:7], v[134:135], 0, s[24:25]
	v_lshl_add_u64 v[8:9], v[136:137], 0, s[24:25]
	v_lshl_add_u64 v[14:15], v[142:143], 0, s[24:25]
	v_lshl_add_u64 v[4:5], v[128:129], 0, s[24:25]
	v_lshl_add_u64 v[10:11], v[138:139], 0, s[24:25]
	v_lshl_add_u64 v[12:13], v[140:141], 0, s[24:25]
	v_lshl_add_u64 v[18:19], v[144:145], 0, s[24:25]
	global_load_dwordx4 v[94:97], v[2:3], off nt
	global_load_dwordx4 v[90:93], v[4:5], off nt
	global_load_dwordx4 v[82:85], v[6:7], off nt
	global_load_dwordx4 v[70:73], v[8:9], off nt
	global_load_dwordx4 v[54:57], v[10:11], off nt
	global_load_dwordx4 v[26:29], v[12:13], off nt
	s_nop 0
	global_load_dwordx4 v[14:17], v[14:15], off nt
	s_nop 0
	global_load_dwordx4 v[6:9], v[18:19], off nt
	v_mov_b32_e32 v2, v197
	s_waitcnt lgkmcnt(0)
	s_waitcnt vmcnt(23)
	v_pk_fma_f32 v[4:5], v[232:233], v[122:123], 0 op_sel_hi:[0,1,0] neg_lo:[1,0,0] neg_hi:[1,0,0]
	v_pk_fma_f32 v[2:3], v[232:233], v[124:125], 0 op_sel_hi:[0,1,0] neg_lo:[1,0,0] neg_hi:[1,0,0]
	v_cvt_pk_bf16_f32 v4, v4, v5
	v_cvt_pk_bf16_f32 v5, v2, v3
	ds_write_b64 v186, v[4:5]
	s_waitcnt vmcnt(22)
	v_pk_fma_f32 v[4:5], v[234:235], v[114:115], 0 op_sel_hi:[0,1,0] neg_lo:[1,0,0] neg_hi:[1,0,0]
	v_pk_fma_f32 v[2:3], v[234:235], v[116:117], 0 op_sel_hi:[0,1,0] neg_lo:[1,0,0] neg_hi:[1,0,0]
	v_cvt_pk_bf16_f32 v4, v4, v5
	v_cvt_pk_bf16_f32 v5, v2, v3
	ds_write_b64 v186, v[4:5] offset:544
	s_waitcnt vmcnt(21)
	v_pk_fma_f32 v[4:5], v[236:237], v[106:107], 0 op_sel_hi:[0,1,0] neg_lo:[1,0,0] neg_hi:[1,0,0]
	v_pk_fma_f32 v[2:3], v[236:237], v[108:109], 0 op_sel_hi:[0,1,0] neg_lo:[1,0,0] neg_hi:[1,0,0]
	v_cvt_pk_bf16_f32 v4, v4, v5
	v_cvt_pk_bf16_f32 v5, v2, v3
	ds_write_b64 v186, v[4:5] offset:1088
	s_waitcnt vmcnt(20)
	v_pk_fma_f32 v[4:5], v[238:239], v[86:87], 0 op_sel_hi:[0,1,0] neg_lo:[1,0,0] neg_hi:[1,0,0]
	v_pk_fma_f32 v[2:3], v[238:239], v[88:89], 0 op_sel_hi:[0,1,0] neg_lo:[1,0,0] neg_hi:[1,0,0]
	v_cvt_pk_bf16_f32 v4, v4, v5
	v_cvt_pk_bf16_f32 v5, v2, v3
	ds_write_b64 v186, v[4:5] offset:1632
	s_waitcnt vmcnt(19)
	v_pk_fma_f32 v[4:5], v[240:241], v[74:75], 0 op_sel_hi:[0,1,0] neg_lo:[1,0,0] neg_hi:[1,0,0]
	v_pk_fma_f32 v[2:3], v[240:241], v[76:77], 0 op_sel_hi:[0,1,0] neg_lo:[1,0,0] neg_hi:[1,0,0]
	v_cvt_pk_bf16_f32 v4, v4, v5
	v_cvt_pk_bf16_f32 v5, v2, v3
	ds_write_b64 v186, v[4:5] offset:2176
	s_waitcnt vmcnt(18)
	v_pk_fma_f32 v[4:5], v[242:243], v[42:43], 0 op_sel_hi:[0,1,0] neg_lo:[1,0,0] neg_hi:[1,0,0]
	v_pk_fma_f32 v[2:3], v[242:243], v[44:45], 0 op_sel_hi:[0,1,0] neg_lo:[1,0,0] neg_hi:[1,0,0]
	v_cvt_pk_bf16_f32 v4, v4, v5
	v_cvt_pk_bf16_f32 v5, v2, v3
	ds_write_b64 v186, v[4:5] offset:2720
	s_waitcnt vmcnt(17)
	v_pk_fma_f32 v[4:5], v[244:245], v[38:39], 0 op_sel_hi:[0,1,0] neg_lo:[1,0,0] neg_hi:[1,0,0]
	v_pk_fma_f32 v[2:3], v[244:245], v[40:41], 0 op_sel_hi:[0,1,0] neg_lo:[1,0,0] neg_hi:[1,0,0]
	v_cvt_pk_bf16_f32 v4, v4, v5
	v_cvt_pk_bf16_f32 v5, v2, v3
	ds_write_b64 v186, v[4:5] offset:3264
	s_waitcnt vmcnt(16)
	v_pk_fma_f32 v[4:5], v[246:247], v[34:35], 0 op_sel_hi:[0,1,0] neg_lo:[1,0,0] neg_hi:[1,0,0]
	v_pk_fma_f32 v[2:3], v[246:247], v[36:37], 0 op_sel_hi:[0,1,0] neg_lo:[1,0,0] neg_hi:[1,0,0]
	v_cvt_pk_bf16_f32 v4, v4, v5
	v_cvt_pk_bf16_f32 v5, v2, v3
	ds_write_b64 v186, v[4:5] offset:3808
	ds_read_b128 v[232:235], v1
	ds_read_b128 v[236:239], v1 offset:64
	ds_read_b128 v[240:243], v1 offset:128
	ds_read_b128 v[244:247], v1 offset:192
	s_waitcnt lgkmcnt(0)
	ds_write_b128 v184, v[232:235] offset:16384
	ds_write_b128 v184, v[236:239] offset:17408
	ds_write_b128 v184, v[240:243] offset:18432
	ds_write_b128 v184, v[244:247] offset:19456
	ds_read_b32 v232, v187 offset:192
	ds_read_b32 v234, v187 offset:200
	ds_read_b32 v236, v187 offset:208
	ds_read_b32 v238, v187 offset:216
	ds_read_b32 v240, v187 offset:224
	ds_read_b32 v242, v187 offset:232
	ds_read_b32 v244, v187 offset:240
	ds_read_b32 v246, v187 offset:248
	s_lshl_b32 s22, s7, 2
	s_mov_b32 s23, s21
	v_lshl_add_u64 v[2:3], v[126:127], 0, s[22:23]
	v_lshl_add_u64 v[4:5], v[128:129], 0, s[22:23]
	v_lshl_add_u64 v[10:11], v[134:135], 0, s[22:23]
	v_lshl_add_u64 v[12:13], v[136:137], 0, s[22:23]
	v_lshl_add_u64 v[34:35], v[138:139], 0, s[22:23]
	v_lshl_add_u64 v[36:37], v[140:141], 0, s[22:23]
	v_lshl_add_u64 v[46:47], v[142:143], 0, s[22:23]
	v_lshl_add_u64 v[48:49], v[144:145], 0, s[22:23]
	global_load_dwordx4 v[86:89], v[2:3], off nt
	global_load_dwordx4 v[78:81], v[4:5], off nt
	global_load_dwordx4 v[66:69], v[10:11], off nt
	global_load_dwordx4 v[42:45], v[12:13], off nt
	global_load_dwordx4 v[38:41], v[34:35], off nt
	global_load_dwordx4 v[18:21], v[36:37], off nt
	s_nop 0
	global_load_dwordx4 v[10:13], v[46:47], off nt
	global_load_dwordx4 v[2:5], v[48:49], off nt
	v_mov_b32_e32 v34, v196
	s_waitcnt lgkmcnt(0)
	s_waitcnt vmcnt(23)
	v_pk_fma_f32 v[36:37], v[232:233], v[118:119], 0 op_sel_hi:[0,1,0] neg_lo:[1,0,0] neg_hi:[1,0,0]
	v_pk_fma_f32 v[34:35], v[232:233], v[120:121], 0 op_sel_hi:[0,1,0] neg_lo:[1,0,0] neg_hi:[1,0,0]
	v_cvt_pk_bf16_f32 v36, v36, v37
	v_cvt_pk_bf16_f32 v37, v34, v35
	ds_write_b64 v186, v[36:37]
	s_waitcnt vmcnt(22)
	v_pk_fma_f32 v[36:37], v[234:235], v[110:111], 0 op_sel_hi:[0,1,0] neg_lo:[1,0,0] neg_hi:[1,0,0]
	v_pk_fma_f32 v[34:35], v[234:235], v[112:113], 0 op_sel_hi:[0,1,0] neg_lo:[1,0,0] neg_hi:[1,0,0]
	v_cvt_pk_bf16_f32 v36, v36, v37
	v_cvt_pk_bf16_f32 v37, v34, v35
	ds_write_b64 v186, v[36:37] offset:544
	s_waitcnt vmcnt(21)
	v_pk_fma_f32 v[36:37], v[236:237], v[102:103], 0 op_sel_hi:[0,1,0] neg_lo:[1,0,0] neg_hi:[1,0,0]
	v_pk_fma_f32 v[34:35], v[236:237], v[104:105], 0 op_sel_hi:[0,1,0] neg_lo:[1,0,0] neg_hi:[1,0,0]
	v_cvt_pk_bf16_f32 v36, v36, v37
	v_cvt_pk_bf16_f32 v37, v34, v35
	ds_write_b64 v186, v[36:37] offset:1088
	s_waitcnt vmcnt(20)
	v_pk_fma_f32 v[36:37], v[238:239], v[98:99], 0 op_sel_hi:[0,1,0] neg_lo:[1,0,0] neg_hi:[1,0,0]
	v_pk_fma_f32 v[34:35], v[238:239], v[100:101], 0 op_sel_hi:[0,1,0] neg_lo:[1,0,0] neg_hi:[1,0,0]
	v_cvt_pk_bf16_f32 v36, v36, v37
	v_cvt_pk_bf16_f32 v37, v34, v35
	ds_write_b64 v186, v[36:37] offset:1632
	s_waitcnt vmcnt(19)
	v_pk_fma_f32 v[36:37], v[240:241], v[58:59], 0 op_sel_hi:[0,1,0] neg_lo:[1,0,0] neg_hi:[1,0,0]
	v_pk_fma_f32 v[34:35], v[240:241], v[60:61], 0 op_sel_hi:[0,1,0] neg_lo:[1,0,0] neg_hi:[1,0,0]
	v_cvt_pk_bf16_f32 v36, v36, v37
	v_cvt_pk_bf16_f32 v37, v34, v35
	ds_write_b64 v186, v[36:37] offset:2176
	s_waitcnt vmcnt(18)
	v_pk_fma_f32 v[36:37], v[242:243], v[50:51], 0 op_sel_hi:[0,1,0] neg_lo:[1,0,0] neg_hi:[1,0,0]
	v_pk_fma_f32 v[34:35], v[242:243], v[52:53], 0 op_sel_hi:[0,1,0] neg_lo:[1,0,0] neg_hi:[1,0,0]
	v_cvt_pk_bf16_f32 v36, v36, v37
	v_cvt_pk_bf16_f32 v37, v34, v35
	ds_write_b64 v186, v[36:37] offset:2720
	s_waitcnt vmcnt(17)
	v_pk_fma_f32 v[30:31], v[244:245], v[30:31], 0 op_sel_hi:[0,1,0] neg_lo:[1,0,0] neg_hi:[1,0,0]
	v_pk_fma_f32 v[32:33], v[244:245], v[32:33], 0 op_sel_hi:[0,1,0] neg_lo:[1,0,0] neg_hi:[1,0,0]
	v_cvt_pk_bf16_f32 v30, v30, v31
	v_cvt_pk_bf16_f32 v31, v32, v33
	ds_write_b64 v186, v[30:31] offset:3264
	s_waitcnt vmcnt(16)
	v_pk_fma_f32 v[22:23], v[246:247], v[22:23], 0 op_sel_hi:[0,1,0] neg_lo:[1,0,0] neg_hi:[1,0,0]
	v_pk_fma_f32 v[24:25], v[246:247], v[24:25], 0 op_sel_hi:[0,1,0] neg_lo:[1,0,0] neg_hi:[1,0,0]
	v_cvt_pk_bf16_f32 v22, v22, v23
	v_cvt_pk_bf16_f32 v23, v24, v25
	ds_write_b64 v186, v[22:23] offset:3808
	ds_read_b128 v[232:235], v1
	ds_read_b128 v[236:239], v1 offset:64
	ds_read_b128 v[240:243], v1 offset:128
	ds_read_b128 v[244:247], v1 offset:192
	s_waitcnt lgkmcnt(0)
	ds_write_b128 v184, v[232:235] offset:20480
	ds_write_b128 v184, v[236:239] offset:21504
	ds_write_b128 v184, v[240:243] offset:22528
	ds_write_b128 v184, v[244:247] offset:23552
	ds_read_b32 v232, v187 offset:192
	ds_read_b32 v234, v187 offset:200
	ds_read_b32 v236, v187 offset:208
	ds_read_b32 v238, v187 offset:216
	ds_read_b32 v240, v187 offset:224
	ds_read_b32 v242, v187 offset:232
	ds_read_b32 v244, v187 offset:240
	ds_read_b32 v246, v187 offset:248
	v_lshl_add_u64 v[22:23], v[130:131], 0, s[30:31]
	s_movk_i32 s7, 0x2000
	v_add_co_u32_e32 v24, vcc, s7, v22
	s_movk_i32 s36, 0x4000
	s_nop 0
	v_addc_co_u32_e32 v25, vcc, 0, v23, vcc
	global_load_dwordx4 v[74:77], v[22:23], off nt
	global_load_dwordx4 v[62:65], v[24:25], off nt
	v_add_co_u32_e32 v24, vcc, s36, v22
	s_movk_i32 s37, 0x6000
	s_nop 0
	v_addc_co_u32_e32 v25, vcc, 0, v23, vcc
	v_add_co_u32_e32 v30, vcc, s37, v22
	s_mov_b32 s38, 0x8000
	s_nop 0
	v_addc_co_u32_e32 v31, vcc, 0, v23, vcc
	global_load_dwordx4 v[58:61], v[24:25], off nt
	global_load_dwordx4 v[46:49], v[30:31], off nt
	v_add_co_u32_e32 v24, vcc, s38, v22
	s_mov_b32 s39, 0xa000
	s_nop 0
	v_addc_co_u32_e32 v25, vcc, 0, v23, vcc
	v_add_co_u32_e32 v34, vcc, s39, v22
	s_mov_b32 s41, 0xc000
	s_nop 0
	v_addc_co_u32_e32 v35, vcc, 0, v23, vcc
	global_load_dwordx4 v[50:53], v[24:25], off nt
	global_load_dwordx4 v[30:33], v[34:35], off nt
	v_add_co_u32_e32 v24, vcc, s41, v22
	s_mov_b32 s42, 0xe000
	s_nop 0
	v_addc_co_u32_e32 v25, vcc, 0, v23, vcc
	v_add_co_u32_e32 v22, vcc, s42, v22
	s_nop 1
	v_addc_co_u32_e32 v23, vcc, 0, v23, vcc
	global_load_dwordx4 v[34:37], v[24:25], off nt
	s_nop 0
	global_load_dwordx4 v[22:25], v[22:23], off nt
	v_mov_b32_e32 v98, v195
	s_waitcnt lgkmcnt(0)
	s_waitcnt vmcnt(23)
	v_pk_fma_f32 v[94:95], v[232:233], v[94:95], 0 op_sel_hi:[0,1,0] neg_lo:[1,0,0] neg_hi:[1,0,0]
	v_pk_fma_f32 v[96:97], v[232:233], v[96:97], 0 op_sel_hi:[0,1,0] neg_lo:[1,0,0] neg_hi:[1,0,0]
	v_cvt_pk_bf16_f32 v94, v94, v95
	v_cvt_pk_bf16_f32 v95, v96, v97
	ds_write_b64 v186, v[94:95]
	s_waitcnt vmcnt(22)
	v_pk_fma_f32 v[90:91], v[234:235], v[90:91], 0 op_sel_hi:[0,1,0] neg_lo:[1,0,0] neg_hi:[1,0,0]
	v_pk_fma_f32 v[92:93], v[234:235], v[92:93], 0 op_sel_hi:[0,1,0] neg_lo:[1,0,0] neg_hi:[1,0,0]
	v_cvt_pk_bf16_f32 v90, v90, v91
	v_cvt_pk_bf16_f32 v91, v92, v93
	ds_write_b64 v186, v[90:91] offset:544
	s_waitcnt vmcnt(21)
	v_pk_fma_f32 v[82:83], v[236:237], v[82:83], 0 op_sel_hi:[0,1,0] neg_lo:[1,0,0] neg_hi:[1,0,0]
	v_pk_fma_f32 v[84:85], v[236:237], v[84:85], 0 op_sel_hi:[0,1,0] neg_lo:[1,0,0] neg_hi:[1,0,0]
	v_cvt_pk_bf16_f32 v82, v82, v83
	v_cvt_pk_bf16_f32 v83, v84, v85
	ds_write_b64 v186, v[82:83] offset:1088
	s_waitcnt vmcnt(20)
	v_pk_fma_f32 v[70:71], v[238:239], v[70:71], 0 op_sel_hi:[0,1,0] neg_lo:[1,0,0] neg_hi:[1,0,0]
	v_pk_fma_f32 v[72:73], v[238:239], v[72:73], 0 op_sel_hi:[0,1,0] neg_lo:[1,0,0] neg_hi:[1,0,0]
	v_cvt_pk_bf16_f32 v70, v70, v71
	v_cvt_pk_bf16_f32 v71, v72, v73
	ds_write_b64 v186, v[70:71] offset:1632
	s_waitcnt vmcnt(19)
	v_pk_fma_f32 v[54:55], v[240:241], v[54:55], 0 op_sel_hi:[0,1,0] neg_lo:[1,0,0] neg_hi:[1,0,0]
	v_pk_fma_f32 v[56:57], v[240:241], v[56:57], 0 op_sel_hi:[0,1,0] neg_lo:[1,0,0] neg_hi:[1,0,0]
	v_cvt_pk_bf16_f32 v54, v54, v55
	v_cvt_pk_bf16_f32 v55, v56, v57
	ds_write_b64 v186, v[54:55] offset:2176
	s_waitcnt vmcnt(18)
	v_pk_fma_f32 v[26:27], v[242:243], v[26:27], 0 op_sel_hi:[0,1,0] neg_lo:[1,0,0] neg_hi:[1,0,0]
	v_pk_fma_f32 v[28:29], v[242:243], v[28:29], 0 op_sel_hi:[0,1,0] neg_lo:[1,0,0] neg_hi:[1,0,0]
	v_cvt_pk_bf16_f32 v26, v26, v27
	v_cvt_pk_bf16_f32 v27, v28, v29
	ds_write_b64 v186, v[26:27] offset:2720
	s_waitcnt vmcnt(17)
	v_pk_fma_f32 v[14:15], v[244:245], v[14:15], 0 op_sel_hi:[0,1,0] neg_lo:[1,0,0] neg_hi:[1,0,0]
	v_pk_fma_f32 v[16:17], v[244:245], v[16:17], 0 op_sel_hi:[0,1,0] neg_lo:[1,0,0] neg_hi:[1,0,0]
	v_cvt_pk_bf16_f32 v14, v14, v15
	v_cvt_pk_bf16_f32 v15, v16, v17
	ds_write_b64 v186, v[14:15] offset:3264
	s_waitcnt vmcnt(16)
	v_pk_fma_f32 v[6:7], v[246:247], v[6:7], 0 op_sel_hi:[0,1,0] neg_lo:[1,0,0] neg_hi:[1,0,0]
	v_pk_fma_f32 v[8:9], v[246:247], v[8:9], 0 op_sel_hi:[0,1,0] neg_lo:[1,0,0] neg_hi:[1,0,0]
	v_cvt_pk_bf16_f32 v6, v6, v7
	v_cvt_pk_bf16_f32 v7, v8, v9
	ds_write_b64 v186, v[6:7] offset:3808
	ds_read_b128 v[232:235], v1
	ds_read_b128 v[236:239], v1 offset:64
	ds_read_b128 v[240:243], v1 offset:128
	ds_read_b128 v[244:247], v1 offset:192
	s_waitcnt lgkmcnt(0)
	ds_write_b128 v184, v[232:235] offset:24576
	ds_write_b128 v184, v[236:239] offset:25600
	ds_write_b128 v184, v[240:243] offset:26624
	ds_write_b128 v184, v[244:247] offset:27648
	ds_read_b32 v232, v187 offset:192
	ds_read_b32 v234, v187 offset:200
	ds_read_b32 v236, v187 offset:208
	ds_read_b32 v238, v187 offset:216
	ds_read_b32 v240, v187 offset:224
	ds_read_b32 v242, v187 offset:232
	ds_read_b32 v244, v187 offset:240
	ds_read_b32 v246, v187 offset:248
	s_mov_b64 s[44:45], 0x10000
	v_lshl_add_u64 v[150:151], v[130:131], 0, s[44:45]
	s_mov_b64 s[44:45], 0x12000
	v_lshl_add_u64 v[152:153], v[130:131], 0, s[44:45]
	s_mov_b64 s[44:45], 0x14000
	v_lshl_add_u64 v[156:157], v[130:131], 0, s[44:45]
	s_mov_b64 s[44:45], 0x16000
	v_lshl_add_u64 v[158:159], v[130:131], 0, s[44:45]
	s_mov_b64 s[44:45], 0x18000
	v_lshl_add_u64 v[160:161], v[130:131], 0, s[44:45]
	s_mov_b64 s[44:45], 0x1a000
	v_lshl_add_u64 v[162:163], v[130:131], 0, s[44:45]
	s_mov_b64 s[44:45], 0x1c000
	v_lshl_add_u64 v[164:165], v[130:131], 0, s[44:45]
	s_mov_b64 s[44:45], 0x1e000
	v_lshl_add_u64 v[6:7], v[150:151], 0, s[30:31]
	v_lshl_add_u64 v[8:9], v[152:153], 0, s[30:31]
	v_lshl_add_u64 v[14:15], v[156:157], 0, s[30:31]
	v_lshl_add_u64 v[16:17], v[158:159], 0, s[30:31]
	v_lshl_add_u64 v[26:27], v[160:161], 0, s[30:31]
	v_lshl_add_u64 v[28:29], v[162:163], 0, s[30:31]
	v_lshl_add_u64 v[166:167], v[130:131], 0, s[44:45]
	v_lshl_add_u64 v[98:99], v[164:165], 0, s[30:31]
	v_lshl_add_u64 v[100:101], v[166:167], 0, s[30:31]
	global_load_dwordx4 v[94:97], v[6:7], off nt
	global_load_dwordx4 v[90:93], v[8:9], off nt
	global_load_dwordx4 v[82:85], v[14:15], off nt
	global_load_dwordx4 v[70:73], v[16:17], off nt
	global_load_dwordx4 v[54:57], v[26:27], off nt
	s_nop 0
	global_load_dwordx4 v[26:29], v[28:29], off nt
	s_nop 0
	global_load_dwordx4 v[14:17], v[98:99], off nt
	global_load_dwordx4 v[6:9], v[100:101], off nt
	v_mov_b32_e32 v98, v194
	s_waitcnt lgkmcnt(0)
	s_waitcnt vmcnt(23)
	v_pk_fma_f32 v[86:87], v[232:233], v[86:87], 0 op_sel_hi:[0,1,0] neg_lo:[1,0,0] neg_hi:[1,0,0]
	v_pk_fma_f32 v[88:89], v[232:233], v[88:89], 0 op_sel_hi:[0,1,0] neg_lo:[1,0,0] neg_hi:[1,0,0]
	v_cvt_pk_bf16_f32 v86, v86, v87
	v_cvt_pk_bf16_f32 v87, v88, v89
	ds_write_b64 v186, v[86:87]
	s_waitcnt vmcnt(22)
	v_pk_fma_f32 v[78:79], v[234:235], v[78:79], 0 op_sel_hi:[0,1,0] neg_lo:[1,0,0] neg_hi:[1,0,0]
	v_pk_fma_f32 v[80:81], v[234:235], v[80:81], 0 op_sel_hi:[0,1,0] neg_lo:[1,0,0] neg_hi:[1,0,0]
	v_cvt_pk_bf16_f32 v78, v78, v79
	v_cvt_pk_bf16_f32 v79, v80, v81
	ds_write_b64 v186, v[78:79] offset:544
	s_waitcnt vmcnt(21)
	v_pk_fma_f32 v[66:67], v[236:237], v[66:67], 0 op_sel_hi:[0,1,0] neg_lo:[1,0,0] neg_hi:[1,0,0]
	v_pk_fma_f32 v[68:69], v[236:237], v[68:69], 0 op_sel_hi:[0,1,0] neg_lo:[1,0,0] neg_hi:[1,0,0]
	v_cvt_pk_bf16_f32 v66, v66, v67
	v_cvt_pk_bf16_f32 v67, v68, v69
	ds_write_b64 v186, v[66:67] offset:1088
	s_waitcnt vmcnt(20)
	v_pk_fma_f32 v[42:43], v[238:239], v[42:43], 0 op_sel_hi:[0,1,0] neg_lo:[1,0,0] neg_hi:[1,0,0]
	v_pk_fma_f32 v[44:45], v[238:239], v[44:45], 0 op_sel_hi:[0,1,0] neg_lo:[1,0,0] neg_hi:[1,0,0]
	v_cvt_pk_bf16_f32 v42, v42, v43
	v_cvt_pk_bf16_f32 v43, v44, v45
	ds_write_b64 v186, v[42:43] offset:1632
	s_waitcnt vmcnt(19)
	v_pk_fma_f32 v[38:39], v[240:241], v[38:39], 0 op_sel_hi:[0,1,0] neg_lo:[1,0,0] neg_hi:[1,0,0]
	v_pk_fma_f32 v[40:41], v[240:241], v[40:41], 0 op_sel_hi:[0,1,0] neg_lo:[1,0,0] neg_hi:[1,0,0]
	v_cvt_pk_bf16_f32 v38, v38, v39
	v_cvt_pk_bf16_f32 v39, v40, v41
	ds_write_b64 v186, v[38:39] offset:2176
	s_waitcnt vmcnt(18)
	v_pk_fma_f32 v[18:19], v[242:243], v[18:19], 0 op_sel_hi:[0,1,0] neg_lo:[1,0,0] neg_hi:[1,0,0]
	v_pk_fma_f32 v[20:21], v[242:243], v[20:21], 0 op_sel_hi:[0,1,0] neg_lo:[1,0,0] neg_hi:[1,0,0]
	v_cvt_pk_bf16_f32 v18, v18, v19
	v_cvt_pk_bf16_f32 v19, v20, v21
	ds_write_b64 v186, v[18:19] offset:2720
	s_waitcnt vmcnt(17)
	v_pk_fma_f32 v[10:11], v[244:245], v[10:11], 0 op_sel_hi:[0,1,0] neg_lo:[1,0,0] neg_hi:[1,0,0]
	v_pk_fma_f32 v[12:13], v[244:245], v[12:13], 0 op_sel_hi:[0,1,0] neg_lo:[1,0,0] neg_hi:[1,0,0]
	v_cvt_pk_bf16_f32 v10, v10, v11
	v_cvt_pk_bf16_f32 v11, v12, v13
	ds_write_b64 v186, v[10:11] offset:3264
	s_waitcnt vmcnt(16)
	v_pk_fma_f32 v[2:3], v[246:247], v[2:3], 0 op_sel_hi:[0,1,0] neg_lo:[1,0,0] neg_hi:[1,0,0]
	v_pk_fma_f32 v[4:5], v[246:247], v[4:5], 0 op_sel_hi:[0,1,0] neg_lo:[1,0,0] neg_hi:[1,0,0]
	v_cvt_pk_bf16_f32 v2, v2, v3
	v_cvt_pk_bf16_f32 v3, v4, v5
	ds_write_b64 v186, v[2:3] offset:3808
	ds_read_b128 v[232:235], v1
	ds_read_b128 v[236:239], v1 offset:64
	ds_read_b128 v[240:243], v1 offset:128
	ds_read_b128 v[244:247], v1 offset:192
	s_waitcnt lgkmcnt(0)
	ds_write_b128 v184, v[232:235] offset:28672
	ds_write_b128 v184, v[236:239] offset:29696
	ds_write_b128 v184, v[240:243] offset:30720
	ds_write_b128 v184, v[244:247] offset:31744
	ds_read_b32 v232, v187 offset:0
	ds_read_b32 v234, v187 offset:8
	ds_read_b32 v236, v187 offset:16
	ds_read_b32 v238, v187 offset:24
	ds_read_b32 v240, v187 offset:32
	ds_read_b32 v242, v187 offset:40
	ds_read_b32 v244, v187 offset:48
	ds_read_b32 v246, v187 offset:56
	s_mov_b64 s[44:45], 0x20000
	v_lshl_add_u64 v[168:169], v[130:131], 0, s[44:45]
	s_mov_b64 s[44:45], 0x22000
	v_lshl_add_u64 v[170:171], v[130:131], 0, s[44:45]
	s_mov_b64 s[44:45], 0x24000
	v_lshl_add_u64 v[172:173], v[130:131], 0, s[44:45]
	s_mov_b64 s[44:45], 0x26000
	v_lshl_add_u64 v[174:175], v[130:131], 0, s[44:45]
	s_mov_b64 s[44:45], 0x28000
	v_lshl_add_u64 v[176:177], v[130:131], 0, s[44:45]
	s_mov_b64 s[44:45], 0x2a000
	v_lshl_add_u64 v[178:179], v[130:131], 0, s[44:45]
	s_mov_b64 s[44:45], 0x2c000
	v_lshl_add_u64 v[180:181], v[130:131], 0, s[44:45]
	s_mov_b64 s[44:45], 0x2e000
	v_lshl_add_u64 v[2:3], v[168:169], 0, s[30:31]
	v_lshl_add_u64 v[4:5], v[170:171], 0, s[30:31]
	v_lshl_add_u64 v[10:11], v[172:173], 0, s[30:31]
	v_lshl_add_u64 v[12:13], v[174:175], 0, s[30:31]
	v_lshl_add_u64 v[18:19], v[176:177], 0, s[30:31]
	v_lshl_add_u64 v[20:21], v[178:179], 0, s[30:31]
	v_lshl_add_u64 v[182:183], v[130:131], 0, s[44:45]
	v_lshl_add_u64 v[42:43], v[180:181], 0, s[30:31]
	v_lshl_add_u64 v[44:45], v[182:183], 0, s[30:31]
	global_load_dwordx4 v[106:109], v[2:3], off nt
	global_load_dwordx4 v[98:101], v[4:5], off nt
	global_load_dwordx4 v[78:81], v[10:11], off nt
	global_load_dwordx4 v[66:69], v[12:13], off nt
	global_load_dwordx4 v[38:41], v[18:19], off nt
	s_nop 0
	global_load_dwordx4 v[18:21], v[20:21], off nt
	s_nop 0
	global_load_dwordx4 v[10:13], v[42:43], off nt
	global_load_dwordx4 v[2:5], v[44:45], off nt
	v_mov_b32_e32 v42, v198
	s_waitcnt lgkmcnt(0)
	s_waitcnt vmcnt(23)
	v_pk_fma_f32 v[44:45], v[232:233], v[74:75], 0 op_sel_hi:[0,1,0] neg_lo:[1,0,0] neg_hi:[1,0,0]
	v_pk_fma_f32 v[42:43], v[232:233], v[76:77], 0 op_sel_hi:[0,1,0] neg_lo:[1,0,0] neg_hi:[1,0,0]
	v_cvt_pk_bf16_f32 v44, v44, v45
	v_cvt_pk_bf16_f32 v45, v42, v43
	ds_write_b64 v186, v[44:45]
	s_waitcnt vmcnt(22)
	v_pk_fma_f32 v[44:45], v[234:235], v[62:63], 0 op_sel_hi:[0,1,0] neg_lo:[1,0,0] neg_hi:[1,0,0]
	v_pk_fma_f32 v[42:43], v[234:235], v[64:65], 0 op_sel_hi:[0,1,0] neg_lo:[1,0,0] neg_hi:[1,0,0]
	v_cvt_pk_bf16_f32 v44, v44, v45
	v_cvt_pk_bf16_f32 v45, v42, v43
	ds_write_b64 v186, v[44:45] offset:544
	s_waitcnt vmcnt(21)
	v_pk_fma_f32 v[44:45], v[236:237], v[58:59], 0 op_sel_hi:[0,1,0] neg_lo:[1,0,0] neg_hi:[1,0,0]
	v_pk_fma_f32 v[42:43], v[236:237], v[60:61], 0 op_sel_hi:[0,1,0] neg_lo:[1,0,0] neg_hi:[1,0,0]
	v_cvt_pk_bf16_f32 v44, v44, v45
	v_cvt_pk_bf16_f32 v45, v42, v43
	ds_write_b64 v186, v[44:45] offset:1088
	s_waitcnt vmcnt(20)
	v_pk_fma_f32 v[44:45], v[238:239], v[46:47], 0 op_sel_hi:[0,1,0] neg_lo:[1,0,0] neg_hi:[1,0,0]
	v_pk_fma_f32 v[42:43], v[238:239], v[48:49], 0 op_sel_hi:[0,1,0] neg_lo:[1,0,0] neg_hi:[1,0,0]
	v_cvt_pk_bf16_f32 v44, v44, v45
	v_cvt_pk_bf16_f32 v45, v42, v43
	ds_write_b64 v186, v[44:45] offset:1632
	s_waitcnt vmcnt(19)
	v_pk_fma_f32 v[44:45], v[240:241], v[50:51], 0 op_sel_hi:[0,1,0] neg_lo:[1,0,0] neg_hi:[1,0,0]
	v_pk_fma_f32 v[42:43], v[240:241], v[52:53], 0 op_sel_hi:[0,1,0] neg_lo:[1,0,0] neg_hi:[1,0,0]
	v_cvt_pk_bf16_f32 v44, v44, v45
	v_cvt_pk_bf16_f32 v45, v42, v43
	ds_write_b64 v186, v[44:45] offset:2176
	s_waitcnt vmcnt(18)
	v_pk_fma_f32 v[30:31], v[242:243], v[30:31], 0 op_sel_hi:[0,1,0] neg_lo:[1,0,0] neg_hi:[1,0,0]
	v_pk_fma_f32 v[32:33], v[242:243], v[32:33], 0 op_sel_hi:[0,1,0] neg_lo:[1,0,0] neg_hi:[1,0,0]
	v_cvt_pk_bf16_f32 v30, v30, v31
	v_cvt_pk_bf16_f32 v31, v32, v33
	ds_write_b64 v186, v[30:31] offset:2720
	s_waitcnt vmcnt(17)
	v_pk_fma_f32 v[32:33], v[244:245], v[34:35], 0 op_sel_hi:[0,1,0] neg_lo:[1,0,0] neg_hi:[1,0,0]
	v_pk_fma_f32 v[30:31], v[244:245], v[36:37], 0 op_sel_hi:[0,1,0] neg_lo:[1,0,0] neg_hi:[1,0,0]
	v_cvt_pk_bf16_f32 v32, v32, v33
	v_cvt_pk_bf16_f32 v33, v30, v31
	ds_write_b64 v186, v[32:33] offset:3264
	s_waitcnt vmcnt(16)
	v_pk_fma_f32 v[22:23], v[246:247], v[22:23], 0 op_sel_hi:[0,1,0] neg_lo:[1,0,0] neg_hi:[1,0,0]
	v_pk_fma_f32 v[24:25], v[246:247], v[24:25], 0 op_sel_hi:[0,1,0] neg_lo:[1,0,0] neg_hi:[1,0,0]
	v_cvt_pk_bf16_f32 v22, v22, v23
	v_cvt_pk_bf16_f32 v23, v24, v25
	ds_write_b64 v186, v[22:23] offset:3808
	ds_read_b32 v232, v187 offset:64
	ds_read_b32 v234, v187 offset:72
	ds_read_b32 v236, v187 offset:80
	ds_read_b32 v238, v187 offset:88
	ds_read_b32 v240, v187 offset:96
	ds_read_b32 v242, v187 offset:104
	ds_read_b32 v244, v187 offset:112
	ds_read_b32 v246, v187 offset:120
	ds_read_b128 a[0:3], v1
	ds_read_b128 a[4:7], v1 offset:64
	ds_read_b128 a[8:11], v1 offset:128
	ds_read_b128 a[12:15], v1 offset:192
	v_lshl_add_u64 v[22:23], v[130:131], 0, s[28:29]
	v_add_co_u32_e32 v24, vcc, s7, v22
	s_nop 1
	v_addc_co_u32_e32 v25, vcc, 0, v23, vcc
	global_load_dwordx4 v[102:105], v[22:23], off nt
	global_load_dwordx4 v[86:89], v[24:25], off nt
	v_add_co_u32_e32 v24, vcc, s36, v22
	s_nop 1
	v_addc_co_u32_e32 v25, vcc, 0, v23, vcc
	v_add_co_u32_e32 v30, vcc, s37, v22
	s_nop 1
	v_addc_co_u32_e32 v31, vcc, 0, v23, vcc
	global_load_dwordx4 v[74:77], v[24:25], off nt
	global_load_dwordx4 v[62:65], v[30:31], off nt
	v_add_co_u32_e32 v24, vcc, s38, v22
	s_nop 1
	v_addc_co_u32_e32 v25, vcc, 0, v23, vcc
	v_add_co_u32_e32 v30, vcc, s39, v22
	s_nop 1
	v_addc_co_u32_e32 v31, vcc, 0, v23, vcc
	global_load_dwordx4 v[58:61], v[24:25], off nt
	global_load_dwordx4 v[46:49], v[30:31], off nt
	v_add_co_u32_e32 v24, vcc, s41, v22
	s_nop 1
	v_addc_co_u32_e32 v25, vcc, 0, v23, vcc
	v_add_co_u32_e32 v22, vcc, s42, v22
	s_nop 1
	v_addc_co_u32_e32 v23, vcc, 0, v23, vcc
	global_load_dwordx4 v[42:45], v[24:25], off nt
	global_load_dwordx4 v[30:33], v[22:23], off nt
	v_mov_b32_e32 v22, v198
	s_waitcnt lgkmcnt(0)
	s_waitcnt vmcnt(23)
	v_pk_fma_f32 v[24:25], v[232:233], v[94:95], 0 op_sel_hi:[0,1,0] neg_lo:[1,0,0] neg_hi:[1,0,0]
	v_pk_fma_f32 v[22:23], v[232:233], v[96:97], 0 op_sel_hi:[0,1,0] neg_lo:[1,0,0] neg_hi:[1,0,0]
	v_cvt_pk_bf16_f32 v24, v24, v25
	v_cvt_pk_bf16_f32 v25, v22, v23
	ds_write_b64 v186, v[24:25]
	s_waitcnt vmcnt(22)
	v_pk_fma_f32 v[24:25], v[234:235], v[90:91], 0 op_sel_hi:[0,1,0] neg_lo:[1,0,0] neg_hi:[1,0,0]
	v_pk_fma_f32 v[22:23], v[234:235], v[92:93], 0 op_sel_hi:[0,1,0] neg_lo:[1,0,0] neg_hi:[1,0,0]
	v_cvt_pk_bf16_f32 v24, v24, v25
	v_cvt_pk_bf16_f32 v25, v22, v23
	ds_write_b64 v186, v[24:25] offset:544
	s_waitcnt vmcnt(21)
	v_pk_fma_f32 v[24:25], v[236:237], v[82:83], 0 op_sel_hi:[0,1,0] neg_lo:[1,0,0] neg_hi:[1,0,0]
	v_pk_fma_f32 v[22:23], v[236:237], v[84:85], 0 op_sel_hi:[0,1,0] neg_lo:[1,0,0] neg_hi:[1,0,0]
	v_cvt_pk_bf16_f32 v24, v24, v25
	v_cvt_pk_bf16_f32 v25, v22, v23
	ds_write_b64 v186, v[24:25] offset:1088
	s_waitcnt vmcnt(20)
	v_pk_fma_f32 v[24:25], v[238:239], v[70:71], 0 op_sel_hi:[0,1,0] neg_lo:[1,0,0] neg_hi:[1,0,0]
	v_pk_fma_f32 v[22:23], v[238:239], v[72:73], 0 op_sel_hi:[0,1,0] neg_lo:[1,0,0] neg_hi:[1,0,0]
	v_cvt_pk_bf16_f32 v24, v24, v25
	v_cvt_pk_bf16_f32 v25, v22, v23
	ds_write_b64 v186, v[24:25] offset:1632
	s_waitcnt vmcnt(19)
	v_pk_fma_f32 v[24:25], v[240:241], v[54:55], 0 op_sel_hi:[0,1,0] neg_lo:[1,0,0] neg_hi:[1,0,0]
	v_pk_fma_f32 v[22:23], v[240:241], v[56:57], 0 op_sel_hi:[0,1,0] neg_lo:[1,0,0] neg_hi:[1,0,0]
	v_cvt_pk_bf16_f32 v24, v24, v25
	v_cvt_pk_bf16_f32 v25, v22, v23
	ds_write_b64 v186, v[24:25] offset:2176
	s_waitcnt vmcnt(18)
	v_pk_fma_f32 v[24:25], v[242:243], v[26:27], 0 op_sel_hi:[0,1,0] neg_lo:[1,0,0] neg_hi:[1,0,0]
	v_pk_fma_f32 v[22:23], v[242:243], v[28:29], 0 op_sel_hi:[0,1,0] neg_lo:[1,0,0] neg_hi:[1,0,0]
	v_cvt_pk_bf16_f32 v24, v24, v25
	v_cvt_pk_bf16_f32 v25, v22, v23
	ds_write_b64 v186, v[24:25] offset:2720
	s_waitcnt vmcnt(17)
	v_pk_fma_f32 v[14:15], v[244:245], v[14:15], 0 op_sel_hi:[0,1,0] neg_lo:[1,0,0] neg_hi:[1,0,0]
	v_pk_fma_f32 v[16:17], v[244:245], v[16:17], 0 op_sel_hi:[0,1,0] neg_lo:[1,0,0] neg_hi:[1,0,0]
	v_cvt_pk_bf16_f32 v14, v14, v15
	v_cvt_pk_bf16_f32 v15, v16, v17
	ds_write_b64 v186, v[14:15] offset:3264
	s_waitcnt vmcnt(16)
	v_pk_fma_f32 v[6:7], v[246:247], v[6:7], 0 op_sel_hi:[0,1,0] neg_lo:[1,0,0] neg_hi:[1,0,0]
	v_pk_fma_f32 v[8:9], v[246:247], v[8:9], 0 op_sel_hi:[0,1,0] neg_lo:[1,0,0] neg_hi:[1,0,0]
	v_cvt_pk_bf16_f32 v6, v6, v7
	v_cvt_pk_bf16_f32 v7, v8, v9
	ds_write_b64 v186, v[6:7] offset:3808
	ds_read_b32 v232, v187 offset:128
	ds_read_b32 v234, v187 offset:136
	ds_read_b32 v236, v187 offset:144
	ds_read_b32 v238, v187 offset:152
	ds_read_b32 v240, v187 offset:160
	ds_read_b32 v242, v187 offset:168
	ds_read_b32 v244, v187 offset:176
	ds_read_b32 v246, v187 offset:184
	ds_read_b128 a[16:19], v1
	ds_read_b128 a[20:23], v1 offset:64
	ds_read_b128 a[24:27], v1 offset:128
	ds_read_b128 a[28:31], v1 offset:192
	v_lshl_add_u64 v[6:7], v[150:151], 0, s[28:29]
	v_lshl_add_u64 v[8:9], v[152:153], 0, s[28:29]
	v_lshl_add_u64 v[14:15], v[156:157], 0, s[28:29]
	v_lshl_add_u64 v[16:17], v[158:159], 0, s[28:29]
	v_lshl_add_u64 v[22:23], v[160:161], 0, s[28:29]
	v_lshl_add_u64 v[24:25], v[162:163], 0, s[28:29]
	v_lshl_add_u64 v[26:27], v[164:165], 0, s[28:29]
	v_lshl_add_u64 v[28:29], v[166:167], 0, s[28:29]
	global_load_dwordx4 v[110:113], v[6:7], off nt
	global_load_dwordx4 v[90:93], v[8:9], off nt
	global_load_dwordx4 v[70:73], v[14:15], off nt
	global_load_dwordx4 v[50:53], v[16:17], off nt
	global_load_dwordx4 v[34:37], v[22:23], off nt
	s_nop 0
	global_load_dwordx4 v[22:25], v[24:25], off nt
	s_nop 0
	global_load_dwordx4 v[14:17], v[26:27], off nt
	global_load_dwordx4 v[6:9], v[28:29], off nt
	s_waitcnt lgkmcnt(0)
	s_waitcnt vmcnt(23)
	v_pk_fma_f32 v[28:29], v[232:233], v[106:107], 0 op_sel_hi:[0,1,0] neg_lo:[1,0,0] neg_hi:[1,0,0]
	v_pk_fma_f32 v[26:27], v[232:233], v[108:109], 0 op_sel_hi:[0,1,0] neg_lo:[1,0,0] neg_hi:[1,0,0]
	v_cvt_pk_bf16_f32 v28, v28, v29
	v_cvt_pk_bf16_f32 v29, v26, v27
	ds_write_b64 v186, v[28:29]
	s_waitcnt vmcnt(22)
	v_pk_fma_f32 v[28:29], v[234:235], v[98:99], 0 op_sel_hi:[0,1,0] neg_lo:[1,0,0] neg_hi:[1,0,0]
	v_pk_fma_f32 v[26:27], v[234:235], v[100:101], 0 op_sel_hi:[0,1,0] neg_lo:[1,0,0] neg_hi:[1,0,0]
	v_cvt_pk_bf16_f32 v28, v28, v29
	v_cvt_pk_bf16_f32 v29, v26, v27
	ds_write_b64 v186, v[28:29] offset:544
	s_waitcnt vmcnt(21)
	v_pk_fma_f32 v[28:29], v[236:237], v[78:79], 0 op_sel_hi:[0,1,0] neg_lo:[1,0,0] neg_hi:[1,0,0]
	v_pk_fma_f32 v[26:27], v[236:237], v[80:81], 0 op_sel_hi:[0,1,0] neg_lo:[1,0,0] neg_hi:[1,0,0]
	v_cvt_pk_bf16_f32 v28, v28, v29
	v_cvt_pk_bf16_f32 v29, v26, v27
	ds_write_b64 v186, v[28:29] offset:1088
	s_waitcnt vmcnt(20)
	v_pk_fma_f32 v[28:29], v[238:239], v[66:67], 0 op_sel_hi:[0,1,0] neg_lo:[1,0,0] neg_hi:[1,0,0]
	v_pk_fma_f32 v[26:27], v[238:239], v[68:69], 0 op_sel_hi:[0,1,0] neg_lo:[1,0,0] neg_hi:[1,0,0]
	v_cvt_pk_bf16_f32 v28, v28, v29
	v_cvt_pk_bf16_f32 v29, v26, v27
	ds_write_b64 v186, v[28:29] offset:1632
	s_waitcnt vmcnt(19)
	v_pk_fma_f32 v[28:29], v[240:241], v[38:39], 0 op_sel_hi:[0,1,0] neg_lo:[1,0,0] neg_hi:[1,0,0]
	v_pk_fma_f32 v[26:27], v[240:241], v[40:41], 0 op_sel_hi:[0,1,0] neg_lo:[1,0,0] neg_hi:[1,0,0]
	v_cvt_pk_bf16_f32 v28, v28, v29
	v_cvt_pk_bf16_f32 v29, v26, v27
	ds_write_b64 v186, v[28:29] offset:2176
	s_waitcnt vmcnt(18)
	v_pk_fma_f32 v[18:19], v[242:243], v[18:19], 0 op_sel_hi:[0,1,0] neg_lo:[1,0,0] neg_hi:[1,0,0]
	v_pk_fma_f32 v[20:21], v[242:243], v[20:21], 0 op_sel_hi:[0,1,0] neg_lo:[1,0,0] neg_hi:[1,0,0]
	v_cvt_pk_bf16_f32 v18, v18, v19
	v_cvt_pk_bf16_f32 v19, v20, v21
	ds_write_b64 v186, v[18:19] offset:2720
	s_waitcnt vmcnt(17)
	v_pk_fma_f32 v[10:11], v[244:245], v[10:11], 0 op_sel_hi:[0,1,0] neg_lo:[1,0,0] neg_hi:[1,0,0]
	v_pk_fma_f32 v[12:13], v[244:245], v[12:13], 0 op_sel_hi:[0,1,0] neg_lo:[1,0,0] neg_hi:[1,0,0]
	v_cvt_pk_bf16_f32 v10, v10, v11
	v_cvt_pk_bf16_f32 v11, v12, v13
	ds_write_b64 v186, v[10:11] offset:3264
	s_waitcnt vmcnt(16)
	v_pk_fma_f32 v[2:3], v[246:247], v[2:3], 0 op_sel_hi:[0,1,0] neg_lo:[1,0,0] neg_hi:[1,0,0]
	v_pk_fma_f32 v[4:5], v[246:247], v[4:5], 0 op_sel_hi:[0,1,0] neg_lo:[1,0,0] neg_hi:[1,0,0]
	v_cvt_pk_bf16_f32 v2, v2, v3
	v_cvt_pk_bf16_f32 v3, v4, v5
	ds_write_b64 v186, v[2:3] offset:3808
	ds_read_b32 v232, v187 offset:0
	ds_read_b32 v234, v187 offset:8
	ds_read_b32 v236, v187 offset:16
	ds_read_b32 v238, v187 offset:24
	ds_read_b32 v240, v187 offset:32
	ds_read_b32 v242, v187 offset:40
	ds_read_b32 v244, v187 offset:48
	ds_read_b32 v246, v187 offset:56
	ds_read_b128 a[32:35], v1
	ds_read_b128 a[36:39], v1 offset:64
	ds_read_b128 a[40:43], v1 offset:128
	ds_read_b128 a[44:47], v1 offset:192
	v_lshl_add_u64 v[2:3], v[168:169], 0, s[28:29]
	v_lshl_add_u64 v[4:5], v[170:171], 0, s[28:29]
	v_lshl_add_u64 v[10:11], v[172:173], 0, s[28:29]
	v_lshl_add_u64 v[12:13], v[174:175], 0, s[28:29]
	v_lshl_add_u64 v[18:19], v[176:177], 0, s[28:29]
	v_lshl_add_u64 v[20:21], v[178:179], 0, s[28:29]
	v_lshl_add_u64 v[26:27], v[180:181], 0, s[28:29]
	v_lshl_add_u64 v[28:29], v[182:183], 0, s[28:29]
	global_load_dwordx4 v[106:109], v[2:3], off nt
	global_load_dwordx4 v[94:97], v[4:5], off nt
	global_load_dwordx4 v[66:69], v[10:11], off nt
	global_load_dwordx4 v[54:57], v[12:13], off nt
	global_load_dwordx4 v[38:41], v[18:19], off nt
	s_nop 0
	global_load_dwordx4 v[18:21], v[20:21], off nt
	s_nop 0
	global_load_dwordx4 v[10:13], v[26:27], off nt
	global_load_dwordx4 v[2:5], v[28:29], off nt
	v_mov_b32_e32 v26, v197
	s_waitcnt lgkmcnt(0)
	s_waitcnt vmcnt(23)
	v_pk_fma_f32 v[28:29], v[232:233], v[102:103], 0 op_sel_hi:[0,1,0] neg_lo:[1,0,0] neg_hi:[1,0,0]
	v_pk_fma_f32 v[26:27], v[232:233], v[104:105], 0 op_sel_hi:[0,1,0] neg_lo:[1,0,0] neg_hi:[1,0,0]
	v_cvt_pk_bf16_f32 v28, v28, v29
	v_cvt_pk_bf16_f32 v29, v26, v27
	ds_write_b64 v186, v[28:29]
	s_waitcnt vmcnt(22)
	v_pk_fma_f32 v[28:29], v[234:235], v[86:87], 0 op_sel_hi:[0,1,0] neg_lo:[1,0,0] neg_hi:[1,0,0]
	v_pk_fma_f32 v[26:27], v[234:235], v[88:89], 0 op_sel_hi:[0,1,0] neg_lo:[1,0,0] neg_hi:[1,0,0]
	v_cvt_pk_bf16_f32 v28, v28, v29
	v_cvt_pk_bf16_f32 v29, v26, v27
	ds_write_b64 v186, v[28:29] offset:544
	s_waitcnt vmcnt(21)
	v_pk_fma_f32 v[28:29], v[236:237], v[74:75], 0 op_sel_hi:[0,1,0] neg_lo:[1,0,0] neg_hi:[1,0,0]
	v_pk_fma_f32 v[26:27], v[236:237], v[76:77], 0 op_sel_hi:[0,1,0] neg_lo:[1,0,0] neg_hi:[1,0,0]
	v_cvt_pk_bf16_f32 v28, v28, v29
	v_cvt_pk_bf16_f32 v29, v26, v27
	ds_write_b64 v186, v[28:29] offset:1088
	s_waitcnt vmcnt(20)
	v_pk_fma_f32 v[28:29], v[238:239], v[62:63], 0 op_sel_hi:[0,1,0] neg_lo:[1,0,0] neg_hi:[1,0,0]
	v_pk_fma_f32 v[26:27], v[238:239], v[64:65], 0 op_sel_hi:[0,1,0] neg_lo:[1,0,0] neg_hi:[1,0,0]
	v_cvt_pk_bf16_f32 v28, v28, v29
	v_cvt_pk_bf16_f32 v29, v26, v27
	ds_write_b64 v186, v[28:29] offset:1632
	s_waitcnt vmcnt(19)
	v_pk_fma_f32 v[28:29], v[240:241], v[58:59], 0 op_sel_hi:[0,1,0] neg_lo:[1,0,0] neg_hi:[1,0,0]
	v_pk_fma_f32 v[26:27], v[240:241], v[60:61], 0 op_sel_hi:[0,1,0] neg_lo:[1,0,0] neg_hi:[1,0,0]
	v_cvt_pk_bf16_f32 v28, v28, v29
	v_cvt_pk_bf16_f32 v29, v26, v27
	ds_write_b64 v186, v[28:29] offset:2176
	s_waitcnt vmcnt(18)
	v_pk_fma_f32 v[28:29], v[242:243], v[46:47], 0 op_sel_hi:[0,1,0] neg_lo:[1,0,0] neg_hi:[1,0,0]
	v_pk_fma_f32 v[26:27], v[242:243], v[48:49], 0 op_sel_hi:[0,1,0] neg_lo:[1,0,0] neg_hi:[1,0,0]
	v_cvt_pk_bf16_f32 v28, v28, v29
	v_cvt_pk_bf16_f32 v29, v26, v27
	ds_write_b64 v186, v[28:29] offset:2720
	s_waitcnt vmcnt(17)
	v_pk_fma_f32 v[28:29], v[244:245], v[42:43], 0 op_sel_hi:[0,1,0] neg_lo:[1,0,0] neg_hi:[1,0,0]
	v_pk_fma_f32 v[26:27], v[244:245], v[44:45], 0 op_sel_hi:[0,1,0] neg_lo:[1,0,0] neg_hi:[1,0,0]
	v_cvt_pk_bf16_f32 v28, v28, v29
	v_cvt_pk_bf16_f32 v29, v26, v27
	ds_write_b64 v186, v[28:29] offset:3264
	s_waitcnt vmcnt(16)
	v_pk_fma_f32 v[28:29], v[246:247], v[30:31], 0 op_sel_hi:[0,1,0] neg_lo:[1,0,0] neg_hi:[1,0,0]
	v_pk_fma_f32 v[26:27], v[246:247], v[32:33], 0 op_sel_hi:[0,1,0] neg_lo:[1,0,0] neg_hi:[1,0,0]
	v_cvt_pk_bf16_f32 v28, v28, v29
	v_cvt_pk_bf16_f32 v29, v26, v27
	ds_write_b64 v186, v[28:29] offset:3808
	ds_read_b32 v232, v187 offset:64
	ds_read_b32 v234, v187 offset:72
	ds_read_b32 v236, v187 offset:80
	ds_read_b32 v238, v187 offset:88
	ds_read_b32 v240, v187 offset:96
	ds_read_b32 v242, v187 offset:104
	ds_read_b32 v244, v187 offset:112
	ds_read_b32 v246, v187 offset:120
	ds_read_b128 a[48:51], v1
	ds_read_b128 a[52:55], v1 offset:64
	ds_read_b128 a[56:59], v1 offset:128
	ds_read_b128 a[60:63], v1 offset:192
	v_lshl_add_u64 v[26:27], v[130:131], 0, s[26:27]
	v_add_co_u32_e32 v28, vcc, s7, v26
	s_nop 1
	v_addc_co_u32_e32 v29, vcc, 0, v27, vcc
	global_load_dwordx4 v[86:89], v[26:27], off nt
	global_load_dwordx4 v[82:85], v[28:29], off nt
	v_add_co_u32_e32 v28, vcc, s36, v26
	s_nop 1
	v_addc_co_u32_e32 v29, vcc, 0, v27, vcc
	v_add_co_u32_e32 v30, vcc, s37, v26
	s_nop 1
	v_addc_co_u32_e32 v31, vcc, 0, v27, vcc
	global_load_dwordx4 v[78:81], v[28:29], off nt
	global_load_dwordx4 v[58:61], v[30:31], off nt
	v_add_co_u32_e32 v28, vcc, s38, v26
	s_nop 1
	v_addc_co_u32_e32 v29, vcc, 0, v27, vcc
	v_add_co_u32_e32 v30, vcc, s39, v26
	s_nop 1
	v_addc_co_u32_e32 v31, vcc, 0, v27, vcc
	global_load_dwordx4 v[46:49], v[28:29], off nt
	global_load_dwordx4 v[42:45], v[30:31], off nt
	v_add_co_u32_e32 v28, vcc, s41, v26
	s_nop 1
	v_addc_co_u32_e32 v29, vcc, 0, v27, vcc
	v_add_co_u32_e32 v26, vcc, s42, v26
	s_nop 1
	v_addc_co_u32_e32 v27, vcc, 0, v27, vcc
	global_load_dwordx4 v[30:33], v[28:29], off nt
	s_nop 0
	global_load_dwordx4 v[26:29], v[26:27], off nt
	v_mov_b32_e32 v62, v197
	s_waitcnt lgkmcnt(0)
	s_waitcnt vmcnt(23)
	v_pk_fma_f32 v[64:65], v[232:233], v[110:111], 0 op_sel_hi:[0,1,0] neg_lo:[1,0,0] neg_hi:[1,0,0]
	v_pk_fma_f32 v[62:63], v[232:233], v[112:113], 0 op_sel_hi:[0,1,0] neg_lo:[1,0,0] neg_hi:[1,0,0]
	v_cvt_pk_bf16_f32 v64, v64, v65
	v_cvt_pk_bf16_f32 v65, v62, v63
	ds_write_b64 v186, v[64:65]
	s_waitcnt vmcnt(22)
	v_pk_fma_f32 v[64:65], v[234:235], v[90:91], 0 op_sel_hi:[0,1,0] neg_lo:[1,0,0] neg_hi:[1,0,0]
	v_pk_fma_f32 v[62:63], v[234:235], v[92:93], 0 op_sel_hi:[0,1,0] neg_lo:[1,0,0] neg_hi:[1,0,0]
	v_cvt_pk_bf16_f32 v64, v64, v65
	v_cvt_pk_bf16_f32 v65, v62, v63
	ds_write_b64 v186, v[64:65] offset:544
	s_waitcnt vmcnt(21)
	v_pk_fma_f32 v[64:65], v[236:237], v[70:71], 0 op_sel_hi:[0,1,0] neg_lo:[1,0,0] neg_hi:[1,0,0]
	v_pk_fma_f32 v[62:63], v[236:237], v[72:73], 0 op_sel_hi:[0,1,0] neg_lo:[1,0,0] neg_hi:[1,0,0]
	v_cvt_pk_bf16_f32 v64, v64, v65
	v_cvt_pk_bf16_f32 v65, v62, v63
	ds_write_b64 v186, v[64:65] offset:1088
	s_waitcnt vmcnt(20)
	v_pk_fma_f32 v[50:51], v[238:239], v[50:51], 0 op_sel_hi:[0,1,0] neg_lo:[1,0,0] neg_hi:[1,0,0]
	v_pk_fma_f32 v[52:53], v[238:239], v[52:53], 0 op_sel_hi:[0,1,0] neg_lo:[1,0,0] neg_hi:[1,0,0]
	v_cvt_pk_bf16_f32 v50, v50, v51
	v_cvt_pk_bf16_f32 v51, v52, v53
	ds_write_b64 v186, v[50:51] offset:1632
	s_waitcnt vmcnt(19)
	v_pk_fma_f32 v[34:35], v[240:241], v[34:35], 0 op_sel_hi:[0,1,0] neg_lo:[1,0,0] neg_hi:[1,0,0]
	v_pk_fma_f32 v[36:37], v[240:241], v[36:37], 0 op_sel_hi:[0,1,0] neg_lo:[1,0,0] neg_hi:[1,0,0]
	v_cvt_pk_bf16_f32 v34, v34, v35
	v_cvt_pk_bf16_f32 v35, v36, v37
	ds_write_b64 v186, v[34:35] offset:2176
	s_waitcnt vmcnt(18)
	v_pk_fma_f32 v[22:23], v[242:243], v[22:23], 0 op_sel_hi:[0,1,0] neg_lo:[1,0,0] neg_hi:[1,0,0]
	v_pk_fma_f32 v[24:25], v[242:243], v[24:25], 0 op_sel_hi:[0,1,0] neg_lo:[1,0,0] neg_hi:[1,0,0]
	v_cvt_pk_bf16_f32 v22, v22, v23
	v_cvt_pk_bf16_f32 v23, v24, v25
	ds_write_b64 v186, v[22:23] offset:2720
	s_waitcnt vmcnt(17)
	v_pk_fma_f32 v[14:15], v[244:245], v[14:15], 0 op_sel_hi:[0,1,0] neg_lo:[1,0,0] neg_hi:[1,0,0]
	v_pk_fma_f32 v[16:17], v[244:245], v[16:17], 0 op_sel_hi:[0,1,0] neg_lo:[1,0,0] neg_hi:[1,0,0]
	v_cvt_pk_bf16_f32 v14, v14, v15
	v_cvt_pk_bf16_f32 v15, v16, v17
	ds_write_b64 v186, v[14:15] offset:3264
	s_waitcnt vmcnt(16)
	v_pk_fma_f32 v[6:7], v[246:247], v[6:7], 0 op_sel_hi:[0,1,0] neg_lo:[1,0,0] neg_hi:[1,0,0]
	v_pk_fma_f32 v[8:9], v[246:247], v[8:9], 0 op_sel_hi:[0,1,0] neg_lo:[1,0,0] neg_hi:[1,0,0]
	v_cvt_pk_bf16_f32 v6, v6, v7
	v_cvt_pk_bf16_f32 v7, v8, v9
	ds_write_b64 v186, v[6:7] offset:3808
	ds_read_b32 v232, v187 offset:128
	ds_read_b32 v234, v187 offset:136
	ds_read_b32 v236, v187 offset:144
	ds_read_b32 v238, v187 offset:152
	ds_read_b32 v240, v187 offset:160
	ds_read_b32 v242, v187 offset:168
	ds_read_b32 v244, v187 offset:176
	ds_read_b32 v246, v187 offset:184
	ds_read_b128 a[64:67], v1
	ds_read_b128 a[68:71], v1 offset:64
	ds_read_b128 a[72:75], v1 offset:128
	ds_read_b128 a[76:79], v1 offset:192
	v_lshl_add_u64 v[6:7], v[150:151], 0, s[26:27]
	v_lshl_add_u64 v[8:9], v[152:153], 0, s[26:27]
	v_lshl_add_u64 v[14:15], v[156:157], 0, s[26:27]
	v_lshl_add_u64 v[16:17], v[158:159], 0, s[26:27]
	v_lshl_add_u64 v[22:23], v[160:161], 0, s[26:27]
	v_lshl_add_u64 v[24:25], v[162:163], 0, s[26:27]
	v_lshl_add_u64 v[70:71], v[164:165], 0, s[26:27]
	v_lshl_add_u64 v[72:73], v[166:167], 0, s[26:27]
	global_load_dwordx4 v[110:113], v[6:7], off nt
	global_load_dwordx4 v[98:101], v[8:9], off nt
	global_load_dwordx4 v[62:65], v[14:15], off nt
	global_load_dwordx4 v[50:53], v[16:17], off nt
	global_load_dwordx4 v[34:37], v[22:23], off nt
	s_nop 0
	global_load_dwordx4 v[22:25], v[24:25], off nt
	s_nop 0
	global_load_dwordx4 v[14:17], v[70:71], off nt
	global_load_dwordx4 v[6:9], v[72:73], off nt
	s_waitcnt lgkmcnt(0)
	s_waitcnt vmcnt(23)
	v_pk_fma_f32 v[72:73], v[232:233], v[106:107], 0 op_sel_hi:[0,1,0] neg_lo:[1,0,0] neg_hi:[1,0,0]
	v_pk_fma_f32 v[70:71], v[232:233], v[108:109], 0 op_sel_hi:[0,1,0] neg_lo:[1,0,0] neg_hi:[1,0,0]
	v_cvt_pk_bf16_f32 v72, v72, v73
	v_cvt_pk_bf16_f32 v73, v70, v71
	ds_write_b64 v186, v[72:73]
	s_waitcnt vmcnt(22)
	v_pk_fma_f32 v[72:73], v[234:235], v[94:95], 0 op_sel_hi:[0,1,0] neg_lo:[1,0,0] neg_hi:[1,0,0]
	v_pk_fma_f32 v[70:71], v[234:235], v[96:97], 0 op_sel_hi:[0,1,0] neg_lo:[1,0,0] neg_hi:[1,0,0]
	v_cvt_pk_bf16_f32 v72, v72, v73
	v_cvt_pk_bf16_f32 v73, v70, v71
	ds_write_b64 v186, v[72:73] offset:544
	s_waitcnt vmcnt(21)
	v_pk_fma_f32 v[66:67], v[236:237], v[66:67], 0 op_sel_hi:[0,1,0] neg_lo:[1,0,0] neg_hi:[1,0,0]
	v_pk_fma_f32 v[68:69], v[236:237], v[68:69], 0 op_sel_hi:[0,1,0] neg_lo:[1,0,0] neg_hi:[1,0,0]
	v_cvt_pk_bf16_f32 v66, v66, v67
	v_cvt_pk_bf16_f32 v67, v68, v69
	ds_write_b64 v186, v[66:67] offset:1088
	s_waitcnt vmcnt(20)
	v_pk_fma_f32 v[54:55], v[238:239], v[54:55], 0 op_sel_hi:[0,1,0] neg_lo:[1,0,0] neg_hi:[1,0,0]
	v_pk_fma_f32 v[56:57], v[238:239], v[56:57], 0 op_sel_hi:[0,1,0] neg_lo:[1,0,0] neg_hi:[1,0,0]
	v_cvt_pk_bf16_f32 v54, v54, v55
	v_cvt_pk_bf16_f32 v55, v56, v57
	ds_write_b64 v186, v[54:55] offset:1632
	s_waitcnt vmcnt(19)
	v_pk_fma_f32 v[38:39], v[240:241], v[38:39], 0 op_sel_hi:[0,1,0] neg_lo:[1,0,0] neg_hi:[1,0,0]
	v_pk_fma_f32 v[40:41], v[240:241], v[40:41], 0 op_sel_hi:[0,1,0] neg_lo:[1,0,0] neg_hi:[1,0,0]
	v_cvt_pk_bf16_f32 v38, v38, v39
	v_cvt_pk_bf16_f32 v39, v40, v41
	ds_write_b64 v186, v[38:39] offset:2176
	s_waitcnt vmcnt(18)
	v_pk_fma_f32 v[18:19], v[242:243], v[18:19], 0 op_sel_hi:[0,1,0] neg_lo:[1,0,0] neg_hi:[1,0,0]
	v_pk_fma_f32 v[20:21], v[242:243], v[20:21], 0 op_sel_hi:[0,1,0] neg_lo:[1,0,0] neg_hi:[1,0,0]
	v_cvt_pk_bf16_f32 v18, v18, v19
	v_cvt_pk_bf16_f32 v19, v20, v21
	ds_write_b64 v186, v[18:19] offset:2720
	s_waitcnt vmcnt(17)
	v_pk_fma_f32 v[10:11], v[244:245], v[10:11], 0 op_sel_hi:[0,1,0] neg_lo:[1,0,0] neg_hi:[1,0,0]
	v_pk_fma_f32 v[12:13], v[244:245], v[12:13], 0 op_sel_hi:[0,1,0] neg_lo:[1,0,0] neg_hi:[1,0,0]
	v_cvt_pk_bf16_f32 v10, v10, v11
	v_cvt_pk_bf16_f32 v11, v12, v13
	ds_write_b64 v186, v[10:11] offset:3264
	s_waitcnt vmcnt(16)
	v_pk_fma_f32 v[2:3], v[246:247], v[2:3], 0 op_sel_hi:[0,1,0] neg_lo:[1,0,0] neg_hi:[1,0,0]
	v_pk_fma_f32 v[4:5], v[246:247], v[4:5], 0 op_sel_hi:[0,1,0] neg_lo:[1,0,0] neg_hi:[1,0,0]
	v_cvt_pk_bf16_f32 v2, v2, v3
	v_cvt_pk_bf16_f32 v3, v4, v5
	ds_write_b64 v186, v[2:3] offset:3808
	ds_read_b32 v232, v187 offset:0
	ds_read_b32 v234, v187 offset:8
	ds_read_b32 v236, v187 offset:16
	ds_read_b32 v238, v187 offset:24
	ds_read_b32 v240, v187 offset:32
	ds_read_b32 v242, v187 offset:40
	ds_read_b32 v244, v187 offset:48
	ds_read_b32 v246, v187 offset:56
	ds_read_b128 a[80:83], v1
	ds_read_b128 a[84:87], v1 offset:64
	ds_read_b128 a[88:91], v1 offset:128
	ds_read_b128 a[92:95], v1 offset:192
	v_lshl_add_u64 v[2:3], v[168:169], 0, s[26:27]
	v_lshl_add_u64 v[4:5], v[170:171], 0, s[26:27]
	v_lshl_add_u64 v[10:11], v[172:173], 0, s[26:27]
	v_lshl_add_u64 v[12:13], v[174:175], 0, s[26:27]
	v_lshl_add_u64 v[18:19], v[176:177], 0, s[26:27]
	v_lshl_add_u64 v[20:21], v[178:179], 0, s[26:27]
	v_lshl_add_u64 v[66:67], v[180:181], 0, s[26:27]
	v_lshl_add_u64 v[68:69], v[182:183], 0, s[26:27]
	global_load_dwordx4 v[106:109], v[2:3], off nt
	global_load_dwordx4 v[94:97], v[4:5], off nt
	global_load_dwordx4 v[74:77], v[10:11], off nt
	global_load_dwordx4 v[54:57], v[12:13], off nt
	global_load_dwordx4 v[38:41], v[18:19], off nt
	s_nop 0
	global_load_dwordx4 v[18:21], v[20:21], off nt
	s_nop 0
	global_load_dwordx4 v[10:13], v[66:67], off nt
	global_load_dwordx4 v[2:5], v[68:69], off nt
	v_mov_b32_e32 v66, v196
	s_waitcnt lgkmcnt(0)
	s_waitcnt vmcnt(23)
	v_pk_fma_f32 v[68:69], v[232:233], v[86:87], 0 op_sel_hi:[0,1,0] neg_lo:[1,0,0] neg_hi:[1,0,0]
	v_pk_fma_f32 v[66:67], v[232:233], v[88:89], 0 op_sel_hi:[0,1,0] neg_lo:[1,0,0] neg_hi:[1,0,0]
	v_cvt_pk_bf16_f32 v68, v68, v69
	v_cvt_pk_bf16_f32 v69, v66, v67
	ds_write_b64 v186, v[68:69]
	s_waitcnt vmcnt(22)
	v_pk_fma_f32 v[68:69], v[234:235], v[82:83], 0 op_sel_hi:[0,1,0] neg_lo:[1,0,0] neg_hi:[1,0,0]
	v_pk_fma_f32 v[66:67], v[234:235], v[84:85], 0 op_sel_hi:[0,1,0] neg_lo:[1,0,0] neg_hi:[1,0,0]
	v_cvt_pk_bf16_f32 v68, v68, v69
	v_cvt_pk_bf16_f32 v69, v66, v67
	ds_write_b64 v186, v[68:69] offset:544
	s_waitcnt vmcnt(21)
	v_pk_fma_f32 v[68:69], v[236:237], v[78:79], 0 op_sel_hi:[0,1,0] neg_lo:[1,0,0] neg_hi:[1,0,0]
	v_pk_fma_f32 v[66:67], v[236:237], v[80:81], 0 op_sel_hi:[0,1,0] neg_lo:[1,0,0] neg_hi:[1,0,0]
	v_cvt_pk_bf16_f32 v68, v68, v69
	v_cvt_pk_bf16_f32 v69, v66, v67
	ds_write_b64 v186, v[68:69] offset:1088
	s_waitcnt vmcnt(20)
	v_pk_fma_f32 v[58:59], v[238:239], v[58:59], 0 op_sel_hi:[0,1,0] neg_lo:[1,0,0] neg_hi:[1,0,0]
	v_pk_fma_f32 v[60:61], v[238:239], v[60:61], 0 op_sel_hi:[0,1,0] neg_lo:[1,0,0] neg_hi:[1,0,0]
	v_cvt_pk_bf16_f32 v58, v58, v59
	v_cvt_pk_bf16_f32 v59, v60, v61
	ds_write_b64 v186, v[58:59] offset:1632
	s_waitcnt vmcnt(19)
	v_pk_fma_f32 v[46:47], v[240:241], v[46:47], 0 op_sel_hi:[0,1,0] neg_lo:[1,0,0] neg_hi:[1,0,0]
	v_pk_fma_f32 v[48:49], v[240:241], v[48:49], 0 op_sel_hi:[0,1,0] neg_lo:[1,0,0] neg_hi:[1,0,0]
	v_cvt_pk_bf16_f32 v46, v46, v47
	v_cvt_pk_bf16_f32 v47, v48, v49
	ds_write_b64 v186, v[46:47] offset:2176
	s_waitcnt vmcnt(18)
	v_pk_fma_f32 v[42:43], v[242:243], v[42:43], 0 op_sel_hi:[0,1,0] neg_lo:[1,0,0] neg_hi:[1,0,0]
	v_pk_fma_f32 v[44:45], v[242:243], v[44:45], 0 op_sel_hi:[0,1,0] neg_lo:[1,0,0] neg_hi:[1,0,0]
	v_cvt_pk_bf16_f32 v42, v42, v43
	v_cvt_pk_bf16_f32 v43, v44, v45
	ds_write_b64 v186, v[42:43] offset:2720
	s_waitcnt vmcnt(17)
	v_pk_fma_f32 v[30:31], v[244:245], v[30:31], 0 op_sel_hi:[0,1,0] neg_lo:[1,0,0] neg_hi:[1,0,0]
	v_pk_fma_f32 v[32:33], v[244:245], v[32:33], 0 op_sel_hi:[0,1,0] neg_lo:[1,0,0] neg_hi:[1,0,0]
	v_cvt_pk_bf16_f32 v30, v30, v31
	v_cvt_pk_bf16_f32 v31, v32, v33
	ds_write_b64 v186, v[30:31] offset:3264
	s_waitcnt vmcnt(16)
	v_pk_fma_f32 v[26:27], v[246:247], v[26:27], 0 op_sel_hi:[0,1,0] neg_lo:[1,0,0] neg_hi:[1,0,0]
	v_pk_fma_f32 v[28:29], v[246:247], v[28:29], 0 op_sel_hi:[0,1,0] neg_lo:[1,0,0] neg_hi:[1,0,0]
	v_cvt_pk_bf16_f32 v26, v26, v27
	v_cvt_pk_bf16_f32 v27, v28, v29
	ds_write_b64 v186, v[26:27] offset:3808
	ds_read_b32 v232, v187 offset:64
	ds_read_b32 v234, v187 offset:72
	ds_read_b32 v236, v187 offset:80
	ds_read_b32 v238, v187 offset:88
	ds_read_b32 v240, v187 offset:96
	ds_read_b32 v242, v187 offset:104
	ds_read_b32 v244, v187 offset:112
	ds_read_b32 v246, v187 offset:120
	ds_read_b128 a[96:99], v1
	ds_read_b128 a[100:103], v1 offset:64
	ds_read_b128 a[104:107], v1 offset:128
	ds_read_b128 a[108:111], v1 offset:192
	v_lshl_add_u64 v[26:27], v[130:131], 0, s[24:25]
	v_add_co_u32_e32 v28, vcc, s7, v26
	s_nop 1
	v_addc_co_u32_e32 v29, vcc, 0, v27, vcc
	global_load_dwordx4 v[102:105], v[26:27], off nt
	global_load_dwordx4 v[90:93], v[28:29], off nt
	v_add_co_u32_e32 v28, vcc, s36, v26
	s_nop 1
	v_addc_co_u32_e32 v29, vcc, 0, v27, vcc
	v_add_co_u32_e32 v30, vcc, s37, v26
	s_nop 1
	v_addc_co_u32_e32 v31, vcc, 0, v27, vcc
	global_load_dwordx4 v[86:89], v[28:29], off nt
	global_load_dwordx4 v[70:73], v[30:31], off nt
	v_add_co_u32_e32 v28, vcc, s38, v26
	s_nop 1
	v_addc_co_u32_e32 v29, vcc, 0, v27, vcc
	v_add_co_u32_e32 v30, vcc, s39, v26
	s_nop 1
	v_addc_co_u32_e32 v31, vcc, 0, v27, vcc
	global_load_dwordx4 v[66:69], v[28:29], off nt
	global_load_dwordx4 v[46:49], v[30:31], off nt
	v_add_co_u32_e32 v28, vcc, s41, v26
	s_nop 1
	v_addc_co_u32_e32 v29, vcc, 0, v27, vcc
	v_add_co_u32_e32 v26, vcc, s42, v26
	s_nop 1
	v_addc_co_u32_e32 v27, vcc, 0, v27, vcc
	global_load_dwordx4 v[42:45], v[28:29], off nt
	global_load_dwordx4 v[30:33], v[26:27], off nt
	v_mov_b32_e32 v26, v196
	s_waitcnt lgkmcnt(0)
	s_waitcnt vmcnt(23)
	v_pk_fma_f32 v[28:29], v[232:233], v[110:111], 0 op_sel_hi:[0,1,0] neg_lo:[1,0,0] neg_hi:[1,0,0]
	v_pk_fma_f32 v[26:27], v[232:233], v[112:113], 0 op_sel_hi:[0,1,0] neg_lo:[1,0,0] neg_hi:[1,0,0]
	v_cvt_pk_bf16_f32 v28, v28, v29
	v_cvt_pk_bf16_f32 v29, v26, v27
	ds_write_b64 v186, v[28:29]
	s_waitcnt vmcnt(22)
	v_pk_fma_f32 v[28:29], v[234:235], v[98:99], 0 op_sel_hi:[0,1,0] neg_lo:[1,0,0] neg_hi:[1,0,0]
	v_pk_fma_f32 v[26:27], v[234:235], v[100:101], 0 op_sel_hi:[0,1,0] neg_lo:[1,0,0] neg_hi:[1,0,0]
	v_cvt_pk_bf16_f32 v28, v28, v29
	v_cvt_pk_bf16_f32 v29, v26, v27
	ds_write_b64 v186, v[28:29] offset:544
	s_waitcnt vmcnt(21)
	v_pk_fma_f32 v[28:29], v[236:237], v[62:63], 0 op_sel_hi:[0,1,0] neg_lo:[1,0,0] neg_hi:[1,0,0]
	v_pk_fma_f32 v[26:27], v[236:237], v[64:65], 0 op_sel_hi:[0,1,0] neg_lo:[1,0,0] neg_hi:[1,0,0]
	v_cvt_pk_bf16_f32 v28, v28, v29
	v_cvt_pk_bf16_f32 v29, v26, v27
	ds_write_b64 v186, v[28:29] offset:1088
	s_waitcnt vmcnt(20)
	v_pk_fma_f32 v[28:29], v[238:239], v[50:51], 0 op_sel_hi:[0,1,0] neg_lo:[1,0,0] neg_hi:[1,0,0]
	v_pk_fma_f32 v[26:27], v[238:239], v[52:53], 0 op_sel_hi:[0,1,0] neg_lo:[1,0,0] neg_hi:[1,0,0]
	v_cvt_pk_bf16_f32 v28, v28, v29
	v_cvt_pk_bf16_f32 v29, v26, v27
	ds_write_b64 v186, v[28:29] offset:1632
	s_waitcnt vmcnt(19)
	v_pk_fma_f32 v[28:29], v[240:241], v[34:35], 0 op_sel_hi:[0,1,0] neg_lo:[1,0,0] neg_hi:[1,0,0]
	v_pk_fma_f32 v[26:27], v[240:241], v[36:37], 0 op_sel_hi:[0,1,0] neg_lo:[1,0,0] neg_hi:[1,0,0]
	v_cvt_pk_bf16_f32 v28, v28, v29
	v_cvt_pk_bf16_f32 v29, v26, v27
	ds_write_b64 v186, v[28:29] offset:2176
	s_waitcnt vmcnt(18)
	v_pk_fma_f32 v[22:23], v[242:243], v[22:23], 0 op_sel_hi:[0,1,0] neg_lo:[1,0,0] neg_hi:[1,0,0]
	v_pk_fma_f32 v[24:25], v[242:243], v[24:25], 0 op_sel_hi:[0,1,0] neg_lo:[1,0,0] neg_hi:[1,0,0]
	v_cvt_pk_bf16_f32 v22, v22, v23
	v_cvt_pk_bf16_f32 v23, v24, v25
	ds_write_b64 v186, v[22:23] offset:2720
	s_waitcnt vmcnt(17)
	v_pk_fma_f32 v[14:15], v[244:245], v[14:15], 0 op_sel_hi:[0,1,0] neg_lo:[1,0,0] neg_hi:[1,0,0]
	v_pk_fma_f32 v[16:17], v[244:245], v[16:17], 0 op_sel_hi:[0,1,0] neg_lo:[1,0,0] neg_hi:[1,0,0]
	v_cvt_pk_bf16_f32 v14, v14, v15
	v_cvt_pk_bf16_f32 v15, v16, v17
	ds_write_b64 v186, v[14:15] offset:3264
	s_waitcnt vmcnt(16)
	v_pk_fma_f32 v[6:7], v[246:247], v[6:7], 0 op_sel_hi:[0,1,0] neg_lo:[1,0,0] neg_hi:[1,0,0]
	v_pk_fma_f32 v[8:9], v[246:247], v[8:9], 0 op_sel_hi:[0,1,0] neg_lo:[1,0,0] neg_hi:[1,0,0]
	v_cvt_pk_bf16_f32 v6, v6, v7
	v_cvt_pk_bf16_f32 v7, v8, v9
	ds_write_b64 v186, v[6:7] offset:3808
	ds_read_b32 v232, v187 offset:128
	ds_read_b32 v234, v187 offset:136
	ds_read_b32 v236, v187 offset:144
	ds_read_b32 v238, v187 offset:152
	ds_read_b32 v240, v187 offset:160
	ds_read_b32 v242, v187 offset:168
	ds_read_b32 v244, v187 offset:176
	ds_read_b32 v246, v187 offset:184
	ds_read_b128 a[112:115], v1
	ds_read_b128 a[116:119], v1 offset:64
	ds_read_b128 a[120:123], v1 offset:128
	ds_read_b128 a[124:127], v1 offset:192
	v_lshl_add_u64 v[6:7], v[150:151], 0, s[24:25]
	v_lshl_add_u64 v[8:9], v[152:153], 0, s[24:25]
	v_lshl_add_u64 v[14:15], v[156:157], 0, s[24:25]
	v_lshl_add_u64 v[16:17], v[158:159], 0, s[24:25]
	v_lshl_add_u64 v[22:23], v[160:161], 0, s[24:25]
	v_lshl_add_u64 v[24:25], v[162:163], 0, s[24:25]
	v_lshl_add_u64 v[26:27], v[164:165], 0, s[24:25]
	v_lshl_add_u64 v[28:29], v[166:167], 0, s[24:25]
	global_load_dwordx4 v[110:113], v[6:7], off nt
	global_load_dwordx4 v[98:101], v[8:9], off nt
	global_load_dwordx4 v[78:81], v[14:15], off nt
	global_load_dwordx4 v[58:61], v[16:17], off nt
	global_load_dwordx4 v[34:37], v[22:23], off nt
	s_nop 0
	global_load_dwordx4 v[22:25], v[24:25], off nt
	s_nop 0
	global_load_dwordx4 v[14:17], v[26:27], off nt
	global_load_dwordx4 v[6:9], v[28:29], off nt
	s_waitcnt lgkmcnt(0)
	s_waitcnt vmcnt(23)
	v_pk_fma_f32 v[28:29], v[232:233], v[106:107], 0 op_sel_hi:[0,1,0] neg_lo:[1,0,0] neg_hi:[1,0,0]
	v_pk_fma_f32 v[26:27], v[232:233], v[108:109], 0 op_sel_hi:[0,1,0] neg_lo:[1,0,0] neg_hi:[1,0,0]
	v_cvt_pk_bf16_f32 v28, v28, v29
	v_cvt_pk_bf16_f32 v29, v26, v27
	ds_write_b64 v186, v[28:29]
	s_waitcnt vmcnt(22)
	v_pk_fma_f32 v[28:29], v[234:235], v[94:95], 0 op_sel_hi:[0,1,0] neg_lo:[1,0,0] neg_hi:[1,0,0]
	v_pk_fma_f32 v[26:27], v[234:235], v[96:97], 0 op_sel_hi:[0,1,0] neg_lo:[1,0,0] neg_hi:[1,0,0]
	v_cvt_pk_bf16_f32 v28, v28, v29
	v_cvt_pk_bf16_f32 v29, v26, v27
	ds_write_b64 v186, v[28:29] offset:544
	s_waitcnt vmcnt(21)
	v_pk_fma_f32 v[28:29], v[236:237], v[74:75], 0 op_sel_hi:[0,1,0] neg_lo:[1,0,0] neg_hi:[1,0,0]
	v_pk_fma_f32 v[26:27], v[236:237], v[76:77], 0 op_sel_hi:[0,1,0] neg_lo:[1,0,0] neg_hi:[1,0,0]
	v_cvt_pk_bf16_f32 v28, v28, v29
	v_cvt_pk_bf16_f32 v29, v26, v27
	ds_write_b64 v186, v[28:29] offset:1088
	s_waitcnt vmcnt(20)
	v_pk_fma_f32 v[28:29], v[238:239], v[54:55], 0 op_sel_hi:[0,1,0] neg_lo:[1,0,0] neg_hi:[1,0,0]
	v_pk_fma_f32 v[26:27], v[238:239], v[56:57], 0 op_sel_hi:[0,1,0] neg_lo:[1,0,0] neg_hi:[1,0,0]
	v_cvt_pk_bf16_f32 v28, v28, v29
	v_cvt_pk_bf16_f32 v29, v26, v27
	ds_write_b64 v186, v[28:29] offset:1632
	s_waitcnt vmcnt(19)
	v_pk_fma_f32 v[28:29], v[240:241], v[38:39], 0 op_sel_hi:[0,1,0] neg_lo:[1,0,0] neg_hi:[1,0,0]
	v_pk_fma_f32 v[26:27], v[240:241], v[40:41], 0 op_sel_hi:[0,1,0] neg_lo:[1,0,0] neg_hi:[1,0,0]
	v_cvt_pk_bf16_f32 v28, v28, v29
	v_cvt_pk_bf16_f32 v29, v26, v27
	ds_write_b64 v186, v[28:29] offset:2176
	s_waitcnt vmcnt(18)
	v_pk_fma_f32 v[18:19], v[242:243], v[18:19], 0 op_sel_hi:[0,1,0] neg_lo:[1,0,0] neg_hi:[1,0,0]
	v_pk_fma_f32 v[20:21], v[242:243], v[20:21], 0 op_sel_hi:[0,1,0] neg_lo:[1,0,0] neg_hi:[1,0,0]
	v_cvt_pk_bf16_f32 v18, v18, v19
	v_cvt_pk_bf16_f32 v19, v20, v21
	ds_write_b64 v186, v[18:19] offset:2720
	s_waitcnt vmcnt(17)
	v_pk_fma_f32 v[10:11], v[244:245], v[10:11], 0 op_sel_hi:[0,1,0] neg_lo:[1,0,0] neg_hi:[1,0,0]
	v_pk_fma_f32 v[12:13], v[244:245], v[12:13], 0 op_sel_hi:[0,1,0] neg_lo:[1,0,0] neg_hi:[1,0,0]
	v_cvt_pk_bf16_f32 v10, v10, v11
	v_cvt_pk_bf16_f32 v11, v12, v13
	ds_write_b64 v186, v[10:11] offset:3264
	s_waitcnt vmcnt(16)
	v_pk_fma_f32 v[2:3], v[246:247], v[2:3], 0 op_sel_hi:[0,1,0] neg_lo:[1,0,0] neg_hi:[1,0,0]
	v_pk_fma_f32 v[4:5], v[246:247], v[4:5], 0 op_sel_hi:[0,1,0] neg_lo:[1,0,0] neg_hi:[1,0,0]
	v_cvt_pk_bf16_f32 v2, v2, v3
	v_cvt_pk_bf16_f32 v3, v4, v5
	ds_write_b64 v186, v[2:3] offset:3808
	ds_read_b32 v232, v187 offset:0
	ds_read_b32 v234, v187 offset:8
	ds_read_b32 v236, v187 offset:16
	ds_read_b32 v238, v187 offset:24
	ds_read_b32 v240, v187 offset:32
	ds_read_b32 v242, v187 offset:40
	ds_read_b32 v244, v187 offset:48
	ds_read_b32 v246, v187 offset:56
	ds_read_b128 a[128:131], v1
	ds_read_b128 a[132:135], v1 offset:64
	ds_read_b128 a[136:139], v1 offset:128
	ds_read_b128 a[140:143], v1 offset:192
	v_lshl_add_u64 v[2:3], v[168:169], 0, s[24:25]
	v_lshl_add_u64 v[4:5], v[170:171], 0, s[24:25]
	v_lshl_add_u64 v[10:11], v[172:173], 0, s[24:25]
	v_lshl_add_u64 v[12:13], v[174:175], 0, s[24:25]
	v_lshl_add_u64 v[18:19], v[176:177], 0, s[24:25]
	v_lshl_add_u64 v[20:21], v[178:179], 0, s[24:25]
	v_lshl_add_u64 v[50:51], v[180:181], 0, s[24:25]
	v_lshl_add_u64 v[52:53], v[182:183], 0, s[24:25]
	global_load_dwordx4 v[114:117], v[2:3], off nt
	global_load_dwordx4 v[94:97], v[4:5], off nt
	global_load_dwordx4 v[82:85], v[10:11], off nt
	global_load_dwordx4 v[62:65], v[12:13], off nt
	global_load_dwordx4 v[38:41], v[18:19], off nt
	global_load_dwordx4 v[26:29], v[20:21], off nt
	s_nop 0
	global_load_dwordx4 v[10:13], v[50:51], off nt
	global_load_dwordx4 v[2:5], v[52:53], off nt
	v_mov_b32_e32 v18, v195
	s_waitcnt lgkmcnt(0)
	s_waitcnt vmcnt(23)
	v_pk_fma_f32 v[20:21], v[232:233], v[102:103], 0 op_sel_hi:[0,1,0] neg_lo:[1,0,0] neg_hi:[1,0,0]
	v_pk_fma_f32 v[18:19], v[232:233], v[104:105], 0 op_sel_hi:[0,1,0] neg_lo:[1,0,0] neg_hi:[1,0,0]
	v_cvt_pk_bf16_f32 v20, v20, v21
	v_cvt_pk_bf16_f32 v21, v18, v19
	ds_write_b64 v186, v[20:21]
	s_waitcnt vmcnt(22)
	v_pk_fma_f32 v[20:21], v[234:235], v[90:91], 0 op_sel_hi:[0,1,0] neg_lo:[1,0,0] neg_hi:[1,0,0]
	v_pk_fma_f32 v[18:19], v[234:235], v[92:93], 0 op_sel_hi:[0,1,0] neg_lo:[1,0,0] neg_hi:[1,0,0]
	v_cvt_pk_bf16_f32 v20, v20, v21
	v_cvt_pk_bf16_f32 v21, v18, v19
	ds_write_b64 v186, v[20:21] offset:544
	s_waitcnt vmcnt(21)
	v_pk_fma_f32 v[20:21], v[236:237], v[86:87], 0 op_sel_hi:[0,1,0] neg_lo:[1,0,0] neg_hi:[1,0,0]
	v_pk_fma_f32 v[18:19], v[236:237], v[88:89], 0 op_sel_hi:[0,1,0] neg_lo:[1,0,0] neg_hi:[1,0,0]
	v_cvt_pk_bf16_f32 v20, v20, v21
	v_cvt_pk_bf16_f32 v21, v18, v19
	ds_write_b64 v186, v[20:21] offset:1088
	s_waitcnt vmcnt(20)
	v_pk_fma_f32 v[20:21], v[238:239], v[70:71], 0 op_sel_hi:[0,1,0] neg_lo:[1,0,0] neg_hi:[1,0,0]
	v_pk_fma_f32 v[18:19], v[238:239], v[72:73], 0 op_sel_hi:[0,1,0] neg_lo:[1,0,0] neg_hi:[1,0,0]
	v_cvt_pk_bf16_f32 v20, v20, v21
	v_cvt_pk_bf16_f32 v21, v18, v19
	ds_write_b64 v186, v[20:21] offset:1632
	s_waitcnt vmcnt(19)
	v_pk_fma_f32 v[20:21], v[240:241], v[66:67], 0 op_sel_hi:[0,1,0] neg_lo:[1,0,0] neg_hi:[1,0,0]
	v_pk_fma_f32 v[18:19], v[240:241], v[68:69], 0 op_sel_hi:[0,1,0] neg_lo:[1,0,0] neg_hi:[1,0,0]
	v_cvt_pk_bf16_f32 v20, v20, v21
	v_cvt_pk_bf16_f32 v21, v18, v19
	ds_write_b64 v186, v[20:21] offset:2176
	s_waitcnt vmcnt(18)
	v_pk_fma_f32 v[20:21], v[242:243], v[46:47], 0 op_sel_hi:[0,1,0] neg_lo:[1,0,0] neg_hi:[1,0,0]
	v_pk_fma_f32 v[18:19], v[242:243], v[48:49], 0 op_sel_hi:[0,1,0] neg_lo:[1,0,0] neg_hi:[1,0,0]
	v_cvt_pk_bf16_f32 v20, v20, v21
	v_cvt_pk_bf16_f32 v21, v18, v19
	ds_write_b64 v186, v[20:21] offset:2720
	s_waitcnt vmcnt(17)
	v_pk_fma_f32 v[20:21], v[244:245], v[42:43], 0 op_sel_hi:[0,1,0] neg_lo:[1,0,0] neg_hi:[1,0,0]
	v_pk_fma_f32 v[18:19], v[244:245], v[44:45], 0 op_sel_hi:[0,1,0] neg_lo:[1,0,0] neg_hi:[1,0,0]
	v_cvt_pk_bf16_f32 v20, v20, v21
	v_cvt_pk_bf16_f32 v21, v18, v19
	ds_write_b64 v186, v[20:21] offset:3264
	s_waitcnt vmcnt(16)
	v_pk_fma_f32 v[20:21], v[246:247], v[30:31], 0 op_sel_hi:[0,1,0] neg_lo:[1,0,0] neg_hi:[1,0,0]
	v_pk_fma_f32 v[18:19], v[246:247], v[32:33], 0 op_sel_hi:[0,1,0] neg_lo:[1,0,0] neg_hi:[1,0,0]
	v_cvt_pk_bf16_f32 v20, v20, v21
	v_cvt_pk_bf16_f32 v21, v18, v19
	ds_write_b64 v186, v[20:21] offset:3808
	ds_read_b32 v232, v187 offset:64
	ds_read_b32 v234, v187 offset:72
	ds_read_b32 v236, v187 offset:80
	ds_read_b32 v238, v187 offset:88
	ds_read_b32 v240, v187 offset:96
	ds_read_b32 v242, v187 offset:104
	ds_read_b32 v244, v187 offset:112
	ds_read_b32 v246, v187 offset:120
	ds_read_b128 a[144:147], v1
	ds_read_b128 a[148:151], v1 offset:64
	ds_read_b128 a[152:155], v1 offset:128
	ds_read_b128 a[156:159], v1 offset:192
	v_lshl_add_u64 v[18:19], v[130:131], 0, s[22:23]
	v_add_co_u32_e32 v20, vcc, s7, v18
	s_nop 1
	v_addc_co_u32_e32 v21, vcc, 0, v19, vcc
	global_load_dwordx4 v[106:109], v[18:19], off nt
	global_load_dwordx4 v[90:93], v[20:21], off nt
	v_add_co_u32_e32 v20, vcc, s36, v18
	s_nop 1
	v_addc_co_u32_e32 v21, vcc, 0, v19, vcc
	v_add_co_u32_e32 v30, vcc, s37, v18
	s_nop 1
	v_addc_co_u32_e32 v31, vcc, 0, v19, vcc
	global_load_dwordx4 v[86:89], v[20:21], off nt
	global_load_dwordx4 v[74:77], v[30:31], off nt
	v_add_co_u32_e32 v20, vcc, s38, v18
	s_nop 1
	v_addc_co_u32_e32 v21, vcc, 0, v19, vcc
	v_add_co_u32_e32 v30, vcc, s39, v18
	s_nop 1
	v_addc_co_u32_e32 v31, vcc, 0, v19, vcc
	global_load_dwordx4 v[70:73], v[20:21], off nt
	global_load_dwordx4 v[54:57], v[30:31], off nt
	v_add_co_u32_e32 v20, vcc, s41, v18
	s_nop 1
	v_addc_co_u32_e32 v21, vcc, 0, v19, vcc
	v_add_co_u32_e32 v18, vcc, s42, v18
	s_nop 1
	v_addc_co_u32_e32 v19, vcc, 0, v19, vcc
	global_load_dwordx4 v[50:53], v[20:21], off nt
	global_load_dwordx4 v[46:49], v[18:19], off nt
	v_mov_b32_e32 v18, v195
	s_waitcnt lgkmcnt(0)
	s_waitcnt vmcnt(23)
	v_pk_fma_f32 v[20:21], v[232:233], v[110:111], 0 op_sel_hi:[0,1,0] neg_lo:[1,0,0] neg_hi:[1,0,0]
	v_pk_fma_f32 v[18:19], v[232:233], v[112:113], 0 op_sel_hi:[0,1,0] neg_lo:[1,0,0] neg_hi:[1,0,0]
	v_cvt_pk_bf16_f32 v20, v20, v21
	v_cvt_pk_bf16_f32 v21, v18, v19
	ds_write_b64 v186, v[20:21]
	s_waitcnt vmcnt(22)
	v_pk_fma_f32 v[20:21], v[234:235], v[98:99], 0 op_sel_hi:[0,1,0] neg_lo:[1,0,0] neg_hi:[1,0,0]
	v_pk_fma_f32 v[18:19], v[234:235], v[100:101], 0 op_sel_hi:[0,1,0] neg_lo:[1,0,0] neg_hi:[1,0,0]
	v_cvt_pk_bf16_f32 v20, v20, v21
	v_cvt_pk_bf16_f32 v21, v18, v19
	ds_write_b64 v186, v[20:21] offset:544
	s_waitcnt vmcnt(21)
	v_pk_fma_f32 v[20:21], v[236:237], v[78:79], 0 op_sel_hi:[0,1,0] neg_lo:[1,0,0] neg_hi:[1,0,0]
	v_pk_fma_f32 v[18:19], v[236:237], v[80:81], 0 op_sel_hi:[0,1,0] neg_lo:[1,0,0] neg_hi:[1,0,0]
	v_cvt_pk_bf16_f32 v20, v20, v21
	v_cvt_pk_bf16_f32 v21, v18, v19
	ds_write_b64 v186, v[20:21] offset:1088
	s_waitcnt vmcnt(20)
	v_pk_fma_f32 v[20:21], v[238:239], v[58:59], 0 op_sel_hi:[0,1,0] neg_lo:[1,0,0] neg_hi:[1,0,0]
	v_pk_fma_f32 v[18:19], v[238:239], v[60:61], 0 op_sel_hi:[0,1,0] neg_lo:[1,0,0] neg_hi:[1,0,0]
	v_cvt_pk_bf16_f32 v20, v20, v21
	v_cvt_pk_bf16_f32 v21, v18, v19
	ds_write_b64 v186, v[20:21] offset:1632
	s_waitcnt vmcnt(19)
	v_pk_fma_f32 v[20:21], v[240:241], v[34:35], 0 op_sel_hi:[0,1,0] neg_lo:[1,0,0] neg_hi:[1,0,0]
	v_pk_fma_f32 v[18:19], v[240:241], v[36:37], 0 op_sel_hi:[0,1,0] neg_lo:[1,0,0] neg_hi:[1,0,0]
	v_cvt_pk_bf16_f32 v20, v20, v21
	v_cvt_pk_bf16_f32 v21, v18, v19
	ds_write_b64 v186, v[20:21] offset:2176
	s_waitcnt vmcnt(18)
	v_pk_fma_f32 v[20:21], v[242:243], v[22:23], 0 op_sel_hi:[0,1,0] neg_lo:[1,0,0] neg_hi:[1,0,0]
	v_pk_fma_f32 v[18:19], v[242:243], v[24:25], 0 op_sel_hi:[0,1,0] neg_lo:[1,0,0] neg_hi:[1,0,0]
	v_cvt_pk_bf16_f32 v20, v20, v21
	v_cvt_pk_bf16_f32 v21, v18, v19
	ds_write_b64 v186, v[20:21] offset:2720
	s_waitcnt vmcnt(17)
	v_pk_fma_f32 v[14:15], v[244:245], v[14:15], 0 op_sel_hi:[0,1,0] neg_lo:[1,0,0] neg_hi:[1,0,0]
	v_pk_fma_f32 v[16:17], v[244:245], v[16:17], 0 op_sel_hi:[0,1,0] neg_lo:[1,0,0] neg_hi:[1,0,0]
	v_cvt_pk_bf16_f32 v14, v14, v15
	v_cvt_pk_bf16_f32 v15, v16, v17
	ds_write_b64 v186, v[14:15] offset:3264
	s_waitcnt vmcnt(16)
	v_pk_fma_f32 v[6:7], v[246:247], v[6:7], 0 op_sel_hi:[0,1,0] neg_lo:[1,0,0] neg_hi:[1,0,0]
	v_pk_fma_f32 v[8:9], v[246:247], v[8:9], 0 op_sel_hi:[0,1,0] neg_lo:[1,0,0] neg_hi:[1,0,0]
	v_cvt_pk_bf16_f32 v6, v6, v7
	v_cvt_pk_bf16_f32 v7, v8, v9
	ds_write_b64 v186, v[6:7] offset:3808
	ds_read_b32 v232, v187 offset:128
	ds_read_b32 v234, v187 offset:136
	ds_read_b32 v236, v187 offset:144
	ds_read_b32 v238, v187 offset:152
	ds_read_b32 v240, v187 offset:160
	ds_read_b32 v242, v187 offset:168
	ds_read_b32 v244, v187 offset:176
	ds_read_b32 v246, v187 offset:184
	ds_read_b128 a[160:163], v1
	ds_read_b128 a[164:167], v1 offset:64
	ds_read_b128 a[168:171], v1 offset:128
	ds_read_b128 a[172:175], v1 offset:192
	v_lshl_add_u64 v[6:7], v[150:151], 0, s[22:23]
	v_lshl_add_u64 v[18:19], v[160:161], 0, s[22:23]
	v_lshl_add_u64 v[20:21], v[162:163], 0, s[22:23]
	v_lshl_add_u64 v[22:23], v[164:165], 0, s[22:23]
	v_lshl_add_u64 v[8:9], v[152:153], 0, s[22:23]
	v_lshl_add_u64 v[14:15], v[156:157], 0, s[22:23]
	v_lshl_add_u64 v[16:17], v[158:159], 0, s[22:23]
	v_lshl_add_u64 v[34:35], v[166:167], 0, s[22:23]
	global_load_dwordx4 v[110:113], v[6:7], off nt
	global_load_dwordx4 v[98:101], v[8:9], off nt
	global_load_dwordx4 v[78:81], v[14:15], off nt
	global_load_dwordx4 v[66:69], v[16:17], off nt
	global_load_dwordx4 v[58:61], v[18:19], off nt
	global_load_dwordx4 v[30:33], v[20:21], off nt
	s_nop 0
	global_load_dwordx4 v[22:25], v[22:23], off nt
	s_nop 0
	global_load_dwordx4 v[18:21], v[34:35], off nt
	s_waitcnt lgkmcnt(0)
	s_waitcnt vmcnt(23)
	v_pk_fma_f32 v[8:9], v[232:233], v[114:115], 0 op_sel_hi:[0,1,0] neg_lo:[1,0,0] neg_hi:[1,0,0]
	v_pk_fma_f32 v[6:7], v[232:233], v[116:117], 0 op_sel_hi:[0,1,0] neg_lo:[1,0,0] neg_hi:[1,0,0]
	v_cvt_pk_bf16_f32 v8, v8, v9
	v_cvt_pk_bf16_f32 v9, v6, v7
	ds_write_b64 v186, v[8:9]
	s_waitcnt vmcnt(22)
	v_pk_fma_f32 v[8:9], v[234:235], v[94:95], 0 op_sel_hi:[0,1,0] neg_lo:[1,0,0] neg_hi:[1,0,0]
	v_pk_fma_f32 v[6:7], v[234:235], v[96:97], 0 op_sel_hi:[0,1,0] neg_lo:[1,0,0] neg_hi:[1,0,0]
	v_cvt_pk_bf16_f32 v8, v8, v9
	v_cvt_pk_bf16_f32 v9, v6, v7
	ds_write_b64 v186, v[8:9] offset:544
	s_waitcnt vmcnt(21)
	v_pk_fma_f32 v[8:9], v[236:237], v[82:83], 0 op_sel_hi:[0,1,0] neg_lo:[1,0,0] neg_hi:[1,0,0]
	v_pk_fma_f32 v[6:7], v[236:237], v[84:85], 0 op_sel_hi:[0,1,0] neg_lo:[1,0,0] neg_hi:[1,0,0]
	v_cvt_pk_bf16_f32 v8, v8, v9
	v_cvt_pk_bf16_f32 v9, v6, v7
	ds_write_b64 v186, v[8:9] offset:1088
	s_waitcnt vmcnt(20)
	v_pk_fma_f32 v[8:9], v[238:239], v[62:63], 0 op_sel_hi:[0,1,0] neg_lo:[1,0,0] neg_hi:[1,0,0]
	v_pk_fma_f32 v[6:7], v[238:239], v[64:65], 0 op_sel_hi:[0,1,0] neg_lo:[1,0,0] neg_hi:[1,0,0]
	v_cvt_pk_bf16_f32 v8, v8, v9
	v_cvt_pk_bf16_f32 v9, v6, v7
	ds_write_b64 v186, v[8:9] offset:1632
	s_waitcnt vmcnt(19)
	v_pk_fma_f32 v[8:9], v[240:241], v[38:39], 0 op_sel_hi:[0,1,0] neg_lo:[1,0,0] neg_hi:[1,0,0]
	v_pk_fma_f32 v[6:7], v[240:241], v[40:41], 0 op_sel_hi:[0,1,0] neg_lo:[1,0,0] neg_hi:[1,0,0]
	v_cvt_pk_bf16_f32 v8, v8, v9
	v_cvt_pk_bf16_f32 v9, v6, v7
	ds_write_b64 v186, v[8:9] offset:2176
	s_waitcnt vmcnt(18)
	v_pk_fma_f32 v[8:9], v[242:243], v[26:27], 0 op_sel_hi:[0,1,0] neg_lo:[1,0,0] neg_hi:[1,0,0]
	v_pk_fma_f32 v[6:7], v[242:243], v[28:29], 0 op_sel_hi:[0,1,0] neg_lo:[1,0,0] neg_hi:[1,0,0]
	v_cvt_pk_bf16_f32 v8, v8, v9
	v_cvt_pk_bf16_f32 v9, v6, v7
	ds_write_b64 v186, v[8:9] offset:2720
	s_waitcnt vmcnt(17)
	v_pk_fma_f32 v[8:9], v[244:245], v[10:11], 0 op_sel_hi:[0,1,0] neg_lo:[1,0,0] neg_hi:[1,0,0]
	v_pk_fma_f32 v[6:7], v[244:245], v[12:13], 0 op_sel_hi:[0,1,0] neg_lo:[1,0,0] neg_hi:[1,0,0]
	v_cvt_pk_bf16_f32 v8, v8, v9
	v_cvt_pk_bf16_f32 v9, v6, v7
	ds_write_b64 v186, v[8:9] offset:3264
	s_waitcnt vmcnt(16)
	v_pk_fma_f32 v[2:3], v[246:247], v[2:3], 0 op_sel_hi:[0,1,0] neg_lo:[1,0,0] neg_hi:[1,0,0]
	v_pk_fma_f32 v[4:5], v[246:247], v[4:5], 0 op_sel_hi:[0,1,0] neg_lo:[1,0,0] neg_hi:[1,0,0]
	v_cvt_pk_bf16_f32 v2, v2, v3
	v_cvt_pk_bf16_f32 v3, v4, v5
	ds_write_b64 v186, v[2:3] offset:3808
	ds_read_b32 v232, v187 offset:0
	ds_read_b32 v234, v187 offset:8
	ds_read_b32 v236, v187 offset:16
	ds_read_b32 v238, v187 offset:24
	ds_read_b32 v240, v187 offset:32
	ds_read_b32 v242, v187 offset:40
	ds_read_b32 v244, v187 offset:48
	ds_read_b32 v246, v187 offset:56
	ds_read_b128 a[176:179], v1
	ds_read_b128 a[180:183], v1 offset:64
	ds_read_b128 a[184:187], v1 offset:128
	ds_read_b128 a[188:191], v1 offset:192
	v_lshl_add_u64 v[2:3], v[168:169], 0, s[22:23]
	v_lshl_add_u64 v[4:5], v[170:171], 0, s[22:23]
	v_lshl_add_u64 v[6:7], v[172:173], 0, s[22:23]
	v_lshl_add_u64 v[8:9], v[174:175], 0, s[22:23]
	v_lshl_add_u64 v[10:11], v[176:177], 0, s[22:23]
	v_lshl_add_u64 v[12:13], v[178:179], 0, s[22:23]
	v_lshl_add_u64 v[14:15], v[180:181], 0, s[22:23]
	v_lshl_add_u64 v[16:17], v[182:183], 0, s[22:23]
	global_load_dwordx4 v[114:117], v[2:3], off nt
	global_load_dwordx4 v[102:105], v[4:5], off nt
	global_load_dwordx4 v[94:97], v[6:7], off nt
	global_load_dwordx4 v[82:85], v[8:9], off nt
	global_load_dwordx4 v[62:65], v[10:11], off nt
	global_load_dwordx4 v[42:45], v[12:13], off nt
	global_load_dwordx4 v[38:41], v[14:15], off nt
	global_load_dwordx4 v[34:37], v[16:17], off nt
	v_mov_b32_e32 v2, v194
	s_waitcnt lgkmcnt(0)
	s_waitcnt vmcnt(23)
	v_pk_fma_f32 v[4:5], v[232:233], v[106:107], 0 op_sel_hi:[0,1,0] neg_lo:[1,0,0] neg_hi:[1,0,0]
	v_pk_fma_f32 v[2:3], v[232:233], v[108:109], 0 op_sel_hi:[0,1,0] neg_lo:[1,0,0] neg_hi:[1,0,0]
	v_cvt_pk_bf16_f32 v4, v4, v5
	v_cvt_pk_bf16_f32 v5, v2, v3
	ds_write_b64 v186, v[4:5]
	s_waitcnt vmcnt(22)
	v_pk_fma_f32 v[4:5], v[234:235], v[90:91], 0 op_sel_hi:[0,1,0] neg_lo:[1,0,0] neg_hi:[1,0,0]
	v_pk_fma_f32 v[2:3], v[234:235], v[92:93], 0 op_sel_hi:[0,1,0] neg_lo:[1,0,0] neg_hi:[1,0,0]
	v_cvt_pk_bf16_f32 v4, v4, v5
	v_cvt_pk_bf16_f32 v5, v2, v3
	ds_write_b64 v186, v[4:5] offset:544
	s_waitcnt vmcnt(21)
	v_pk_fma_f32 v[4:5], v[236:237], v[86:87], 0 op_sel_hi:[0,1,0] neg_lo:[1,0,0] neg_hi:[1,0,0]
	v_pk_fma_f32 v[2:3], v[236:237], v[88:89], 0 op_sel_hi:[0,1,0] neg_lo:[1,0,0] neg_hi:[1,0,0]
	v_cvt_pk_bf16_f32 v4, v4, v5
	v_cvt_pk_bf16_f32 v5, v2, v3
	ds_write_b64 v186, v[4:5] offset:1088
	s_waitcnt vmcnt(20)
	v_pk_fma_f32 v[4:5], v[238:239], v[74:75], 0 op_sel_hi:[0,1,0] neg_lo:[1,0,0] neg_hi:[1,0,0]
	v_pk_fma_f32 v[2:3], v[238:239], v[76:77], 0 op_sel_hi:[0,1,0] neg_lo:[1,0,0] neg_hi:[1,0,0]
	v_cvt_pk_bf16_f32 v4, v4, v5
	v_cvt_pk_bf16_f32 v5, v2, v3
	ds_write_b64 v186, v[4:5] offset:1632
	s_waitcnt vmcnt(19)
	v_pk_fma_f32 v[4:5], v[240:241], v[70:71], 0 op_sel_hi:[0,1,0] neg_lo:[1,0,0] neg_hi:[1,0,0]
	v_pk_fma_f32 v[2:3], v[240:241], v[72:73], 0 op_sel_hi:[0,1,0] neg_lo:[1,0,0] neg_hi:[1,0,0]
	v_cvt_pk_bf16_f32 v4, v4, v5
	v_cvt_pk_bf16_f32 v5, v2, v3
	ds_write_b64 v186, v[4:5] offset:2176
	s_waitcnt vmcnt(18)
	v_pk_fma_f32 v[4:5], v[242:243], v[54:55], 0 op_sel_hi:[0,1,0] neg_lo:[1,0,0] neg_hi:[1,0,0]
	v_pk_fma_f32 v[2:3], v[242:243], v[56:57], 0 op_sel_hi:[0,1,0] neg_lo:[1,0,0] neg_hi:[1,0,0]
	v_cvt_pk_bf16_f32 v4, v4, v5
	v_cvt_pk_bf16_f32 v5, v2, v3
	ds_write_b64 v186, v[4:5] offset:2720
	s_waitcnt vmcnt(17)
	v_pk_fma_f32 v[4:5], v[244:245], v[50:51], 0 op_sel_hi:[0,1,0] neg_lo:[1,0,0] neg_hi:[1,0,0]
	v_pk_fma_f32 v[2:3], v[244:245], v[52:53], 0 op_sel_hi:[0,1,0] neg_lo:[1,0,0] neg_hi:[1,0,0]
	v_cvt_pk_bf16_f32 v4, v4, v5
	v_cvt_pk_bf16_f32 v5, v2, v3
	ds_write_b64 v186, v[4:5] offset:3264
	s_waitcnt vmcnt(16)
	v_pk_fma_f32 v[4:5], v[246:247], v[46:47], 0 op_sel_hi:[0,1,0] neg_lo:[1,0,0] neg_hi:[1,0,0]
	v_pk_fma_f32 v[2:3], v[246:247], v[48:49], 0 op_sel_hi:[0,1,0] neg_lo:[1,0,0] neg_hi:[1,0,0]
	v_cvt_pk_bf16_f32 v4, v4, v5
	v_cvt_pk_bf16_f32 v5, v2, v3
	ds_write_b64 v186, v[4:5] offset:3808
	ds_read_b32 v232, v187 offset:64
	ds_read_b32 v234, v187 offset:72
	ds_read_b32 v236, v187 offset:80
	ds_read_b32 v238, v187 offset:88
	ds_read_b32 v240, v187 offset:96
	ds_read_b32 v242, v187 offset:104
	ds_read_b32 v244, v187 offset:112
	ds_read_b32 v246, v187 offset:120
	ds_read_b128 a[192:195], v1
	ds_read_b128 a[196:199], v1 offset:64
	ds_read_b128 a[200:203], v1 offset:128
	ds_read_b128 a[204:207], v1 offset:192
	v_lshl_add_u64 v[118:119], v[130:131], 0, s[20:21]
	v_add_co_u32_e32 v126, vcc, s7, v118
	s_nop 1
	v_addc_co_u32_e32 v127, vcc, 0, v119, vcc
	v_add_co_u32_e32 v128, vcc, s36, v118
	global_load_dwordx4 v[90:93], v[118:119], off nt
	global_load_dwordx4 v[86:89], v[126:127], off nt
	v_addc_co_u32_e32 v129, vcc, 0, v119, vcc
	v_add_co_u32_e32 v134, vcc, s37, v118
	s_nop 1
	v_addc_co_u32_e32 v135, vcc, 0, v119, vcc
	v_add_co_u32_e32 v136, vcc, s38, v118
	global_load_dwordx4 v[54:57], v[128:129], off nt
	global_load_dwordx4 v[50:53], v[134:135], off nt
	v_addc_co_u32_e32 v137, vcc, 0, v119, vcc
	v_add_co_u32_e32 v138, vcc, s39, v118
	s_nop 1
	v_addc_co_u32_e32 v139, vcc, 0, v119, vcc
	v_add_co_u32_e32 v140, vcc, s41, v118
	global_load_dwordx4 v[14:17], v[136:137], off nt
	global_load_dwordx4 v[10:13], v[138:139], off nt
	v_addc_co_u32_e32 v141, vcc, 0, v119, vcc
	v_add_co_u32_e32 v142, vcc, s42, v118
	s_nop 1
	v_addc_co_u32_e32 v143, vcc, 0, v119, vcc
	global_load_dwordx4 v[6:9], v[140:141], off nt
	global_load_dwordx4 v[2:5], v[142:143], off nt
	v_mov_b32_e32 v26, v194
	s_waitcnt lgkmcnt(0)
	s_waitcnt vmcnt(23)
	v_pk_fma_f32 v[28:29], v[232:233], v[110:111], 0 op_sel_hi:[0,1,0] neg_lo:[1,0,0] neg_hi:[1,0,0]
	v_pk_fma_f32 v[26:27], v[232:233], v[112:113], 0 op_sel_hi:[0,1,0] neg_lo:[1,0,0] neg_hi:[1,0,0]
	v_cvt_pk_bf16_f32 v28, v28, v29
	v_cvt_pk_bf16_f32 v29, v26, v27
	ds_write_b64 v186, v[28:29]
	s_waitcnt vmcnt(22)
	v_pk_fma_f32 v[28:29], v[234:235], v[98:99], 0 op_sel_hi:[0,1,0] neg_lo:[1,0,0] neg_hi:[1,0,0]
	v_pk_fma_f32 v[26:27], v[234:235], v[100:101], 0 op_sel_hi:[0,1,0] neg_lo:[1,0,0] neg_hi:[1,0,0]
	v_cvt_pk_bf16_f32 v28, v28, v29
	v_cvt_pk_bf16_f32 v29, v26, v27
	ds_write_b64 v186, v[28:29] offset:544
	s_waitcnt vmcnt(21)
	v_pk_fma_f32 v[28:29], v[236:237], v[78:79], 0 op_sel_hi:[0,1,0] neg_lo:[1,0,0] neg_hi:[1,0,0]
	v_pk_fma_f32 v[26:27], v[236:237], v[80:81], 0 op_sel_hi:[0,1,0] neg_lo:[1,0,0] neg_hi:[1,0,0]
	v_cvt_pk_bf16_f32 v28, v28, v29
	v_cvt_pk_bf16_f32 v29, v26, v27
	ds_write_b64 v186, v[28:29] offset:1088
	s_waitcnt vmcnt(20)
	v_pk_fma_f32 v[28:29], v[238:239], v[66:67], 0 op_sel_hi:[0,1,0] neg_lo:[1,0,0] neg_hi:[1,0,0]
	v_pk_fma_f32 v[26:27], v[238:239], v[68:69], 0 op_sel_hi:[0,1,0] neg_lo:[1,0,0] neg_hi:[1,0,0]
	v_cvt_pk_bf16_f32 v28, v28, v29
	v_cvt_pk_bf16_f32 v29, v26, v27
	ds_write_b64 v186, v[28:29] offset:1632
	s_waitcnt vmcnt(19)
	v_pk_fma_f32 v[28:29], v[240:241], v[58:59], 0 op_sel_hi:[0,1,0] neg_lo:[1,0,0] neg_hi:[1,0,0]
	v_pk_fma_f32 v[26:27], v[240:241], v[60:61], 0 op_sel_hi:[0,1,0] neg_lo:[1,0,0] neg_hi:[1,0,0]
	v_cvt_pk_bf16_f32 v28, v28, v29
	v_cvt_pk_bf16_f32 v29, v26, v27
	ds_write_b64 v186, v[28:29] offset:2176
	s_waitcnt vmcnt(18)
	v_pk_fma_f32 v[28:29], v[242:243], v[30:31], 0 op_sel_hi:[0,1,0] neg_lo:[1,0,0] neg_hi:[1,0,0]
	v_pk_fma_f32 v[26:27], v[242:243], v[32:33], 0 op_sel_hi:[0,1,0] neg_lo:[1,0,0] neg_hi:[1,0,0]
	v_cvt_pk_bf16_f32 v28, v28, v29
	v_cvt_pk_bf16_f32 v29, v26, v27
	ds_write_b64 v186, v[28:29] offset:2720
	s_waitcnt vmcnt(17)
	v_pk_fma_f32 v[22:23], v[244:245], v[22:23], 0 op_sel_hi:[0,1,0] neg_lo:[1,0,0] neg_hi:[1,0,0]
	v_pk_fma_f32 v[24:25], v[244:245], v[24:25], 0 op_sel_hi:[0,1,0] neg_lo:[1,0,0] neg_hi:[1,0,0]
	v_cvt_pk_bf16_f32 v22, v22, v23
	v_cvt_pk_bf16_f32 v23, v24, v25
	ds_write_b64 v186, v[22:23] offset:3264
	s_waitcnt vmcnt(16)
	v_pk_fma_f32 v[18:19], v[246:247], v[18:19], 0 op_sel_hi:[0,1,0] neg_lo:[1,0,0] neg_hi:[1,0,0]
	v_pk_fma_f32 v[20:21], v[246:247], v[20:21], 0 op_sel_hi:[0,1,0] neg_lo:[1,0,0] neg_hi:[1,0,0]
	v_cvt_pk_bf16_f32 v18, v18, v19
	v_cvt_pk_bf16_f32 v19, v20, v21
	ds_write_b64 v186, v[18:19] offset:3808
	ds_read_b32 v232, v187 offset:128
	ds_read_b32 v234, v187 offset:136
	ds_read_b32 v236, v187 offset:144
	ds_read_b32 v238, v187 offset:152
	ds_read_b32 v240, v187 offset:160
	ds_read_b32 v242, v187 offset:168
	ds_read_b32 v244, v187 offset:176
	ds_read_b32 v246, v187 offset:184
	ds_read_b128 a[208:211], v1
	ds_read_b128 a[212:215], v1 offset:64
	ds_read_b128 a[216:219], v1 offset:128
	ds_read_b128 a[220:223], v1 offset:192
	v_lshl_add_u64 v[18:19], v[150:151], 0, s[20:21]
	v_lshl_add_u64 v[20:21], v[152:153], 0, s[20:21]
	v_lshl_add_u64 v[22:23], v[156:157], 0, s[20:21]
	v_lshl_add_u64 v[24:25], v[158:159], 0, s[20:21]
	v_lshl_add_u64 v[26:27], v[160:161], 0, s[20:21]
	v_lshl_add_u64 v[28:29], v[162:163], 0, s[20:21]
	v_lshl_add_u64 v[46:47], v[164:165], 0, s[20:21]
	v_lshl_add_u64 v[48:49], v[166:167], 0, s[20:21]
	global_load_dwordx4 v[78:81], v[18:19], off nt
	global_load_dwordx4 v[74:77], v[20:21], off nt
	global_load_dwordx4 v[70:73], v[22:23], off nt
	global_load_dwordx4 v[66:69], v[24:25], off nt
	global_load_dwordx4 v[30:33], v[26:27], off nt
	s_nop 0
	global_load_dwordx4 v[26:29], v[28:29], off nt
	s_nop 0
	global_load_dwordx4 v[22:25], v[46:47], off nt
	global_load_dwordx4 v[18:21], v[48:49], off nt
	s_waitcnt lgkmcnt(0)
	s_waitcnt vmcnt(23)
	v_pk_fma_f32 v[48:49], v[232:233], v[114:115], 0 op_sel_hi:[0,1,0] neg_lo:[1,0,0] neg_hi:[1,0,0]
	v_pk_fma_f32 v[46:47], v[232:233], v[116:117], 0 op_sel_hi:[0,1,0] neg_lo:[1,0,0] neg_hi:[1,0,0]
	v_cvt_pk_bf16_f32 v48, v48, v49
	v_cvt_pk_bf16_f32 v49, v46, v47
	ds_write_b64 v186, v[48:49]
	s_waitcnt vmcnt(22)
	v_pk_fma_f32 v[48:49], v[234:235], v[102:103], 0 op_sel_hi:[0,1,0] neg_lo:[1,0,0] neg_hi:[1,0,0]
	v_pk_fma_f32 v[46:47], v[234:235], v[104:105], 0 op_sel_hi:[0,1,0] neg_lo:[1,0,0] neg_hi:[1,0,0]
	v_cvt_pk_bf16_f32 v48, v48, v49
	v_cvt_pk_bf16_f32 v49, v46, v47
	ds_write_b64 v186, v[48:49] offset:544
	s_waitcnt vmcnt(21)
	v_pk_fma_f32 v[48:49], v[236:237], v[94:95], 0 op_sel_hi:[0,1,0] neg_lo:[1,0,0] neg_hi:[1,0,0]
	v_pk_fma_f32 v[46:47], v[236:237], v[96:97], 0 op_sel_hi:[0,1,0] neg_lo:[1,0,0] neg_hi:[1,0,0]
	v_cvt_pk_bf16_f32 v48, v48, v49
	v_cvt_pk_bf16_f32 v49, v46, v47
	ds_write_b64 v186, v[48:49] offset:1088
	s_waitcnt vmcnt(20)
	v_pk_fma_f32 v[48:49], v[238:239], v[82:83], 0 op_sel_hi:[0,1,0] neg_lo:[1,0,0] neg_hi:[1,0,0]
	v_pk_fma_f32 v[46:47], v[238:239], v[84:85], 0 op_sel_hi:[0,1,0] neg_lo:[1,0,0] neg_hi:[1,0,0]
	v_cvt_pk_bf16_f32 v48, v48, v49
	v_cvt_pk_bf16_f32 v49, v46, v47
	ds_write_b64 v186, v[48:49] offset:1632
	s_waitcnt vmcnt(19)
	v_pk_fma_f32 v[48:49], v[240:241], v[62:63], 0 op_sel_hi:[0,1,0] neg_lo:[1,0,0] neg_hi:[1,0,0]
	v_pk_fma_f32 v[46:47], v[240:241], v[64:65], 0 op_sel_hi:[0,1,0] neg_lo:[1,0,0] neg_hi:[1,0,0]
	v_cvt_pk_bf16_f32 v48, v48, v49
	v_cvt_pk_bf16_f32 v49, v46, v47
	ds_write_b64 v186, v[48:49] offset:2176
	s_waitcnt vmcnt(18)
	v_pk_fma_f32 v[42:43], v[242:243], v[42:43], 0 op_sel_hi:[0,1,0] neg_lo:[1,0,0] neg_hi:[1,0,0]
	v_pk_fma_f32 v[44:45], v[242:243], v[44:45], 0 op_sel_hi:[0,1,0] neg_lo:[1,0,0] neg_hi:[1,0,0]
	v_cvt_pk_bf16_f32 v42, v42, v43
	v_cvt_pk_bf16_f32 v43, v44, v45
	ds_write_b64 v186, v[42:43] offset:2720
	s_waitcnt vmcnt(17)
	v_pk_fma_f32 v[38:39], v[244:245], v[38:39], 0 op_sel_hi:[0,1,0] neg_lo:[1,0,0] neg_hi:[1,0,0]
	v_pk_fma_f32 v[40:41], v[244:245], v[40:41], 0 op_sel_hi:[0,1,0] neg_lo:[1,0,0] neg_hi:[1,0,0]
	v_cvt_pk_bf16_f32 v38, v38, v39
	v_cvt_pk_bf16_f32 v39, v40, v41
	ds_write_b64 v186, v[38:39] offset:3264
	s_waitcnt vmcnt(16)
	v_pk_fma_f32 v[34:35], v[246:247], v[34:35], 0 op_sel_hi:[0,1,0] neg_lo:[1,0,0] neg_hi:[1,0,0]
	v_pk_fma_f32 v[36:37], v[246:247], v[36:37], 0 op_sel_hi:[0,1,0] neg_lo:[1,0,0] neg_hi:[1,0,0]
	v_cvt_pk_bf16_f32 v34, v34, v35
	v_cvt_pk_bf16_f32 v35, v36, v37
	ds_write_b64 v186, v[34:35] offset:3808
	ds_read_b32 v232, v187 offset:0
	ds_read_b32 v234, v187 offset:8
	ds_read_b32 v236, v187 offset:16
	ds_read_b32 v238, v187 offset:24
	ds_read_b32 v240, v187 offset:32
	ds_read_b32 v242, v187 offset:40
	ds_read_b32 v244, v187 offset:48
	ds_read_b32 v246, v187 offset:56
	ds_read_b128 a[224:227], v1
	ds_read_b128 a[228:231], v1 offset:64
	ds_read_b128 a[232:235], v1 offset:128
	ds_read_b128 a[236:239], v1 offset:192
	v_lshl_add_u64 v[34:35], v[168:169], 0, s[20:21]
	v_lshl_add_u64 v[36:37], v[170:171], 0, s[20:21]
	v_lshl_add_u64 v[38:39], v[172:173], 0, s[20:21]
	v_lshl_add_u64 v[40:41], v[174:175], 0, s[20:21]
	v_lshl_add_u64 v[42:43], v[176:177], 0, s[20:21]
	v_lshl_add_u64 v[44:45], v[178:179], 0, s[20:21]
	v_lshl_add_u64 v[58:59], v[180:181], 0, s[20:21]
	v_lshl_add_u64 v[60:61], v[182:183], 0, s[20:21]
	global_load_dwordx4 v[122:125], v[34:35], off nt
	global_load_dwordx4 v[106:109], v[36:37], off nt
	global_load_dwordx4 v[94:97], v[38:39], off nt
	global_load_dwordx4 v[82:85], v[40:41], off nt
	global_load_dwordx4 v[46:49], v[42:43], off nt
	s_nop 0
	global_load_dwordx4 v[42:45], v[44:45], off nt
	s_nop 0
	global_load_dwordx4 v[38:41], v[58:59], off nt
	global_load_dwordx4 v[34:37], v[60:61], off nt
	v_mov_b32_e32 v98, v133
	v_add_u32_e32 v99, 1, v98
	v_cmp_eq_u32_e32 vcc, v98, v132
	s_nop 1
	v_cndmask_b32_e64 v60, 0, 1.0, vcc
	v_cmp_eq_u32_e32 vcc, v99, v132
	s_nop 1
	v_cndmask_b32_e64 v61, 0, 1.0, vcc
	s_waitcnt lgkmcnt(0)
	s_waitcnt vmcnt(23)
	v_pk_fma_f32 v[62:63], v[232:233], v[90:91], v[60:61] op_sel_hi:[0,1,1] neg_lo:[1,0,0] neg_hi:[1,0,0]
	v_add_u32_e32 v90, 3, v98
	v_add_u32_e32 v91, 2, v98
	v_cmp_eq_u32_e32 vcc, v90, v132
	v_cvt_pk_bf16_f32 v62, v62, v63
	s_nop 0
	v_cndmask_b32_e64 v65, 0, 1.0, vcc
	v_cmp_eq_u32_e32 vcc, v91, v132
	s_nop 1
	v_cndmask_b32_e64 v64, 0, 1.0, vcc
	v_pk_fma_f32 v[58:59], v[232:233], v[92:93], v[64:65] op_sel_hi:[0,1,1] neg_lo:[1,0,0] neg_hi:[1,0,0]
	v_cvt_pk_bf16_f32 v63, v58, v59
	ds_write_b64 v186, v[62:63]
	v_cmp_eq_u32_e32 vcc, v98, v193
	s_nop 1
	v_cndmask_b32_e64 v62, 0, 1.0, vcc
	v_cmp_eq_u32_e32 vcc, v99, v193
	s_nop 1
	v_cndmask_b32_e64 v63, 0, 1.0, vcc
	v_cmp_eq_u32_e32 vcc, v90, v193
	s_waitcnt vmcnt(22)
	v_pk_fma_f32 v[62:63], v[234:235], v[86:87], v[62:63] op_sel_hi:[0,1,1] neg_lo:[1,0,0] neg_hi:[1,0,0]
	v_cvt_pk_bf16_f32 v62, v62, v63
	v_cndmask_b32_e64 v61, 0, 1.0, vcc
	v_pk_fma_f32 v[58:59], v[234:235], v[88:89], v[60:61] op_sel_hi:[0,1,1] neg_lo:[1,0,0] neg_hi:[1,0,0]
	v_cvt_pk_bf16_f32 v63, v58, v59
	ds_write_b64 v186, v[62:63] offset:544
	v_cmp_eq_u32_e32 vcc, v98, v192
	s_nop 1
	v_cndmask_b32_e64 v60, 0, 1.0, vcc
	v_cmp_eq_u32_e32 vcc, v99, v192
	s_nop 1
	v_cndmask_b32_e64 v61, 0, 1.0, vcc
	v_cmp_eq_u32_e32 vcc, v90, v192
	s_waitcnt vmcnt(21)
	v_pk_fma_f32 v[54:55], v[236:237], v[54:55], v[60:61] op_sel_hi:[0,1,1] neg_lo:[1,0,0] neg_hi:[1,0,0]
	v_cvt_pk_bf16_f32 v54, v54, v55
	v_cndmask_b32_e64 v61, 0, 1.0, vcc
	v_cmp_eq_u32_e32 vcc, v91, v192
	s_nop 1
	v_cndmask_b32_e64 v60, 0, 1.0, vcc
	v_pk_fma_f32 v[56:57], v[236:237], v[56:57], v[60:61] op_sel_hi:[0,1,1] neg_lo:[1,0,0] neg_hi:[1,0,0]
	v_cvt_pk_bf16_f32 v55, v56, v57
	ds_write_b64 v186, v[54:55] offset:1088
	v_cmp_eq_u32_e32 vcc, v98, v190
	s_nop 1
	v_cndmask_b32_e64 v56, 0, 1.0, vcc
	v_cmp_eq_u32_e32 vcc, v99, v190
	s_nop 1
	v_cndmask_b32_e64 v57, 0, 1.0, vcc
	v_cmp_eq_u32_e32 vcc, v90, v190
	s_waitcnt vmcnt(20)
	v_pk_fma_f32 v[50:51], v[238:239], v[50:51], v[56:57] op_sel_hi:[0,1,1] neg_lo:[1,0,0] neg_hi:[1,0,0]
	v_cvt_pk_bf16_f32 v50, v50, v51
	v_cndmask_b32_e64 v57, 0, 1.0, vcc
	v_cmp_eq_u32_e32 vcc, v91, v190
	s_nop 1
	v_cndmask_b32_e64 v56, 0, 1.0, vcc
	v_pk_fma_f32 v[52:53], v[238:239], v[52:53], v[56:57] op_sel_hi:[0,1,1] neg_lo:[1,0,0] neg_hi:[1,0,0]
	v_cvt_pk_bf16_f32 v51, v52, v53
	ds_write_b64 v186, v[50:51] offset:1632
	v_cmp_eq_u32_e32 vcc, v98, v149
	s_nop 1
	v_cndmask_b32_e64 v52, 0, 1.0, vcc
	v_cmp_eq_u32_e32 vcc, v99, v149
	s_nop 1
	v_cndmask_b32_e64 v53, 0, 1.0, vcc
	v_cmp_eq_u32_e32 vcc, v90, v149
	s_waitcnt vmcnt(19)
	v_pk_fma_f32 v[14:15], v[240:241], v[14:15], v[52:53] op_sel_hi:[0,1,1] neg_lo:[1,0,0] neg_hi:[1,0,0]
	v_cvt_pk_bf16_f32 v14, v14, v15
	v_cndmask_b32_e64 v53, 0, 1.0, vcc
	v_cmp_eq_u32_e32 vcc, v91, v149
	s_nop 1
	v_cndmask_b32_e64 v52, 0, 1.0, vcc
	v_pk_fma_f32 v[16:17], v[240:241], v[16:17], v[52:53] op_sel_hi:[0,1,1] neg_lo:[1,0,0] neg_hi:[1,0,0]
	v_cvt_pk_bf16_f32 v15, v16, v17
	ds_write_b64 v186, v[14:15] offset:2176
	v_cmp_eq_u32_e32 vcc, v98, v148
	s_nop 1
	v_cndmask_b32_e64 v16, 0, 1.0, vcc
	v_cmp_eq_u32_e32 vcc, v99, v148
	s_nop 1
	v_cndmask_b32_e64 v17, 0, 1.0, vcc
	v_cmp_eq_u32_e32 vcc, v90, v148
	s_waitcnt vmcnt(18)
	v_pk_fma_f32 v[10:11], v[242:243], v[10:11], v[16:17] op_sel_hi:[0,1,1] neg_lo:[1,0,0] neg_hi:[1,0,0]
	v_cvt_pk_bf16_f32 v10, v10, v11
	v_cndmask_b32_e64 v17, 0, 1.0, vcc
	v_cmp_eq_u32_e32 vcc, v91, v148
	s_nop 1
	v_cndmask_b32_e64 v16, 0, 1.0, vcc
	v_pk_fma_f32 v[12:13], v[242:243], v[12:13], v[16:17] op_sel_hi:[0,1,1] neg_lo:[1,0,0] neg_hi:[1,0,0]
	v_cvt_pk_bf16_f32 v11, v12, v13
	ds_write_b64 v186, v[10:11] offset:2720
	v_cmp_eq_u32_e32 vcc, v98, v147
	s_nop 1
	v_cndmask_b32_e64 v12, 0, 1.0, vcc
	v_cmp_eq_u32_e32 vcc, v99, v147
	s_nop 1
	v_cndmask_b32_e64 v13, 0, 1.0, vcc
	v_cmp_eq_u32_e32 vcc, v90, v147
	s_waitcnt vmcnt(17)
	v_pk_fma_f32 v[6:7], v[244:245], v[6:7], v[12:13] op_sel_hi:[0,1,1] neg_lo:[1,0,0] neg_hi:[1,0,0]
	v_cvt_pk_bf16_f32 v6, v6, v7
	v_cndmask_b32_e64 v13, 0, 1.0, vcc
	v_cmp_eq_u32_e32 vcc, v91, v147
	s_nop 1
	v_cndmask_b32_e64 v12, 0, 1.0, vcc
	v_pk_fma_f32 v[8:9], v[244:245], v[8:9], v[12:13] op_sel_hi:[0,1,1] neg_lo:[1,0,0] neg_hi:[1,0,0]
	v_cvt_pk_bf16_f32 v7, v8, v9
	ds_write_b64 v186, v[6:7] offset:3264
	v_cmp_eq_u32_e32 vcc, v98, v146
	s_nop 1
	v_cndmask_b32_e64 v8, 0, 1.0, vcc
	v_cmp_eq_u32_e32 vcc, v99, v146
	s_nop 1
	v_cndmask_b32_e64 v9, 0, 1.0, vcc
	v_cmp_eq_u32_e32 vcc, v90, v146
	s_waitcnt vmcnt(16)
	v_pk_fma_f32 v[2:3], v[246:247], v[2:3], v[8:9] op_sel_hi:[0,1,1] neg_lo:[1,0,0] neg_hi:[1,0,0]
	v_cvt_pk_bf16_f32 v2, v2, v3
	v_cndmask_b32_e64 v9, 0, 1.0, vcc
	v_cmp_eq_u32_e32 vcc, v91, v146
	s_nop 1
	v_cndmask_b32_e64 v8, 0, 1.0, vcc
	v_pk_fma_f32 v[4:5], v[246:247], v[4:5], v[8:9] op_sel_hi:[0,1,1] neg_lo:[1,0,0] neg_hi:[1,0,0]
	v_cvt_pk_bf16_f32 v3, v4, v5
	ds_write_b64 v186, v[2:3] offset:3808
	ds_read_b32 v232, v187 offset:64
	ds_read_b32 v234, v187 offset:72
	ds_read_b32 v236, v187 offset:80
	ds_read_b32 v238, v187 offset:88
	ds_read_b32 v240, v187 offset:96
	ds_read_b32 v242, v187 offset:104
	ds_read_b32 v244, v187 offset:112
	ds_read_b32 v246, v187 offset:120
	ds_read_b128 v[2:5], v1
	ds_read_b128 v[6:9], v1 offset:64
	ds_read_b128 v[10:13], v1 offset:128
	ds_read_b128 v[14:17], v1 offset:192
	global_load_dwordx4 v[118:121], v[118:119], off offset:512 nt
	s_nop 0
	global_load_dwordx4 v[110:113], v[126:127], off offset:512 nt
	global_load_dwordx4 v[98:101], v[128:129], off offset:512 nt
	global_load_dwordx4 v[86:89], v[134:135], off offset:512 nt
	global_load_dwordx4 v[62:65], v[136:137], off offset:512 nt
	global_load_dwordx4 v[58:61], v[138:139], off offset:512 nt
	global_load_dwordx4 v[54:57], v[140:141], off offset:512 nt
	global_load_dwordx4 v[50:53], v[142:143], off offset:512 nt
	v_mov_b32_e32 v91, v133
	v_or_b32_e32 v138, 16, v132
	v_add_u32_e32 v102, 1, v91
	v_cmp_eq_u32_e32 vcc, v91, v138
	v_add_u32_e32 v103, 3, v91
	v_add_u32_e32 v104, 2, v91
	v_cndmask_b32_e64 v92, 0, 1.0, vcc
	v_cmp_eq_u32_e32 vcc, v102, v138
	v_or_b32_e32 v139, 18, v132
	v_or_b32_e32 v140, 20, v132
	v_cndmask_b32_e64 v93, 0, 1.0, vcc
	v_cmp_eq_u32_e32 vcc, v103, v138
	s_waitcnt lgkmcnt(0)
	s_waitcnt vmcnt(23)
	v_pk_fma_f32 v[78:79], v[232:233], v[78:79], v[92:93] op_sel_hi:[0,1,1] neg_lo:[1,0,0] neg_hi:[1,0,0]
	v_cvt_pk_bf16_f32 v78, v78, v79
	v_cndmask_b32_e64 v93, 0, 1.0, vcc
	v_cmp_eq_u32_e32 vcc, v104, v138
	v_or_b32_e32 v141, 22, v132
	v_or_b32_e32 v142, 24, v132
	v_cndmask_b32_e64 v92, 0, 1.0, vcc
	v_pk_fma_f32 v[80:81], v[232:233], v[80:81], v[92:93] op_sel_hi:[0,1,1] neg_lo:[1,0,0] neg_hi:[1,0,0]
	v_cvt_pk_bf16_f32 v79, v80, v81
	ds_write_b64 v186, v[78:79]
	v_cmp_eq_u32_e32 vcc, v91, v139
	v_or_b32_e32 v143, 26, v132
	v_or_b32_e32 v144, 28, v132
	v_cndmask_b32_e64 v80, 0, 1.0, vcc
	v_cmp_eq_u32_e32 vcc, v102, v139
	v_or_b32_e32 v145, 30, v132
	s_nop 0
	v_cndmask_b32_e64 v81, 0, 1.0, vcc
	v_cmp_eq_u32_e32 vcc, v103, v139
	s_waitcnt vmcnt(22)
	v_pk_fma_f32 v[74:75], v[234:235], v[74:75], v[80:81] op_sel_hi:[0,1,1] neg_lo:[1,0,0] neg_hi:[1,0,0]
	v_cvt_pk_bf16_f32 v74, v74, v75
	v_cndmask_b32_e64 v81, 0, 1.0, vcc
	v_cmp_eq_u32_e32 vcc, v104, v139
	s_nop 1
	v_cndmask_b32_e64 v80, 0, 1.0, vcc
	v_pk_fma_f32 v[76:77], v[234:235], v[76:77], v[80:81] op_sel_hi:[0,1,1] neg_lo:[1,0,0] neg_hi:[1,0,0]
	v_cvt_pk_bf16_f32 v75, v76, v77
	ds_write_b64 v186, v[74:75] offset:544
	v_cmp_eq_u32_e32 vcc, v91, v140
	s_nop 1
	v_cndmask_b32_e64 v76, 0, 1.0, vcc
	v_cmp_eq_u32_e32 vcc, v102, v140
	s_nop 1
	v_cndmask_b32_e64 v77, 0, 1.0, vcc
	v_cmp_eq_u32_e32 vcc, v103, v140
	s_waitcnt vmcnt(21)
	v_pk_fma_f32 v[70:71], v[236:237], v[70:71], v[76:77] op_sel_hi:[0,1,1] neg_lo:[1,0,0] neg_hi:[1,0,0]
	v_cvt_pk_bf16_f32 v70, v70, v71
	v_cndmask_b32_e64 v77, 0, 1.0, vcc
	v_cmp_eq_u32_e32 vcc, v104, v140
	s_nop 1
	v_cndmask_b32_e64 v76, 0, 1.0, vcc
	v_pk_fma_f32 v[72:73], v[236:237], v[72:73], v[76:77] op_sel_hi:[0,1,1] neg_lo:[1,0,0] neg_hi:[1,0,0]
	v_cvt_pk_bf16_f32 v71, v72, v73
	ds_write_b64 v186, v[70:71] offset:1088
	v_cmp_eq_u32_e32 vcc, v91, v141
	s_nop 1
	v_cndmask_b32_e64 v72, 0, 1.0, vcc
	v_cmp_eq_u32_e32 vcc, v102, v141
	s_nop 1
	v_cndmask_b32_e64 v73, 0, 1.0, vcc
	v_cmp_eq_u32_e32 vcc, v103, v141
	s_waitcnt vmcnt(20)
	v_pk_fma_f32 v[66:67], v[238:239], v[66:67], v[72:73] op_sel_hi:[0,1,1] neg_lo:[1,0,0] neg_hi:[1,0,0]
	v_cvt_pk_bf16_f32 v66, v66, v67
	v_cndmask_b32_e64 v73, 0, 1.0, vcc
	v_cmp_eq_u32_e32 vcc, v104, v141
	s_nop 1
	v_cndmask_b32_e64 v72, 0, 1.0, vcc
	v_pk_fma_f32 v[68:69], v[238:239], v[68:69], v[72:73] op_sel_hi:[0,1,1] neg_lo:[1,0,0] neg_hi:[1,0,0]
	v_cvt_pk_bf16_f32 v67, v68, v69
	ds_write_b64 v186, v[66:67] offset:1632
	v_cmp_eq_u32_e32 vcc, v91, v142
	s_nop 1
	v_cndmask_b32_e64 v68, 0, 1.0, vcc
	v_cmp_eq_u32_e32 vcc, v102, v142
	s_nop 1
	v_cndmask_b32_e64 v69, 0, 1.0, vcc
	v_cmp_eq_u32_e32 vcc, v103, v142
	s_waitcnt vmcnt(19)
	v_pk_fma_f32 v[30:31], v[240:241], v[30:31], v[68:69] op_sel_hi:[0,1,1] neg_lo:[1,0,0] neg_hi:[1,0,0]
	v_cvt_pk_bf16_f32 v30, v30, v31
	v_cndmask_b32_e64 v69, 0, 1.0, vcc
	v_cmp_eq_u32_e32 vcc, v104, v142
	s_nop 1
	v_cndmask_b32_e64 v68, 0, 1.0, vcc
	v_pk_fma_f32 v[32:33], v[240:241], v[32:33], v[68:69] op_sel_hi:[0,1,1] neg_lo:[1,0,0] neg_hi:[1,0,0]
	v_cvt_pk_bf16_f32 v31, v32, v33
	ds_write_b64 v186, v[30:31] offset:2176
	v_cmp_eq_u32_e32 vcc, v91, v143
	s_nop 1
	v_cndmask_b32_e64 v32, 0, 1.0, vcc
	v_cmp_eq_u32_e32 vcc, v102, v143
	s_nop 1
	v_cndmask_b32_e64 v33, 0, 1.0, vcc
	v_cmp_eq_u32_e32 vcc, v103, v143
	s_waitcnt vmcnt(18)
	v_pk_fma_f32 v[26:27], v[242:243], v[26:27], v[32:33] op_sel_hi:[0,1,1] neg_lo:[1,0,0] neg_hi:[1,0,0]
	v_cvt_pk_bf16_f32 v26, v26, v27
	v_cndmask_b32_e64 v33, 0, 1.0, vcc
	v_cmp_eq_u32_e32 vcc, v104, v143
	s_nop 1
	v_cndmask_b32_e64 v32, 0, 1.0, vcc
	v_pk_fma_f32 v[28:29], v[242:243], v[28:29], v[32:33] op_sel_hi:[0,1,1] neg_lo:[1,0,0] neg_hi:[1,0,0]
	v_cvt_pk_bf16_f32 v27, v28, v29
	ds_write_b64 v186, v[26:27] offset:2720
	v_cmp_eq_u32_e32 vcc, v91, v144
	s_nop 1
	v_cndmask_b32_e64 v28, 0, 1.0, vcc
	v_cmp_eq_u32_e32 vcc, v102, v144
	s_nop 1
	v_cndmask_b32_e64 v29, 0, 1.0, vcc
	v_cmp_eq_u32_e32 vcc, v103, v144
	s_waitcnt vmcnt(17)
	v_pk_fma_f32 v[22:23], v[244:245], v[22:23], v[28:29] op_sel_hi:[0,1,1] neg_lo:[1,0,0] neg_hi:[1,0,0]
	v_cvt_pk_bf16_f32 v22, v22, v23
	v_cndmask_b32_e64 v29, 0, 1.0, vcc
	v_cmp_eq_u32_e32 vcc, v104, v144
	s_nop 1
	v_cndmask_b32_e64 v28, 0, 1.0, vcc
	v_pk_fma_f32 v[24:25], v[244:245], v[24:25], v[28:29] op_sel_hi:[0,1,1] neg_lo:[1,0,0] neg_hi:[1,0,0]
	v_cvt_pk_bf16_f32 v23, v24, v25
	ds_write_b64 v186, v[22:23] offset:3264
	v_cmp_eq_u32_e32 vcc, v91, v145
	s_nop 1
	v_cndmask_b32_e64 v24, 0, 1.0, vcc
	v_cmp_eq_u32_e32 vcc, v102, v145
	s_nop 1
	v_cndmask_b32_e64 v25, 0, 1.0, vcc
	v_cmp_eq_u32_e32 vcc, v103, v145
	s_waitcnt vmcnt(16)
	v_pk_fma_f32 v[18:19], v[246:247], v[18:19], v[24:25] op_sel_hi:[0,1,1] neg_lo:[1,0,0] neg_hi:[1,0,0]
	v_cvt_pk_bf16_f32 v18, v18, v19
	v_cndmask_b32_e64 v25, 0, 1.0, vcc
	v_cmp_eq_u32_e32 vcc, v104, v145
	s_nop 1
	v_cndmask_b32_e64 v24, 0, 1.0, vcc
	v_pk_fma_f32 v[20:21], v[246:247], v[20:21], v[24:25] op_sel_hi:[0,1,1] neg_lo:[1,0,0] neg_hi:[1,0,0]
	v_cvt_pk_bf16_f32 v19, v20, v21
	ds_write_b64 v186, v[18:19] offset:3808
	ds_read_b32 v232, v187 offset:128
	ds_read_b32 v234, v187 offset:136
	ds_read_b32 v236, v187 offset:144
	ds_read_b32 v238, v187 offset:152
	ds_read_b32 v240, v187 offset:160
	ds_read_b32 v242, v187 offset:168
	ds_read_b32 v244, v187 offset:176
	ds_read_b32 v246, v187 offset:184
	ds_read_b128 v[18:21], v1
	ds_read_b128 v[22:25], v1 offset:64
	ds_read_b128 v[26:29], v1 offset:128
	ds_read_b128 v[30:33], v1 offset:192
	v_lshl_add_u64 v[66:67], v[150:151], 0, s[8:9]
	v_lshl_add_u64 v[68:69], v[152:153], 0, s[8:9]
	v_lshl_add_u64 v[70:71], v[156:157], 0, s[8:9]
	v_lshl_add_u64 v[72:73], v[158:159], 0, s[8:9]
	v_lshl_add_u64 v[74:75], v[160:161], 0, s[8:9]
	v_lshl_add_u64 v[76:77], v[162:163], 0, s[8:9]
	v_lshl_add_u64 v[134:135], v[164:165], 0, s[8:9]
	v_lshl_add_u64 v[136:137], v[166:167], 0, s[8:9]
	global_load_dwordx4 v[126:129], v[66:67], off nt
	global_load_dwordx4 v[114:117], v[68:69], off nt
	global_load_dwordx4 v[102:105], v[70:71], off nt
	global_load_dwordx4 v[90:93], v[72:73], off nt
	global_load_dwordx4 v[78:81], v[74:75], off nt
	s_nop 0
	global_load_dwordx4 v[74:77], v[76:77], off nt
	s_nop 0
	global_load_dwordx4 v[70:73], v[134:135], off nt
	global_load_dwordx4 v[66:69], v[136:137], off nt
	v_or_b32_e32 v194, 32, v132
	v_add_u32_e32 v135, 1, v133
	v_cmp_eq_u32_e32 vcc, v133, v194
	v_add_u32_e32 v202, 3, v133
	v_add_u32_e32 v203, 2, v133
	v_cndmask_b32_e64 v136, 0, 1.0, vcc
	v_cmp_eq_u32_e32 vcc, v135, v194
	v_or_b32_e32 v195, 34, v132
	v_or_b32_e32 v196, 36, v132
	v_cndmask_b32_e64 v137, 0, 1.0, vcc
	v_cmp_eq_u32_e32 vcc, v202, v194
	s_waitcnt lgkmcnt(0)
	s_waitcnt vmcnt(23)
	v_pk_fma_f32 v[122:123], v[232:233], v[122:123], v[136:137] op_sel_hi:[0,1,1] neg_lo:[1,0,0] neg_hi:[1,0,0]
	v_cvt_pk_bf16_f32 v122, v122, v123
	v_cndmask_b32_e64 v137, 0, 1.0, vcc
	v_cmp_eq_u32_e32 vcc, v203, v194
	v_or_b32_e32 v197, 38, v132
	v_or_b32_e32 v198, 40, v132
	v_cndmask_b32_e64 v136, 0, 1.0, vcc
	v_pk_fma_f32 v[124:125], v[232:233], v[124:125], v[136:137] op_sel_hi:[0,1,1] neg_lo:[1,0,0] neg_hi:[1,0,0]
	v_cvt_pk_bf16_f32 v123, v124, v125
	ds_write_b64 v186, v[122:123]
	v_cmp_eq_u32_e32 vcc, v133, v195
	v_or_b32_e32 v199, 42, v132
	v_or_b32_e32 v200, 44, v132
	v_cndmask_b32_e64 v124, 0, 1.0, vcc
	v_cmp_eq_u32_e32 vcc, v135, v195
	v_or_b32_e32 v201, 46, v132
	s_nop 0
	v_cndmask_b32_e64 v125, 0, 1.0, vcc
	v_cmp_eq_u32_e32 vcc, v202, v195
	s_waitcnt vmcnt(22)
	v_pk_fma_f32 v[106:107], v[234:235], v[106:107], v[124:125] op_sel_hi:[0,1,1] neg_lo:[1,0,0] neg_hi:[1,0,0]
	v_cvt_pk_bf16_f32 v106, v106, v107
	v_cndmask_b32_e64 v125, 0, 1.0, vcc
	v_cmp_eq_u32_e32 vcc, v203, v195
	s_nop 1
	v_cndmask_b32_e64 v124, 0, 1.0, vcc
	v_pk_fma_f32 v[108:109], v[234:235], v[108:109], v[124:125] op_sel_hi:[0,1,1] neg_lo:[1,0,0] neg_hi:[1,0,0]
	v_cvt_pk_bf16_f32 v107, v108, v109
	ds_write_b64 v186, v[106:107] offset:544
	v_cmp_eq_u32_e32 vcc, v133, v196
	s_nop 1
	v_cndmask_b32_e64 v108, 0, 1.0, vcc
	v_cmp_eq_u32_e32 vcc, v135, v196
	s_nop 1
	v_cndmask_b32_e64 v109, 0, 1.0, vcc
	v_cmp_eq_u32_e32 vcc, v202, v196
	s_waitcnt vmcnt(21)
	v_pk_fma_f32 v[94:95], v[236:237], v[94:95], v[108:109] op_sel_hi:[0,1,1] neg_lo:[1,0,0] neg_hi:[1,0,0]
	v_cvt_pk_bf16_f32 v94, v94, v95
	v_cndmask_b32_e64 v109, 0, 1.0, vcc
	v_cmp_eq_u32_e32 vcc, v203, v196
	s_nop 1
	v_cndmask_b32_e64 v108, 0, 1.0, vcc
	v_pk_fma_f32 v[96:97], v[236:237], v[96:97], v[108:109] op_sel_hi:[0,1,1] neg_lo:[1,0,0] neg_hi:[1,0,0]
	v_cvt_pk_bf16_f32 v95, v96, v97
	ds_write_b64 v186, v[94:95] offset:1088
	v_cmp_eq_u32_e32 vcc, v133, v197
	s_nop 1
	v_cndmask_b32_e64 v96, 0, 1.0, vcc
	v_cmp_eq_u32_e32 vcc, v135, v197
	s_nop 1
	v_cndmask_b32_e64 v97, 0, 1.0, vcc
	v_cmp_eq_u32_e32 vcc, v202, v197
	s_waitcnt vmcnt(20)
	v_pk_fma_f32 v[82:83], v[238:239], v[82:83], v[96:97] op_sel_hi:[0,1,1] neg_lo:[1,0,0] neg_hi:[1,0,0]
	v_cvt_pk_bf16_f32 v82, v82, v83
	v_cndmask_b32_e64 v97, 0, 1.0, vcc
	v_cmp_eq_u32_e32 vcc, v203, v197
	s_nop 1
	v_cndmask_b32_e64 v96, 0, 1.0, vcc
	v_pk_fma_f32 v[84:85], v[238:239], v[84:85], v[96:97] op_sel_hi:[0,1,1] neg_lo:[1,0,0] neg_hi:[1,0,0]
	v_cvt_pk_bf16_f32 v83, v84, v85
	ds_write_b64 v186, v[82:83] offset:1632
	v_cmp_eq_u32_e32 vcc, v133, v198
	s_nop 1
	v_cndmask_b32_e64 v84, 0, 1.0, vcc
	v_cmp_eq_u32_e32 vcc, v135, v198
	s_nop 1
	v_cndmask_b32_e64 v85, 0, 1.0, vcc
	v_cmp_eq_u32_e32 vcc, v202, v198
	s_waitcnt vmcnt(19)
	v_pk_fma_f32 v[46:47], v[240:241], v[46:47], v[84:85] op_sel_hi:[0,1,1] neg_lo:[1,0,0] neg_hi:[1,0,0]
	v_cvt_pk_bf16_f32 v46, v46, v47
	v_cndmask_b32_e64 v85, 0, 1.0, vcc
	v_cmp_eq_u32_e32 vcc, v203, v198
	s_nop 1
	v_cndmask_b32_e64 v84, 0, 1.0, vcc
	v_pk_fma_f32 v[48:49], v[240:241], v[48:49], v[84:85] op_sel_hi:[0,1,1] neg_lo:[1,0,0] neg_hi:[1,0,0]
	v_cvt_pk_bf16_f32 v47, v48, v49
	ds_write_b64 v186, v[46:47] offset:2176
	v_cmp_eq_u32_e32 vcc, v133, v199
	s_nop 1
	v_cndmask_b32_e64 v48, 0, 1.0, vcc
	v_cmp_eq_u32_e32 vcc, v135, v199
	s_nop 1
	v_cndmask_b32_e64 v49, 0, 1.0, vcc
	v_cmp_eq_u32_e32 vcc, v202, v199
	s_waitcnt vmcnt(18)
	v_pk_fma_f32 v[42:43], v[242:243], v[42:43], v[48:49] op_sel_hi:[0,1,1] neg_lo:[1,0,0] neg_hi:[1,0,0]
	v_cvt_pk_bf16_f32 v42, v42, v43
	v_cndmask_b32_e64 v49, 0, 1.0, vcc
	v_cmp_eq_u32_e32 vcc, v203, v199
	s_nop 1
	v_cndmask_b32_e64 v48, 0, 1.0, vcc
	v_pk_fma_f32 v[44:45], v[242:243], v[44:45], v[48:49] op_sel_hi:[0,1,1] neg_lo:[1,0,0] neg_hi:[1,0,0]
	v_cvt_pk_bf16_f32 v43, v44, v45
	ds_write_b64 v186, v[42:43] offset:2720
	v_cmp_eq_u32_e32 vcc, v133, v200
	s_nop 1
	v_cndmask_b32_e64 v44, 0, 1.0, vcc
	v_cmp_eq_u32_e32 vcc, v135, v200
	s_nop 1
	v_cndmask_b32_e64 v45, 0, 1.0, vcc
	v_cmp_eq_u32_e32 vcc, v202, v200
	s_waitcnt vmcnt(17)
	v_pk_fma_f32 v[38:39], v[244:245], v[38:39], v[44:45] op_sel_hi:[0,1,1] neg_lo:[1,0,0] neg_hi:[1,0,0]
	v_cvt_pk_bf16_f32 v38, v38, v39
	v_cndmask_b32_e64 v45, 0, 1.0, vcc
	v_cmp_eq_u32_e32 vcc, v203, v200
	s_nop 1
	v_cndmask_b32_e64 v44, 0, 1.0, vcc
	v_pk_fma_f32 v[40:41], v[244:245], v[40:41], v[44:45] op_sel_hi:[0,1,1] neg_lo:[1,0,0] neg_hi:[1,0,0]
	v_cvt_pk_bf16_f32 v39, v40, v41
	ds_write_b64 v186, v[38:39] offset:3264
	v_cmp_eq_u32_e32 vcc, v133, v201
	s_nop 1
	v_cndmask_b32_e64 v40, 0, 1.0, vcc
	v_cmp_eq_u32_e32 vcc, v135, v201
	s_nop 1
	v_cndmask_b32_e64 v41, 0, 1.0, vcc
	v_cmp_eq_u32_e32 vcc, v202, v201
	s_waitcnt vmcnt(16)
	v_pk_fma_f32 v[34:35], v[246:247], v[34:35], v[40:41] op_sel_hi:[0,1,1] neg_lo:[1,0,0] neg_hi:[1,0,0]
	v_cvt_pk_bf16_f32 v34, v34, v35
	v_cndmask_b32_e64 v41, 0, 1.0, vcc
	v_cmp_eq_u32_e32 vcc, v203, v201
	s_nop 1
	v_cndmask_b32_e64 v40, 0, 1.0, vcc
	v_pk_fma_f32 v[36:37], v[246:247], v[36:37], v[40:41] op_sel_hi:[0,1,1] neg_lo:[1,0,0] neg_hi:[1,0,0]
	v_cvt_pk_bf16_f32 v35, v36, v37
	ds_write_b64 v186, v[34:35] offset:3808
	ds_read_b32 v232, v187 offset:0
	ds_read_b32 v234, v187 offset:8
	ds_read_b32 v236, v187 offset:16
	ds_read_b32 v238, v187 offset:24
	ds_read_b32 v240, v187 offset:32
	ds_read_b32 v242, v187 offset:40
	ds_read_b32 v244, v187 offset:48
	ds_read_b32 v246, v187 offset:56
	ds_read_b128 v[34:37], v1
	ds_read_b128 v[38:41], v1 offset:64
	ds_read_b128 v[42:45], v1 offset:128
	ds_read_b128 v[46:49], v1 offset:192
	v_mov_b32_e32 v106, v189
	v_add_u32_e32 v107, 1, v106
	v_cmp_eq_u32_e32 vcc, v106, v132
	v_add_u32_e32 v108, 3, v106
	v_add_u32_e32 v109, 2, v106
	v_cndmask_b32_e64 v84, 0, 1.0, vcc
	v_cmp_eq_u32_e32 vcc, v107, v132
	s_nop 1
	v_cndmask_b32_e64 v85, 0, 1.0, vcc
	v_cmp_eq_u32_e32 vcc, v108, v132
	s_waitcnt lgkmcnt(0)
	s_waitcnt vmcnt(15)
	v_pk_fma_f32 v[94:95], v[232:233], v[118:119], v[84:85] op_sel_hi:[0,1,1] neg_lo:[1,0,0] neg_hi:[1,0,0]
	v_cvt_pk_bf16_f32 v94, v94, v95
	v_cndmask_b32_e64 v97, 0, 1.0, vcc
	v_cmp_eq_u32_e32 vcc, v109, v132
	s_nop 1
	v_cndmask_b32_e64 v96, 0, 1.0, vcc
	v_pk_fma_f32 v[82:83], v[232:233], v[120:121], v[96:97] op_sel_hi:[0,1,1] neg_lo:[1,0,0] neg_hi:[1,0,0]
	v_cvt_pk_bf16_f32 v95, v82, v83
	ds_write_b64 v186, v[94:95]
	v_cmp_eq_u32_e32 vcc, v106, v193
	s_nop 1
	v_cndmask_b32_e64 v94, 0, 1.0, vcc
	v_cmp_eq_u32_e32 vcc, v107, v193
	s_nop 1
	v_cndmask_b32_e64 v95, 0, 1.0, vcc
	v_cmp_eq_u32_e32 vcc, v108, v193
	s_waitcnt vmcnt(14)
	v_pk_fma_f32 v[94:95], v[234:235], v[110:111], v[94:95] op_sel_hi:[0,1,1] neg_lo:[1,0,0] neg_hi:[1,0,0]
	v_cvt_pk_bf16_f32 v94, v94, v95
	v_cndmask_b32_e64 v85, 0, 1.0, vcc
	v_pk_fma_f32 v[82:83], v[234:235], v[112:113], v[84:85] op_sel_hi:[0,1,1] neg_lo:[1,0,0] neg_hi:[1,0,0]
	v_cvt_pk_bf16_f32 v95, v82, v83
	ds_write_b64 v186, v[94:95] offset:544
	v_cmp_eq_u32_e32 vcc, v106, v192
	s_nop 1
	v_cndmask_b32_e64 v84, 0, 1.0, vcc
	v_cmp_eq_u32_e32 vcc, v107, v192
	s_nop 1
	v_cndmask_b32_e64 v85, 0, 1.0, vcc
	v_cmp_eq_u32_e32 vcc, v108, v192
	s_waitcnt vmcnt(13)
	v_pk_fma_f32 v[84:85], v[236:237], v[98:99], v[84:85] op_sel_hi:[0,1,1] neg_lo:[1,0,0] neg_hi:[1,0,0]
	v_cvt_pk_bf16_f32 v84, v84, v85
	v_cndmask_b32_e64 v95, 0, 1.0, vcc
	v_cmp_eq_u32_e32 vcc, v109, v192
	s_nop 1
	v_cndmask_b32_e64 v94, 0, 1.0, vcc
	v_pk_fma_f32 v[82:83], v[236:237], v[100:101], v[94:95] op_sel_hi:[0,1,1] neg_lo:[1,0,0] neg_hi:[1,0,0]
	v_cvt_pk_bf16_f32 v85, v82, v83
	ds_write_b64 v186, v[84:85] offset:1088
	v_cmp_eq_u32_e32 vcc, v106, v190
	s_nop 1
	v_cndmask_b32_e64 v84, 0, 1.0, vcc
	v_cmp_eq_u32_e32 vcc, v107, v190
	s_nop 1
	v_cndmask_b32_e64 v85, 0, 1.0, vcc
	v_cmp_eq_u32_e32 vcc, v108, v190
	s_waitcnt vmcnt(12)
	v_pk_fma_f32 v[84:85], v[238:239], v[86:87], v[84:85] op_sel_hi:[0,1,1] neg_lo:[1,0,0] neg_hi:[1,0,0]
	v_cvt_pk_bf16_f32 v84, v84, v85
	v_cndmask_b32_e64 v87, 0, 1.0, vcc
	v_cmp_eq_u32_e32 vcc, v109, v190
	s_nop 1
	v_cndmask_b32_e64 v86, 0, 1.0, vcc
	v_pk_fma_f32 v[82:83], v[238:239], v[88:89], v[86:87] op_sel_hi:[0,1,1] neg_lo:[1,0,0] neg_hi:[1,0,0]
	v_cvt_pk_bf16_f32 v85, v82, v83
	ds_write_b64 v186, v[84:85] offset:1632
	v_cmp_eq_u32_e32 vcc, v106, v149
	s_nop 1
	v_cndmask_b32_e64 v84, 0, 1.0, vcc
	v_cmp_eq_u32_e32 vcc, v107, v149
	s_nop 1
	v_cndmask_b32_e64 v85, 0, 1.0, vcc
	v_cmp_eq_u32_e32 vcc, v108, v149
	s_waitcnt vmcnt(11)
	v_pk_fma_f32 v[62:63], v[240:241], v[62:63], v[84:85] op_sel_hi:[0,1,1] neg_lo:[1,0,0] neg_hi:[1,0,0]
	v_cvt_pk_bf16_f32 v62, v62, v63
	v_cndmask_b32_e64 v85, 0, 1.0, vcc
	v_cmp_eq_u32_e32 vcc, v109, v149
	s_nop 1
	v_cndmask_b32_e64 v84, 0, 1.0, vcc
	v_pk_fma_f32 v[64:65], v[240:241], v[64:65], v[84:85] op_sel_hi:[0,1,1] neg_lo:[1,0,0] neg_hi:[1,0,0]
	v_cvt_pk_bf16_f32 v63, v64, v65
	ds_write_b64 v186, v[62:63] offset:2176
	v_cmp_eq_u32_e32 vcc, v106, v148
	s_nop 1
	v_cndmask_b32_e64 v64, 0, 1.0, vcc
	v_cmp_eq_u32_e32 vcc, v107, v148
	s_nop 1
	v_cndmask_b32_e64 v65, 0, 1.0, vcc
	v_cmp_eq_u32_e32 vcc, v108, v148
	s_waitcnt vmcnt(10)
	v_pk_fma_f32 v[58:59], v[242:243], v[58:59], v[64:65] op_sel_hi:[0,1,1] neg_lo:[1,0,0] neg_hi:[1,0,0]
	v_cvt_pk_bf16_f32 v58, v58, v59
	v_cndmask_b32_e64 v65, 0, 1.0, vcc
	v_cmp_eq_u32_e32 vcc, v109, v148
	s_nop 1
	v_cndmask_b32_e64 v64, 0, 1.0, vcc
	v_pk_fma_f32 v[60:61], v[242:243], v[60:61], v[64:65] op_sel_hi:[0,1,1] neg_lo:[1,0,0] neg_hi:[1,0,0]
	v_cvt_pk_bf16_f32 v59, v60, v61
	ds_write_b64 v186, v[58:59] offset:2720
	v_cmp_eq_u32_e32 vcc, v106, v147
	s_nop 1
	v_cndmask_b32_e64 v60, 0, 1.0, vcc
	v_cmp_eq_u32_e32 vcc, v107, v147
	s_nop 1
	v_cndmask_b32_e64 v61, 0, 1.0, vcc
	v_cmp_eq_u32_e32 vcc, v108, v147
	s_waitcnt vmcnt(9)
	v_pk_fma_f32 v[54:55], v[244:245], v[54:55], v[60:61] op_sel_hi:[0,1,1] neg_lo:[1,0,0] neg_hi:[1,0,0]
	v_cvt_pk_bf16_f32 v54, v54, v55
	v_cndmask_b32_e64 v61, 0, 1.0, vcc
	v_cmp_eq_u32_e32 vcc, v109, v147
	s_nop 1
	v_cndmask_b32_e64 v60, 0, 1.0, vcc
	v_pk_fma_f32 v[56:57], v[244:245], v[56:57], v[60:61] op_sel_hi:[0,1,1] neg_lo:[1,0,0] neg_hi:[1,0,0]
	v_cvt_pk_bf16_f32 v55, v56, v57
	ds_write_b64 v186, v[54:55] offset:3264
	v_cmp_eq_u32_e32 vcc, v106, v146
	s_nop 1
	v_cndmask_b32_e64 v56, 0, 1.0, vcc
	v_cmp_eq_u32_e32 vcc, v107, v146
	s_nop 1
	v_cndmask_b32_e64 v57, 0, 1.0, vcc
	v_cmp_eq_u32_e32 vcc, v108, v146
	s_waitcnt vmcnt(8)
	v_pk_fma_f32 v[50:51], v[246:247], v[50:51], v[56:57] op_sel_hi:[0,1,1] neg_lo:[1,0,0] neg_hi:[1,0,0]
	v_cvt_pk_bf16_f32 v50, v50, v51
	v_cndmask_b32_e64 v57, 0, 1.0, vcc
	v_cmp_eq_u32_e32 vcc, v109, v146
	s_nop 1
	v_cndmask_b32_e64 v56, 0, 1.0, vcc
	v_pk_fma_f32 v[52:53], v[246:247], v[52:53], v[56:57] op_sel_hi:[0,1,1] neg_lo:[1,0,0] neg_hi:[1,0,0]
	v_cvt_pk_bf16_f32 v51, v52, v53
	ds_write_b64 v186, v[50:51] offset:3808
	ds_read_b32 v232, v187 offset:64
	ds_read_b32 v234, v187 offset:72
	ds_read_b32 v236, v187 offset:80
	ds_read_b32 v238, v187 offset:88
	ds_read_b32 v240, v187 offset:96
	ds_read_b32 v242, v187 offset:104
	ds_read_b32 v244, v187 offset:112
	ds_read_b32 v246, v187 offset:120
	ds_read_b128 v[50:53], v1
	ds_read_b128 v[54:57], v1 offset:64
	ds_read_b128 v[58:61], v1 offset:128
	ds_read_b128 v[62:65], v1 offset:192
	v_lshl_add_u64 v[82:83], v[168:169], 0, s[8:9]
	v_lshl_add_u64 v[84:85], v[170:171], 0, s[8:9]
	v_lshl_add_u64 v[86:87], v[172:173], 0, s[8:9]
	v_lshl_add_u64 v[88:89], v[174:175], 0, s[8:9]
	v_lshl_add_u64 v[94:95], v[176:177], 0, s[8:9]
	v_lshl_add_u64 v[96:97], v[178:179], 0, s[8:9]
	v_lshl_add_u64 v[122:123], v[180:181], 0, s[8:9]
	v_lshl_add_u64 v[124:125], v[182:183], 0, s[8:9]
	global_load_dwordx4 v[134:137], v[82:83], off nt
	global_load_dwordx4 v[118:121], v[84:85], off nt
	global_load_dwordx4 v[110:113], v[86:87], off nt
	global_load_dwordx4 v[106:109], v[88:89], off nt
	global_load_dwordx4 v[98:101], v[94:95], off nt
	s_nop 0
	global_load_dwordx4 v[94:97], v[96:97], off nt
	s_nop 0
	global_load_dwordx4 v[86:89], v[122:123], off nt
	global_load_dwordx4 v[82:85], v[124:125], off nt
	v_mov_b32_e32 v132, v189
	v_add_u32_e32 v133, 1, v132
	v_cmp_eq_u32_e32 vcc, v132, v138
	v_add_u32_e32 v146, 3, v132
	v_add_u32_e32 v147, 2, v132
	v_cndmask_b32_e64 v124, 0, 1.0, vcc
	v_cmp_eq_u32_e32 vcc, v133, v138
	s_nop 1
	v_cndmask_b32_e64 v125, 0, 1.0, vcc
	v_cmp_eq_u32_e32 vcc, v146, v138
	s_waitcnt lgkmcnt(0)
	s_waitcnt vmcnt(15)
	v_pk_fma_f32 v[124:125], v[232:233], v[126:127], v[124:125] op_sel_hi:[0,1,1] neg_lo:[1,0,0] neg_hi:[1,0,0]
	v_cvt_pk_bf16_f32 v124, v124, v125
	v_cndmask_b32_e64 v127, 0, 1.0, vcc
	v_cmp_eq_u32_e32 vcc, v147, v138
	s_nop 1
	v_cndmask_b32_e64 v126, 0, 1.0, vcc
	v_pk_fma_f32 v[122:123], v[232:233], v[128:129], v[126:127] op_sel_hi:[0,1,1] neg_lo:[1,0,0] neg_hi:[1,0,0]
	v_cvt_pk_bf16_f32 v125, v122, v123
	ds_write_b64 v186, v[124:125]
	v_cmp_eq_u32_e32 vcc, v132, v139
	s_nop 1
	v_cndmask_b32_e64 v124, 0, 1.0, vcc
	v_cmp_eq_u32_e32 vcc, v133, v139
	s_nop 1
	v_cndmask_b32_e64 v125, 0, 1.0, vcc
	v_cmp_eq_u32_e32 vcc, v146, v139
	s_waitcnt vmcnt(14)
	v_pk_fma_f32 v[114:115], v[234:235], v[114:115], v[124:125] op_sel_hi:[0,1,1] neg_lo:[1,0,0] neg_hi:[1,0,0]
	v_cvt_pk_bf16_f32 v114, v114, v115
	v_cndmask_b32_e64 v125, 0, 1.0, vcc
	v_cmp_eq_u32_e32 vcc, v147, v139
	s_nop 1
	v_cndmask_b32_e64 v124, 0, 1.0, vcc
	v_pk_fma_f32 v[116:117], v[234:235], v[116:117], v[124:125] op_sel_hi:[0,1,1] neg_lo:[1,0,0] neg_hi:[1,0,0]
	v_cvt_pk_bf16_f32 v115, v116, v117
	ds_write_b64 v186, v[114:115] offset:544
	v_cmp_eq_u32_e32 vcc, v132, v140
	s_nop 1
	v_cndmask_b32_e64 v116, 0, 1.0, vcc
	v_cmp_eq_u32_e32 vcc, v133, v140
	s_nop 1
	v_cndmask_b32_e64 v117, 0, 1.0, vcc
	v_cmp_eq_u32_e32 vcc, v146, v140
	s_waitcnt vmcnt(13)
	v_pk_fma_f32 v[102:103], v[236:237], v[102:103], v[116:117] op_sel_hi:[0,1,1] neg_lo:[1,0,0] neg_hi:[1,0,0]
	v_cvt_pk_bf16_f32 v102, v102, v103
	v_cndmask_b32_e64 v117, 0, 1.0, vcc
	v_cmp_eq_u32_e32 vcc, v147, v140
	s_nop 1
	v_cndmask_b32_e64 v116, 0, 1.0, vcc
	v_pk_fma_f32 v[104:105], v[236:237], v[104:105], v[116:117] op_sel_hi:[0,1,1] neg_lo:[1,0,0] neg_hi:[1,0,0]
	v_cvt_pk_bf16_f32 v103, v104, v105
	ds_write_b64 v186, v[102:103] offset:1088
	v_cmp_eq_u32_e32 vcc, v132, v141
	s_nop 1
	v_cndmask_b32_e64 v104, 0, 1.0, vcc
	v_cmp_eq_u32_e32 vcc, v133, v141
	s_nop 1
	v_cndmask_b32_e64 v105, 0, 1.0, vcc
	v_cmp_eq_u32_e32 vcc, v146, v141
	s_waitcnt vmcnt(12)
	v_pk_fma_f32 v[90:91], v[238:239], v[90:91], v[104:105] op_sel_hi:[0,1,1] neg_lo:[1,0,0] neg_hi:[1,0,0]
	v_cvt_pk_bf16_f32 v90, v90, v91
	v_cndmask_b32_e64 v105, 0, 1.0, vcc
	v_cmp_eq_u32_e32 vcc, v147, v141
	s_nop 1
	v_cndmask_b32_e64 v104, 0, 1.0, vcc
	v_pk_fma_f32 v[92:93], v[238:239], v[92:93], v[104:105] op_sel_hi:[0,1,1] neg_lo:[1,0,0] neg_hi:[1,0,0]
	v_cvt_pk_bf16_f32 v91, v92, v93
	ds_write_b64 v186, v[90:91] offset:1632
	v_cmp_eq_u32_e32 vcc, v132, v142
	s_nop 1
	v_cndmask_b32_e64 v92, 0, 1.0, vcc
	v_cmp_eq_u32_e32 vcc, v133, v142
	s_nop 1
	v_cndmask_b32_e64 v93, 0, 1.0, vcc
	v_cmp_eq_u32_e32 vcc, v146, v142
	s_waitcnt vmcnt(11)
	v_pk_fma_f32 v[78:79], v[240:241], v[78:79], v[92:93] op_sel_hi:[0,1,1] neg_lo:[1,0,0] neg_hi:[1,0,0]
	v_cvt_pk_bf16_f32 v78, v78, v79
	v_cndmask_b32_e64 v93, 0, 1.0, vcc
	v_cmp_eq_u32_e32 vcc, v147, v142
	s_nop 1
	v_cndmask_b32_e64 v92, 0, 1.0, vcc
	v_pk_fma_f32 v[80:81], v[240:241], v[80:81], v[92:93] op_sel_hi:[0,1,1] neg_lo:[1,0,0] neg_hi:[1,0,0]
	v_cvt_pk_bf16_f32 v79, v80, v81
	ds_write_b64 v186, v[78:79] offset:2176
	v_cmp_eq_u32_e32 vcc, v132, v143
	s_nop 1
	v_cndmask_b32_e64 v80, 0, 1.0, vcc
	v_cmp_eq_u32_e32 vcc, v133, v143
	s_nop 1
	v_cndmask_b32_e64 v81, 0, 1.0, vcc
	v_cmp_eq_u32_e32 vcc, v146, v143
	s_waitcnt vmcnt(10)
	v_pk_fma_f32 v[74:75], v[242:243], v[74:75], v[80:81] op_sel_hi:[0,1,1] neg_lo:[1,0,0] neg_hi:[1,0,0]
	v_cvt_pk_bf16_f32 v74, v74, v75
	v_cndmask_b32_e64 v81, 0, 1.0, vcc
	v_cmp_eq_u32_e32 vcc, v147, v143
	s_nop 1
	v_cndmask_b32_e64 v80, 0, 1.0, vcc
	v_pk_fma_f32 v[76:77], v[242:243], v[76:77], v[80:81] op_sel_hi:[0,1,1] neg_lo:[1,0,0] neg_hi:[1,0,0]
	v_cvt_pk_bf16_f32 v75, v76, v77
	ds_write_b64 v186, v[74:75] offset:2720
	v_cmp_eq_u32_e32 vcc, v132, v144
	s_nop 1
	v_cndmask_b32_e64 v76, 0, 1.0, vcc
	v_cmp_eq_u32_e32 vcc, v133, v144
	s_nop 1
	v_cndmask_b32_e64 v77, 0, 1.0, vcc
	v_cmp_eq_u32_e32 vcc, v146, v144
	s_waitcnt vmcnt(9)
	v_pk_fma_f32 v[70:71], v[244:245], v[70:71], v[76:77] op_sel_hi:[0,1,1] neg_lo:[1,0,0] neg_hi:[1,0,0]
	v_cvt_pk_bf16_f32 v70, v70, v71
	v_cndmask_b32_e64 v77, 0, 1.0, vcc
	v_cmp_eq_u32_e32 vcc, v147, v144
	s_nop 1
	v_cndmask_b32_e64 v76, 0, 1.0, vcc
	v_pk_fma_f32 v[72:73], v[244:245], v[72:73], v[76:77] op_sel_hi:[0,1,1] neg_lo:[1,0,0] neg_hi:[1,0,0]
	v_cvt_pk_bf16_f32 v71, v72, v73
	ds_write_b64 v186, v[70:71] offset:3264
	v_cmp_eq_u32_e32 vcc, v132, v145
	s_nop 1
	v_cndmask_b32_e64 v72, 0, 1.0, vcc
	v_cmp_eq_u32_e32 vcc, v133, v145
	s_nop 1
	v_cndmask_b32_e64 v73, 0, 1.0, vcc
	v_cmp_eq_u32_e32 vcc, v146, v145
	s_waitcnt vmcnt(8)
	v_pk_fma_f32 v[66:67], v[246:247], v[66:67], v[72:73] op_sel_hi:[0,1,1] neg_lo:[1,0,0] neg_hi:[1,0,0]
	v_cvt_pk_bf16_f32 v66, v66, v67
	v_cndmask_b32_e64 v73, 0, 1.0, vcc
	v_cmp_eq_u32_e32 vcc, v147, v145
	s_nop 1
	v_cndmask_b32_e64 v72, 0, 1.0, vcc
	v_pk_fma_f32 v[68:69], v[246:247], v[68:69], v[72:73] op_sel_hi:[0,1,1] neg_lo:[1,0,0] neg_hi:[1,0,0]
	v_cvt_pk_bf16_f32 v67, v68, v69
	ds_write_b64 v186, v[66:67] offset:3808
	ds_read_b32 v232, v187 offset:128
	ds_read_b32 v234, v187 offset:136
	ds_read_b32 v236, v187 offset:144
	ds_read_b32 v238, v187 offset:152
	ds_read_b32 v240, v187 offset:160
	ds_read_b32 v242, v187 offset:168
	ds_read_b32 v244, v187 offset:176
	ds_read_b32 v246, v187 offset:184
	ds_read_b128 v[66:69], v1
	ds_read_b128 v[70:73], v1 offset:64
	ds_read_b128 v[74:77], v1 offset:128
	ds_read_b128 v[78:81], v1 offset:192
	v_lshl_add_u64 v[90:91], v[130:131], 0, s[0:1]
	v_add_co_u32_e32 v92, vcc, s7, v90
	s_nop 1
	v_addc_co_u32_e32 v93, vcc, 0, v91, vcc
	global_load_dwordx4 v[146:149], v[90:91], off nt
	global_load_dwordx4 v[142:145], v[92:93], off nt
	v_add_co_u32_e32 v92, vcc, s36, v90
	s_nop 1
	v_addc_co_u32_e32 v93, vcc, 0, v91, vcc
	v_add_co_u32_e32 v102, vcc, s37, v90
	s_nop 1
	v_addc_co_u32_e32 v103, vcc, 0, v91, vcc
	global_load_dwordx4 v[138:141], v[92:93], off nt
	global_load_dwordx4 v[130:133], v[102:103], off nt
	v_add_co_u32_e32 v92, vcc, s38, v90
	s_nop 1
	v_addc_co_u32_e32 v93, vcc, 0, v91, vcc
	v_add_co_u32_e32 v102, vcc, s39, v90
	s_nop 1
	v_addc_co_u32_e32 v103, vcc, 0, v91, vcc
	global_load_dwordx4 v[126:129], v[92:93], off nt
	global_load_dwordx4 v[122:125], v[102:103], off nt
	v_add_co_u32_e32 v92, vcc, s41, v90
	s_nop 1
	v_addc_co_u32_e32 v93, vcc, 0, v91, vcc
	v_add_co_u32_e32 v90, vcc, s42, v90
	s_nop 1
	v_addc_co_u32_e32 v91, vcc, 0, v91, vcc
	global_load_dwordx4 v[114:117], v[92:93], off nt
	global_load_dwordx4 v[102:105], v[90:91], off nt
	v_add_u32_e32 v190, 1, v189
	v_cmp_eq_u32_e32 vcc, v189, v194
	v_add_u32_e32 v192, 3, v189
	v_add_u32_e32 v193, 2, v189
	v_cndmask_b32_e64 v92, 0, 1.0, vcc
	v_cmp_eq_u32_e32 vcc, v190, v194
	s_nop 1
	v_cndmask_b32_e64 v93, 0, 1.0, vcc
	v_cmp_eq_u32_e32 vcc, v192, v194
	s_waitcnt lgkmcnt(0)
	s_waitcnt vmcnt(15)
	v_pk_fma_f32 v[92:93], v[232:233], v[134:135], v[92:93] op_sel_hi:[0,1,1] neg_lo:[1,0,0] neg_hi:[1,0,0]
	v_cvt_pk_bf16_f32 v92, v92, v93
	v_cndmask_b32_e64 v135, 0, 1.0, vcc
	v_cmp_eq_u32_e32 vcc, v193, v194
	s_nop 1
	v_cndmask_b32_e64 v134, 0, 1.0, vcc
	v_pk_fma_f32 v[90:91], v[232:233], v[136:137], v[134:135] op_sel_hi:[0,1,1] neg_lo:[1,0,0] neg_hi:[1,0,0]
	v_cvt_pk_bf16_f32 v93, v90, v91
	ds_write_b64 v186, v[92:93]
	v_cmp_eq_u32_e32 vcc, v189, v195
	s_nop 1
	v_cndmask_b32_e64 v92, 0, 1.0, vcc
	v_cmp_eq_u32_e32 vcc, v190, v195
	s_nop 1
	v_cndmask_b32_e64 v93, 0, 1.0, vcc
	v_cmp_eq_u32_e32 vcc, v192, v195
	s_waitcnt vmcnt(14)
	v_pk_fma_f32 v[92:93], v[234:235], v[118:119], v[92:93] op_sel_hi:[0,1,1] neg_lo:[1,0,0] neg_hi:[1,0,0]
	v_cvt_pk_bf16_f32 v92, v92, v93
	v_cndmask_b32_e64 v119, 0, 1.0, vcc
	v_cmp_eq_u32_e32 vcc, v193, v195
	s_nop 1
	v_cndmask_b32_e64 v118, 0, 1.0, vcc
	v_pk_fma_f32 v[90:91], v[234:235], v[120:121], v[118:119] op_sel_hi:[0,1,1] neg_lo:[1,0,0] neg_hi:[1,0,0]
	v_cvt_pk_bf16_f32 v93, v90, v91
	ds_write_b64 v186, v[92:93] offset:544
	v_cmp_eq_u32_e32 vcc, v189, v196
	s_nop 1
	v_cndmask_b32_e64 v92, 0, 1.0, vcc
	v_cmp_eq_u32_e32 vcc, v190, v196
	s_nop 1
	v_cndmask_b32_e64 v93, 0, 1.0, vcc
	v_cmp_eq_u32_e32 vcc, v192, v196
	s_waitcnt vmcnt(13)
	v_pk_fma_f32 v[92:93], v[236:237], v[110:111], v[92:93] op_sel_hi:[0,1,1] neg_lo:[1,0,0] neg_hi:[1,0,0]
	v_cvt_pk_bf16_f32 v92, v92, v93
	v_cndmask_b32_e64 v111, 0, 1.0, vcc
	v_cmp_eq_u32_e32 vcc, v193, v196
	s_nop 1
	v_cndmask_b32_e64 v110, 0, 1.0, vcc
	v_pk_fma_f32 v[90:91], v[236:237], v[112:113], v[110:111] op_sel_hi:[0,1,1] neg_lo:[1,0,0] neg_hi:[1,0,0]
	v_cvt_pk_bf16_f32 v93, v90, v91
	ds_write_b64 v186, v[92:93] offset:1088
	v_cmp_eq_u32_e32 vcc, v189, v197
	s_nop 1
	v_cndmask_b32_e64 v92, 0, 1.0, vcc
	v_cmp_eq_u32_e32 vcc, v190, v197
	s_nop 1
	v_cndmask_b32_e64 v93, 0, 1.0, vcc
	v_cmp_eq_u32_e32 vcc, v192, v197
	s_waitcnt vmcnt(12)
	v_pk_fma_f32 v[92:93], v[238:239], v[106:107], v[92:93] op_sel_hi:[0,1,1] neg_lo:[1,0,0] neg_hi:[1,0,0]
	v_cvt_pk_bf16_f32 v92, v92, v93
	v_cndmask_b32_e64 v107, 0, 1.0, vcc
	v_cmp_eq_u32_e32 vcc, v193, v197
	s_nop 1
	v_cndmask_b32_e64 v106, 0, 1.0, vcc
	v_pk_fma_f32 v[90:91], v[238:239], v[108:109], v[106:107] op_sel_hi:[0,1,1] neg_lo:[1,0,0] neg_hi:[1,0,0]
	v_cvt_pk_bf16_f32 v93, v90, v91
	ds_write_b64 v186, v[92:93] offset:1632
	v_cmp_eq_u32_e32 vcc, v189, v198
	s_nop 1
	v_cndmask_b32_e64 v92, 0, 1.0, vcc
	v_cmp_eq_u32_e32 vcc, v190, v198
	s_nop 1
	v_cndmask_b32_e64 v93, 0, 1.0, vcc
	v_cmp_eq_u32_e32 vcc, v192, v198
	s_waitcnt vmcnt(11)
	v_pk_fma_f32 v[92:93], v[240:241], v[98:99], v[92:93] op_sel_hi:[0,1,1] neg_lo:[1,0,0] neg_hi:[1,0,0]
	v_cvt_pk_bf16_f32 v92, v92, v93
	v_cndmask_b32_e64 v99, 0, 1.0, vcc
	v_cmp_eq_u32_e32 vcc, v193, v198
	s_nop 1
	v_cndmask_b32_e64 v98, 0, 1.0, vcc
	v_pk_fma_f32 v[90:91], v[240:241], v[100:101], v[98:99] op_sel_hi:[0,1,1] neg_lo:[1,0,0] neg_hi:[1,0,0]
	v_cvt_pk_bf16_f32 v93, v90, v91
	ds_write_b64 v186, v[92:93] offset:2176
	v_cmp_eq_u32_e32 vcc, v189, v199
	s_nop 1
	v_cndmask_b32_e64 v92, 0, 1.0, vcc
	v_cmp_eq_u32_e32 vcc, v190, v199
	s_nop 1
	v_cndmask_b32_e64 v93, 0, 1.0, vcc
	v_cmp_eq_u32_e32 vcc, v192, v199
	s_waitcnt vmcnt(10)
	v_pk_fma_f32 v[92:93], v[242:243], v[94:95], v[92:93] op_sel_hi:[0,1,1] neg_lo:[1,0,0] neg_hi:[1,0,0]
	v_cvt_pk_bf16_f32 v92, v92, v93
	v_cndmask_b32_e64 v95, 0, 1.0, vcc
	v_cmp_eq_u32_e32 vcc, v193, v199
	s_nop 1
	v_cndmask_b32_e64 v94, 0, 1.0, vcc
	v_pk_fma_f32 v[90:91], v[242:243], v[96:97], v[94:95] op_sel_hi:[0,1,1] neg_lo:[1,0,0] neg_hi:[1,0,0]
	v_cvt_pk_bf16_f32 v93, v90, v91
	ds_write_b64 v186, v[92:93] offset:2720
	v_cmp_eq_u32_e32 vcc, v189, v200
	s_nop 1
	v_cndmask_b32_e64 v92, 0, 1.0, vcc
	v_cmp_eq_u32_e32 vcc, v190, v200
	s_nop 1
	v_cndmask_b32_e64 v93, 0, 1.0, vcc
	v_cmp_eq_u32_e32 vcc, v192, v200
	s_waitcnt vmcnt(9)
	v_pk_fma_f32 v[86:87], v[244:245], v[86:87], v[92:93] op_sel_hi:[0,1,1] neg_lo:[1,0,0] neg_hi:[1,0,0]
	v_cvt_pk_bf16_f32 v86, v86, v87
	v_cndmask_b32_e64 v93, 0, 1.0, vcc
	v_cmp_eq_u32_e32 vcc, v193, v200
	s_nop 1
	v_cndmask_b32_e64 v92, 0, 1.0, vcc
	v_pk_fma_f32 v[88:89], v[244:245], v[88:89], v[92:93] op_sel_hi:[0,1,1] neg_lo:[1,0,0] neg_hi:[1,0,0]
	v_cvt_pk_bf16_f32 v87, v88, v89
	ds_write_b64 v186, v[86:87] offset:3264
	v_cmp_eq_u32_e32 vcc, v189, v201
	s_nop 1
	v_cndmask_b32_e64 v88, 0, 1.0, vcc
	v_cmp_eq_u32_e32 vcc, v190, v201
	s_nop 1
	v_cndmask_b32_e64 v89, 0, 1.0, vcc
	v_cmp_eq_u32_e32 vcc, v192, v201
	s_waitcnt vmcnt(8)
	v_pk_fma_f32 v[82:83], v[246:247], v[82:83], v[88:89] op_sel_hi:[0,1,1] neg_lo:[1,0,0] neg_hi:[1,0,0]
	v_cvt_pk_bf16_f32 v82, v82, v83
	v_cndmask_b32_e64 v89, 0, 1.0, vcc
	v_cmp_eq_u32_e32 vcc, v193, v201
	s_nop 1
	v_cndmask_b32_e64 v88, 0, 1.0, vcc
	v_pk_fma_f32 v[84:85], v[246:247], v[84:85], v[88:89] op_sel_hi:[0,1,1] neg_lo:[1,0,0] neg_hi:[1,0,0]
	v_cvt_pk_bf16_f32 v83, v84, v85
	ds_write_b64 v186, v[82:83] offset:3808
	ds_read_b32 v232, v187 offset:0
	ds_read_b32 v234, v187 offset:8
	ds_read_b32 v236, v187 offset:16
	ds_read_b32 v238, v187 offset:24
	ds_read_b32 v240, v187 offset:32
	ds_read_b32 v242, v187 offset:40
	ds_read_b32 v244, v187 offset:48
	ds_read_b32 v246, v187 offset:56
	ds_read_b128 v[82:85], v1
	ds_read_b128 v[86:89], v1 offset:64
	ds_read_b128 v[90:93], v1 offset:128
	ds_read_b128 v[94:97], v1 offset:192
	v_lshl_add_u64 v[98:99], v[150:151], 0, s[0:1]
	v_lshl_add_u64 v[192:193], v[164:165], 0, s[0:1]
	v_lshl_add_u64 v[196:197], v[166:167], 0, s[0:1]
	v_lshl_add_u64 v[100:101], v[152:153], 0, s[0:1]
	v_lshl_add_u64 v[106:107], v[156:157], 0, s[0:1]
	v_lshl_add_u64 v[108:109], v[158:159], 0, s[0:1]
	v_lshl_add_u64 v[110:111], v[160:161], 0, s[0:1]
	v_lshl_add_u64 v[112:113], v[162:163], 0, s[0:1]
	global_load_dwordx4 v[118:121], v[98:99], off nt
	global_load_dwordx4 v[134:137], v[100:101], off nt
	global_load_dwordx4 v[150:153], v[106:107], off nt
	global_load_dwordx4 v[156:159], v[108:109], off nt
	global_load_dwordx4 v[160:163], v[110:111], off nt
	global_load_dwordx4 v[164:167], v[112:113], off nt
	s_nop 0
	global_load_dwordx4 v[192:195], v[192:193], off nt
	s_nop 0
	global_load_dwordx4 v[196:199], v[196:197], off nt
	v_mov_b32_e32 v98, v188
	s_waitcnt lgkmcnt(0)
	s_waitcnt vmcnt(15)
	v_pk_fma_f32 v[100:101], v[232:233], v[146:147], 0 op_sel_hi:[0,1,0] neg_lo:[1,0,0] neg_hi:[1,0,0]
	v_pk_fma_f32 v[98:99], v[232:233], v[148:149], 0 op_sel_hi:[0,1,0] neg_lo:[1,0,0] neg_hi:[1,0,0]
	v_cvt_pk_bf16_f32 v100, v100, v101
	v_cvt_pk_bf16_f32 v101, v98, v99
	ds_write_b64 v186, v[100:101]
	s_waitcnt vmcnt(14)
	v_pk_fma_f32 v[100:101], v[234:235], v[142:143], 0 op_sel_hi:[0,1,0] neg_lo:[1,0,0] neg_hi:[1,0,0]
	v_pk_fma_f32 v[98:99], v[234:235], v[144:145], 0 op_sel_hi:[0,1,0] neg_lo:[1,0,0] neg_hi:[1,0,0]
	v_cvt_pk_bf16_f32 v100, v100, v101
	v_cvt_pk_bf16_f32 v101, v98, v99
	ds_write_b64 v186, v[100:101] offset:544
	s_waitcnt vmcnt(13)
	v_pk_fma_f32 v[100:101], v[236:237], v[138:139], 0 op_sel_hi:[0,1,0] neg_lo:[1,0,0] neg_hi:[1,0,0]
	v_pk_fma_f32 v[98:99], v[236:237], v[140:141], 0 op_sel_hi:[0,1,0] neg_lo:[1,0,0] neg_hi:[1,0,0]
	v_cvt_pk_bf16_f32 v100, v100, v101
	v_cvt_pk_bf16_f32 v101, v98, v99
	ds_write_b64 v186, v[100:101] offset:1088
	s_waitcnt vmcnt(12)
	v_pk_fma_f32 v[100:101], v[238:239], v[130:131], 0 op_sel_hi:[0,1,0] neg_lo:[1,0,0] neg_hi:[1,0,0]
	v_pk_fma_f32 v[98:99], v[238:239], v[132:133], 0 op_sel_hi:[0,1,0] neg_lo:[1,0,0] neg_hi:[1,0,0]
	v_cvt_pk_bf16_f32 v100, v100, v101
	v_cvt_pk_bf16_f32 v101, v98, v99
	ds_write_b64 v186, v[100:101] offset:1632
	s_waitcnt vmcnt(11)
	v_pk_fma_f32 v[100:101], v[240:241], v[126:127], 0 op_sel_hi:[0,1,0] neg_lo:[1,0,0] neg_hi:[1,0,0]
	v_pk_fma_f32 v[98:99], v[240:241], v[128:129], 0 op_sel_hi:[0,1,0] neg_lo:[1,0,0] neg_hi:[1,0,0]
	v_cvt_pk_bf16_f32 v100, v100, v101
	v_cvt_pk_bf16_f32 v101, v98, v99
	ds_write_b64 v186, v[100:101] offset:2176
	s_waitcnt vmcnt(10)
	v_pk_fma_f32 v[100:101], v[242:243], v[122:123], 0 op_sel_hi:[0,1,0] neg_lo:[1,0,0] neg_hi:[1,0,0]
	v_pk_fma_f32 v[98:99], v[242:243], v[124:125], 0 op_sel_hi:[0,1,0] neg_lo:[1,0,0] neg_hi:[1,0,0]
	v_cvt_pk_bf16_f32 v100, v100, v101
	v_cvt_pk_bf16_f32 v101, v98, v99
	ds_write_b64 v186, v[100:101] offset:2720
	s_waitcnt vmcnt(9)
	v_pk_fma_f32 v[100:101], v[244:245], v[114:115], 0 op_sel_hi:[0,1,0] neg_lo:[1,0,0] neg_hi:[1,0,0]
	v_pk_fma_f32 v[98:99], v[244:245], v[116:117], 0 op_sel_hi:[0,1,0] neg_lo:[1,0,0] neg_hi:[1,0,0]
	v_cvt_pk_bf16_f32 v100, v100, v101
	v_cvt_pk_bf16_f32 v101, v98, v99
	ds_write_b64 v186, v[100:101] offset:3264
	s_waitcnt vmcnt(8)
	v_pk_fma_f32 v[100:101], v[246:247], v[102:103], 0 op_sel_hi:[0,1,0] neg_lo:[1,0,0] neg_hi:[1,0,0]
	v_pk_fma_f32 v[98:99], v[246:247], v[104:105], 0 op_sel_hi:[0,1,0] neg_lo:[1,0,0] neg_hi:[1,0,0]
	v_cvt_pk_bf16_f32 v100, v100, v101
	v_cvt_pk_bf16_f32 v101, v98, v99
	ds_write_b64 v186, v[100:101] offset:3808
	ds_read_b32 v232, v187 offset:64
	ds_read_b32 v234, v187 offset:72
	ds_read_b32 v236, v187 offset:80
	ds_read_b32 v238, v187 offset:88
	ds_read_b32 v240, v187 offset:96
	ds_read_b32 v242, v187 offset:104
	ds_read_b32 v244, v187 offset:112
	ds_read_b32 v246, v187 offset:120
	ds_read_b128 v[98:101], v1
	ds_read_b128 v[102:105], v1 offset:64
	ds_read_b128 v[106:109], v1 offset:128
	ds_read_b128 v[110:113], v1 offset:192
	v_lshl_add_u64 v[114:115], v[168:169], 0, s[0:1]
	v_lshl_add_u64 v[126:127], v[176:177], 0, s[0:1]
	v_lshl_add_u64 v[176:177], v[180:181], 0, s[0:1]
	v_lshl_add_u64 v[180:181], v[182:183], 0, s[0:1]
	v_lshl_add_u64 v[116:117], v[170:171], 0, s[0:1]
	v_lshl_add_u64 v[122:123], v[172:173], 0, s[0:1]
	v_lshl_add_u64 v[124:125], v[174:175], 0, s[0:1]
	v_lshl_add_u64 v[128:129], v[178:179], 0, s[0:1]
	global_load_dwordx4 v[130:133], v[114:115], off nt
	global_load_dwordx4 v[138:141], v[116:117], off nt
	global_load_dwordx4 v[142:145], v[122:123], off nt
	global_load_dwordx4 v[146:149], v[124:125], off nt
	global_load_dwordx4 v[168:171], v[126:127], off nt
	global_load_dwordx4 v[172:175], v[128:129], off nt
	s_nop 0
	global_load_dwordx4 v[176:179], v[176:177], off nt
	s_nop 0
	global_load_dwordx4 v[180:183], v[180:181], off nt
	v_mov_b32_e32 v114, v188
	s_waitcnt lgkmcnt(0)
	s_waitcnt vmcnt(15)
	v_pk_fma_f32 v[116:117], v[232:233], v[118:119], 0 op_sel_hi:[0,1,0] neg_lo:[1,0,0] neg_hi:[1,0,0]
	v_pk_fma_f32 v[114:115], v[232:233], v[120:121], 0 op_sel_hi:[0,1,0] neg_lo:[1,0,0] neg_hi:[1,0,0]
	v_cvt_pk_bf16_f32 v116, v116, v117
	v_cvt_pk_bf16_f32 v117, v114, v115
	ds_write_b64 v186, v[116:117]
	s_waitcnt vmcnt(14)
	v_pk_fma_f32 v[116:117], v[234:235], v[134:135], 0 op_sel_hi:[0,1,0] neg_lo:[1,0,0] neg_hi:[1,0,0]
	v_pk_fma_f32 v[114:115], v[234:235], v[136:137], 0 op_sel_hi:[0,1,0] neg_lo:[1,0,0] neg_hi:[1,0,0]
	v_cvt_pk_bf16_f32 v116, v116, v117
	v_cvt_pk_bf16_f32 v117, v114, v115
	ds_write_b64 v186, v[116:117] offset:544
	s_waitcnt vmcnt(13)
	v_pk_fma_f32 v[116:117], v[236:237], v[150:151], 0 op_sel_hi:[0,1,0] neg_lo:[1,0,0] neg_hi:[1,0,0]
	v_pk_fma_f32 v[114:115], v[236:237], v[152:153], 0 op_sel_hi:[0,1,0] neg_lo:[1,0,0] neg_hi:[1,0,0]
	v_cvt_pk_bf16_f32 v116, v116, v117
	v_cvt_pk_bf16_f32 v117, v114, v115
	ds_write_b64 v186, v[116:117] offset:1088
	s_waitcnt vmcnt(12)
	v_pk_fma_f32 v[116:117], v[238:239], v[156:157], 0 op_sel_hi:[0,1,0] neg_lo:[1,0,0] neg_hi:[1,0,0]
	v_pk_fma_f32 v[114:115], v[238:239], v[158:159], 0 op_sel_hi:[0,1,0] neg_lo:[1,0,0] neg_hi:[1,0,0]
	v_cvt_pk_bf16_f32 v116, v116, v117
	v_cvt_pk_bf16_f32 v117, v114, v115
	ds_write_b64 v186, v[116:117] offset:1632
	s_waitcnt vmcnt(11)
	v_pk_fma_f32 v[116:117], v[240:241], v[160:161], 0 op_sel_hi:[0,1,0] neg_lo:[1,0,0] neg_hi:[1,0,0]
	v_pk_fma_f32 v[114:115], v[240:241], v[162:163], 0 op_sel_hi:[0,1,0] neg_lo:[1,0,0] neg_hi:[1,0,0]
	v_cvt_pk_bf16_f32 v116, v116, v117
	v_cvt_pk_bf16_f32 v117, v114, v115
	ds_write_b64 v186, v[116:117] offset:2176
	s_waitcnt vmcnt(10)
	v_pk_fma_f32 v[116:117], v[242:243], v[164:165], 0 op_sel_hi:[0,1,0] neg_lo:[1,0,0] neg_hi:[1,0,0]
	v_pk_fma_f32 v[114:115], v[242:243], v[166:167], 0 op_sel_hi:[0,1,0] neg_lo:[1,0,0] neg_hi:[1,0,0]
	v_cvt_pk_bf16_f32 v116, v116, v117
	v_cvt_pk_bf16_f32 v117, v114, v115
	ds_write_b64 v186, v[116:117] offset:2720
	s_waitcnt vmcnt(9)
	v_pk_fma_f32 v[116:117], v[244:245], v[192:193], 0 op_sel_hi:[0,1,0] neg_lo:[1,0,0] neg_hi:[1,0,0]
	v_pk_fma_f32 v[114:115], v[244:245], v[194:195], 0 op_sel_hi:[0,1,0] neg_lo:[1,0,0] neg_hi:[1,0,0]
	v_cvt_pk_bf16_f32 v116, v116, v117
	v_cvt_pk_bf16_f32 v117, v114, v115
	ds_write_b64 v186, v[116:117] offset:3264
	s_waitcnt vmcnt(8)
	v_pk_fma_f32 v[116:117], v[246:247], v[196:197], 0 op_sel_hi:[0,1,0] neg_lo:[1,0,0] neg_hi:[1,0,0]
	v_pk_fma_f32 v[114:115], v[246:247], v[198:199], 0 op_sel_hi:[0,1,0] neg_lo:[1,0,0] neg_hi:[1,0,0]
	v_cvt_pk_bf16_f32 v116, v116, v117
	v_cvt_pk_bf16_f32 v117, v114, v115
	ds_write_b64 v186, v[116:117] offset:3808
	ds_read_b32 v232, v187 offset:128
	ds_read_b32 v234, v187 offset:136
	ds_read_b32 v236, v187 offset:144
	ds_read_b32 v238, v187 offset:152
	ds_read_b32 v240, v187 offset:160
	ds_read_b32 v242, v187 offset:168
	ds_read_b32 v244, v187 offset:176
	ds_read_b32 v246, v187 offset:184
	ds_read_b128 v[114:117], v1
	ds_read_b128 v[118:121], v1 offset:64
	ds_read_b128 v[122:125], v1 offset:128
	ds_read_b128 v[126:129], v1 offset:192
	s_waitcnt lgkmcnt(0)
	s_waitcnt vmcnt(7)
	v_pk_fma_f32 v[130:131], v[232:233], v[130:131], 0 op_sel_hi:[0,1,0] neg_lo:[1,0,0] neg_hi:[1,0,0]
	v_pk_fma_f32 v[132:133], v[232:233], v[132:133], 0 op_sel_hi:[0,1,0] neg_lo:[1,0,0] neg_hi:[1,0,0]
	v_cvt_pk_bf16_f32 v130, v130, v131
	v_cvt_pk_bf16_f32 v131, v132, v133
	ds_write_b64 v186, v[130:131]
	s_waitcnt vmcnt(6)
	v_pk_fma_f32 v[132:133], v[234:235], v[138:139], 0 op_sel_hi:[0,1,0] neg_lo:[1,0,0] neg_hi:[1,0,0]
	v_pk_fma_f32 v[130:131], v[234:235], v[140:141], 0 op_sel_hi:[0,1,0] neg_lo:[1,0,0] neg_hi:[1,0,0]
	v_cvt_pk_bf16_f32 v132, v132, v133
	v_cvt_pk_bf16_f32 v133, v130, v131
	ds_write_b64 v186, v[132:133] offset:544
	s_waitcnt vmcnt(5)
	v_pk_fma_f32 v[132:133], v[236:237], v[142:143], 0 op_sel_hi:[0,1,0] neg_lo:[1,0,0] neg_hi:[1,0,0]
	v_pk_fma_f32 v[130:131], v[236:237], v[144:145], 0 op_sel_hi:[0,1,0] neg_lo:[1,0,0] neg_hi:[1,0,0]
	v_cvt_pk_bf16_f32 v132, v132, v133
	v_cvt_pk_bf16_f32 v133, v130, v131
	ds_write_b64 v186, v[132:133] offset:1088
	s_waitcnt vmcnt(4)
	v_pk_fma_f32 v[132:133], v[238:239], v[146:147], 0 op_sel_hi:[0,1,0] neg_lo:[1,0,0] neg_hi:[1,0,0]
	v_pk_fma_f32 v[130:131], v[238:239], v[148:149], 0 op_sel_hi:[0,1,0] neg_lo:[1,0,0] neg_hi:[1,0,0]
	v_cvt_pk_bf16_f32 v132, v132, v133
	v_cvt_pk_bf16_f32 v133, v130, v131
	ds_write_b64 v186, v[132:133] offset:1632
	s_waitcnt vmcnt(3)
	v_pk_fma_f32 v[132:133], v[240:241], v[168:169], 0 op_sel_hi:[0,1,0] neg_lo:[1,0,0] neg_hi:[1,0,0]
	v_pk_fma_f32 v[130:131], v[240:241], v[170:171], 0 op_sel_hi:[0,1,0] neg_lo:[1,0,0] neg_hi:[1,0,0]
	v_cvt_pk_bf16_f32 v132, v132, v133
	v_cvt_pk_bf16_f32 v133, v130, v131
	ds_write_b64 v186, v[132:133] offset:2176
	s_waitcnt vmcnt(2)
	v_pk_fma_f32 v[132:133], v[242:243], v[172:173], 0 op_sel_hi:[0,1,0] neg_lo:[1,0,0] neg_hi:[1,0,0]
	v_pk_fma_f32 v[130:131], v[242:243], v[174:175], 0 op_sel_hi:[0,1,0] neg_lo:[1,0,0] neg_hi:[1,0,0]
	v_cvt_pk_bf16_f32 v132, v132, v133
	v_cvt_pk_bf16_f32 v133, v130, v131
	ds_write_b64 v186, v[132:133] offset:2720
	s_waitcnt vmcnt(1)
	v_pk_fma_f32 v[132:133], v[244:245], v[176:177], 0 op_sel_hi:[0,1,0] neg_lo:[1,0,0] neg_hi:[1,0,0]
	v_pk_fma_f32 v[130:131], v[244:245], v[178:179], 0 op_sel_hi:[0,1,0] neg_lo:[1,0,0] neg_hi:[1,0,0]
	v_cvt_pk_bf16_f32 v132, v132, v133
	v_cvt_pk_bf16_f32 v133, v130, v131
	ds_write_b64 v186, v[132:133] offset:3264
	s_waitcnt vmcnt(0)
	v_pk_fma_f32 v[132:133], v[246:247], v[180:181], 0 op_sel_hi:[0,1,0] neg_lo:[1,0,0] neg_hi:[1,0,0]
	v_pk_fma_f32 v[130:131], v[246:247], v[182:183], 0 op_sel_hi:[0,1,0] neg_lo:[1,0,0] neg_hi:[1,0,0]
	v_cvt_pk_bf16_f32 v132, v132, v133
	v_cvt_pk_bf16_f32 v133, v130, v131
	ds_write_b64 v186, v[132:133] offset:3808
	ds_read_b128 v[130:133], v1
	ds_read_b128 v[134:137], v1 offset:64
	ds_read_b128 v[138:141], v1 offset:128
	ds_read_b128 v[142:145], v1 offset:192
	s_ashr_i32 s7, s6, 31
	s_lshl_b64 s[0:1], s[6:7], 2
	s_add_u32 s0, s4, s0
	s_addc_u32 s1, s5, s1
	v_lshlrev_b32_e32 v1, 4, v0
	s_add_i32 s20, s34, 1
	s_add_i32 s34, s34, -1
	v_or_b32_e32 v153, s10, v206
	s_xor_b32 s26, s3, 2
	s_lshl_b64 s[10:11], s[10:11], 3
	s_and_b32 s20, s20, 3
	s_and_b32 s27, s34, 3
	s_add_u32 s10, s14, s10
	s_addc_u32 s11, s15, s11
	s_lshl_b32 s42, s35, 2
	s_add_i32 s41, s42, 0x26a20
	s_add_i32 s42, s42, 0x26a00
	v_lshlrev_b32_e32 v190, 3, v206
	s_cmp_eq_u32 s35, 3
	v_lshlrev_b32_e32 v150, 3, v0
	v_and_b32_e32 v151, 1, v0
	v_lshl_add_u64 v[0:1], v[154:155], 3, s[14:15]
	v_lshl_add_u64 v[192:193], s[10:11], 0, v[190:191]
	s_cselect_b64 s[10:11], -1, 0
	s_lshl_b32 s14, s3, 2
	s_add_u32 s24, s16, s14
	v_or_b32_e32 v155, 0x20000, v150
	v_add_u32_e32 v156, 0x20880, v150
	v_lshlrev_b32_e32 v150, 1, v153
	s_addc_u32 s25, s17, 0
	s_lshl_b32 s43, s3, 9
	v_lshl_add_u32 v212, s26, 9, v150
	s_lshl_b32 s15, s26, 8
	s_add_i32 s26, s43, 0x200
	v_mov_b32_e32 v152, 0x880
	v_cmp_lt_u32_e64 s[0:1], 15, v206
	v_cmp_eq_u32_e32 vcc, 1, v151
	s_and_b32 s45, s26, 0x600
	s_add_i32 s26, s43, 0x500
	v_cndmask_b32_e32 v211, 0, v152, vcc
	s_and_b32 s56, s26, 0x700
	s_add_i32 s26, s43, 0x540
	v_lshl_add_u32 v213, s20, 9, v150
	v_lshl_add_u32 v214, s27, 9, v150
	s_and_b32 s57, s26, 0x740
	s_add_i32 s26, s43, 0x580
	s_and_b32 s58, s26, 0x780
	s_add_i32 s26, s43, 0x5c0
	s_and_b32 s59, s26, 0x7c0
	s_add_i32 s26, s43, 0x600
	s_and_b32 s60, s26, 0x600
	s_add_i32 s26, s43, 0x640
	s_and_b32 s61, s26, 0x640
	s_add_i32 s26, s43, 0x680
	s_and_b32 s62, s26, 0x680
	s_add_i32 s26, s43, 0x6c0
	s_and_b32 s63, s26, 0x6c0
	s_add_i32 s26, s43, 0x700
	s_and_b32 s64, s26, 0x700
	s_add_i32 s26, s43, 0x740
	s_and_b32 s65, s26, 0x740
	s_add_i32 s26, s43, 0x780
	s_lshl_b32 s14, s27, 8
	s_lshl_b32 s20, s20, 8
	s_add_i32 s27, s43, 0x240
	s_add_i32 s28, s43, 0x280
	s_add_i32 s29, s43, 0x2c0
	s_add_i32 s30, s43, 0x300
	s_add_i32 s31, s43, 0x340
	s_add_i32 s34, s43, 0x380
	s_add_i32 s35, s43, 0x3c0
	s_add_i32 s36, s43, 0x440
	s_add_i32 s37, s43, 0x480
	s_add_i32 s38, s43, 0x4c0
	s_and_b32 s66, s26, 0x780
	s_add_i32 s26, s43, 0x7c0
	s_mul_hi_i32 s23, s18, 0x65
	s_mul_i32 s22, s18, 0x65
	v_cmp_eq_u32_e64 s[4:5], 1, v185
	v_cmp_eq_u32_e64 s[6:7], 2, v185
	v_cmp_eq_u32_e64 s[8:9], 63, v206
	s_xor_b32 s44, s43, 0x400
	s_and_b32 s46, s27, 0x640
	s_and_b32 s47, s28, 0x680
	s_waitcnt lgkmcnt(0)
	v_mov_b32_e32 v146, 0x20000
	s_and_b32 s48, s29, 0x6c0
	s_and_b32 s49, s30, 0x700
	s_and_b32 s50, s31, 0x740
	s_and_b32 s51, s34, 0x780
	s_and_b32 s52, s35, 0x7c0
	s_and_b32 s53, s36, 0x640
	s_and_b32 s54, s37, 0x680
	s_and_b32 s55, s38, 0x6c0
	s_and_b32 s67, s26, 0x7c0
	s_and_b64 s[26:27], s[10:11], s[12:13]
	v_lshl_add_u32 v215, v154, 1, v146
	v_mov_b32_e32 v216, 1
	s_lshl_b32 s28, s14, 3
	s_lshl_b32 s30, s15, 3
	s_lshl_b32 s34, s20, 3
	s_movk_i32 s68, 0x7fff
	s_mov_b32 s69, 0
	v_and_b32_e32 v220, 24, v206
	v_lshlrev_b32_e32 v220, 2, v220
	v_and_b32_e32 v221, 2, v206
	v_lshl_or_b32 v220, v221, 3, v220
	v_and_b32_e32 v221, 32, v206
	v_lshrrev_b32_e32 v221, 2, v221
	v_or_b32_e32 v220, v220, v221
	v_and_b32_e32 v221, 4, v206
	v_or_b32_e32 v220, v220, v221
	v_and_b32_e32 v221, 1, v206
	v_lshl_or_b32 v220, v221, 1, v220
	v_mov_b32_e32 v220, v254
	s_lshr_b32 s76, s19, 8
	s_add_i32 s76, s76, 0x20000
	v_add_u32_e32 v220, s76, v220
	v_add_u32_e32 v225, s45, v220
	v_add_u32_e32 v226, s44, v220
	v_add_u32_e32 v227, s60, v220
	v_add_u32_e32 v228, s43, v220
	v_and_b32_e32 v221, 1, v206
	v_mul_u32_u24_e32 v221, 0x880, v221
	v_lshrrev_b32_e32 v220, 4, v206
	v_lshl_add_u32 v221, v220, 5, v221
	v_and_b32_e32 v220, 2, v206
	v_lshl_add_u32 v221, v220, 3, v221
	v_add_u32_e32 v222, 0x20000, v221
	v_cmp_ne_u32_e32 vcc, 0, v220
	v_mov_b32_e32 v220, 0x44444444
	v_mov_b32_e32 v221, 0xeeeeeeee
	s_nop 1
	v_cndmask_b32_e32 v223, v220, v221, vcc
	v_cmp_lt_u32_e64 s[74:75], 47, v206
	s_lshr_b32 s82, s19, 15
	s_mul_i32 s83, s82, 0x1100
	s_add_i32 s83, s83, 0x22200
	v_lshl_add_u32 v254, v206, 2, s83
	v_mov_b32_e32 v220, s41
	s_nop 1
	v_cndmask_b32_e64 v254, v254, v220, s[12:13]
	v_mov_b32_e32 v224, v184
	s_mov_b32 s86, 0x55555555
	s_mov_b32 s87, 0x55555555
	s_lshr_b32 s78, s19, 15
	s_lshl_b32 s79, s78, 11
	v_add_u32_e32 v255, s79, v224
	ds_read_b128 v[166:169], v224 offset:0
	ds_read_b128 v[170:173], v224 offset:1024
	ds_read_b128 v[174:177], v224 offset:2048
	ds_read_b128 v[178:181], v224 offset:3072
	ds_read_b128 v[182:185], v224 offset:4096
	ds_read_b128 v[186:189], v224 offset:5120
	s_mov_b32 s20, 0
